# adds: conv 992 scalar fmac per half as 496 v_pk_fma_f32; V-phase output block uses v_cvt_pk_bf16_f32 + paired stores (same values)
# speedup vs baseline: 1.0016x; 1.0016x over previous
; __device__ __forceinline__ void conv_phase(LAS unsigned char* lds, int tile, int tid, const bf16* __restrict__ U, const float* __restrict__ cw, const float* __restrict__ cb, ...
;     ...
;         __syncthreads();
;         {
;             float uc[UROWS];
; #pragma unroll
;             for (int r = 0; r < UROWS; ++r) uc[r] = __uint_as_float((unsigned)ubuf[r * CH + tid] << 16);
.LBB0_373:
	s_or_b64 exec, exec, s[10:11]
	s_waitcnt lgkmcnt(0)
	s_barrier
	ds_read_u16 v196, v65
	ds_read_u16 v197, v65 offset:1024
	ds_read_u16 v198, v65 offset:2048
	ds_read_u16 v199, v65 offset:3072
	ds_read_u16 v200, v65 offset:4096
	ds_read_u16 v201, v65 offset:5120
	ds_read_u16 v202, v65 offset:6144
	ds_read_u16 v203, v65 offset:7168
	ds_read_u16 v204, v65 offset:8192
	ds_read_u16 v205, v65 offset:9216
	ds_read_u16 v206, v65 offset:10240
	ds_read_u16 v207, v65 offset:11264
	ds_read_u16 v208, v65 offset:12288
	ds_read_u16 v209, v65 offset:13312
	ds_read_u16 v210, v65 offset:14336
	ds_read_u16 v211, v65 offset:15360
	ds_read_u16 v212, v65 offset:16384
	ds_read_u16 v213, v65 offset:17408
	ds_read_u16 v214, v65 offset:18432
	ds_read_u16 v215, v65 offset:19456
	ds_read_u16 v216, v65 offset:20480
	ds_read_u16 v217, v65 offset:21504
	ds_read_u16 v218, v65 offset:22528
	ds_read_u16 v219, v65 offset:23552
	ds_read_u16 v220, v65 offset:24576
	ds_read_u16 v221, v65 offset:25600
	ds_read_u16 v222, v65 offset:26624
	ds_read_u16 v223, v65 offset:27648
	ds_read_u16 v224, v65 offset:28672
	ds_read_u16 v225, v65 offset:29696
	ds_read_u16 v226, v65 offset:30720
	ds_read_u16 v227, v65 offset:31744
	ds_read_u16 v228, v65 offset:32768
	ds_read_u16 v229, v65 offset:33792
	ds_read_u16 v230, v65 offset:34816
	ds_read_u16 v231, v65 offset:35840
	ds_read_u16 v232, v65 offset:36864
	ds_read_u16 v233, v65 offset:37888
	ds_read_u16 v234, v65 offset:38912
	ds_read_u16 v235, v65 offset:39936
	ds_read_u16 v236, v65 offset:40960
	ds_read_u16 v237, v65 offset:41984
	ds_read_u16 v238, v65 offset:43008
	ds_read_u16 v239, v65 offset:44032
	ds_read_u16 v240, v65 offset:45056
	ds_read_u16 v241, v65 offset:46080
	ds_read_u16 v242, v65 offset:47104
	ds_read_u16 v243, v65 offset:48128
	ds_read_u16 v244, v65 offset:49152
	ds_read_u16 v245, v65 offset:50176
	ds_read_u16 v246, v65 offset:51200
	ds_read_u16 v247, v65 offset:52224
	s_waitcnt lgkmcnt(0)
	v_lshlrev_b32_e32 v72, 16, v196
	v_lshlrev_b32_e32 v73, 16, v197
	v_lshlrev_b32_e32 v134, 16, v197
	v_lshlrev_b32_e32 v74, 16, v198
	v_lshlrev_b32_e32 v135, 16, v198
	v_lshlrev_b32_e32 v75, 16, v199
	v_lshlrev_b32_e32 v136, 16, v199
	v_lshlrev_b32_e32 v76, 16, v200
	v_lshlrev_b32_e32 v137, 16, v200
	v_lshlrev_b32_e32 v77, 16, v201
	v_lshlrev_b32_e32 v138, 16, v201
	v_lshlrev_b32_e32 v78, 16, v202
	v_lshlrev_b32_e32 v139, 16, v202
	v_lshlrev_b32_e32 v79, 16, v203
	v_lshlrev_b32_e32 v140, 16, v203
	v_lshlrev_b32_e32 v80, 16, v204
	v_lshlrev_b32_e32 v141, 16, v204
	v_lshlrev_b32_e32 v81, 16, v205
	v_lshlrev_b32_e32 v142, 16, v205
	v_lshlrev_b32_e32 v82, 16, v206
	v_lshlrev_b32_e32 v143, 16, v206
	v_lshlrev_b32_e32 v83, 16, v207
	v_lshlrev_b32_e32 v144, 16, v207
	v_lshlrev_b32_e32 v84, 16, v208
	v_lshlrev_b32_e32 v145, 16, v208
	v_lshlrev_b32_e32 v85, 16, v209
	v_lshlrev_b32_e32 v146, 16, v209
	v_lshlrev_b32_e32 v86, 16, v210
	v_lshlrev_b32_e32 v147, 16, v210
	v_lshlrev_b32_e32 v87, 16, v211
	v_lshlrev_b32_e32 v148, 16, v211
	v_lshlrev_b32_e32 v88, 16, v212
	v_lshlrev_b32_e32 v149, 16, v212
	v_lshlrev_b32_e32 v89, 16, v213
	v_lshlrev_b32_e32 v150, 16, v213
	v_lshlrev_b32_e32 v90, 16, v214
	v_lshlrev_b32_e32 v151, 16, v214
	v_lshlrev_b32_e32 v91, 16, v215
	v_lshlrev_b32_e32 v152, 16, v215
	v_lshlrev_b32_e32 v92, 16, v216
	v_lshlrev_b32_e32 v153, 16, v216
	v_lshlrev_b32_e32 v93, 16, v217
	v_lshlrev_b32_e32 v154, 16, v217
	v_lshlrev_b32_e32 v94, 16, v218
	v_lshlrev_b32_e32 v155, 16, v218
	v_lshlrev_b32_e32 v95, 16, v219
	v_lshlrev_b32_e32 v156, 16, v219
	v_lshlrev_b32_e32 v96, 16, v220
	v_lshlrev_b32_e32 v157, 16, v220
	v_lshlrev_b32_e32 v97, 16, v221
	v_lshlrev_b32_e32 v158, 16, v221
	v_lshlrev_b32_e32 v98, 16, v222
	v_lshlrev_b32_e32 v159, 16, v222
	v_lshlrev_b32_e32 v99, 16, v223
	v_lshlrev_b32_e32 v160, 16, v223
	v_lshlrev_b32_e32 v100, 16, v224
	v_lshlrev_b32_e32 v161, 16, v224
	v_lshlrev_b32_e32 v101, 16, v225
	v_lshlrev_b32_e32 v162, 16, v225
	v_lshlrev_b32_e32 v102, 16, v226
	v_lshlrev_b32_e32 v163, 16, v226
	v_lshlrev_b32_e32 v103, 16, v227
	v_lshlrev_b32_e32 v164, 16, v227
	v_lshlrev_b32_e32 v104, 16, v228
	v_lshlrev_b32_e32 v165, 16, v228
	v_lshlrev_b32_e32 v105, 16, v229
	v_lshlrev_b32_e32 v166, 16, v229
	v_lshlrev_b32_e32 v106, 16, v230
	v_lshlrev_b32_e32 v167, 16, v230
	v_lshlrev_b32_e32 v107, 16, v231
	v_lshlrev_b32_e32 v168, 16, v231
	v_lshlrev_b32_e32 v108, 16, v232
	v_lshlrev_b32_e32 v169, 16, v232
	v_lshlrev_b32_e32 v109, 16, v233
	v_lshlrev_b32_e32 v170, 16, v233
	v_lshlrev_b32_e32 v110, 16, v234
	v_lshlrev_b32_e32 v171, 16, v234
	v_lshlrev_b32_e32 v111, 16, v235
	v_lshlrev_b32_e32 v172, 16, v235
	v_lshlrev_b32_e32 v112, 16, v236
	v_lshlrev_b32_e32 v173, 16, v236
	v_lshlrev_b32_e32 v113, 16, v237
	v_lshlrev_b32_e32 v174, 16, v237
	v_lshlrev_b32_e32 v114, 16, v238
	v_lshlrev_b32_e32 v175, 16, v238
	v_lshlrev_b32_e32 v115, 16, v239
	v_lshlrev_b32_e32 v176, 16, v239
	v_lshlrev_b32_e32 v116, 16, v240
	v_lshlrev_b32_e32 v177, 16, v240
	v_lshlrev_b32_e32 v117, 16, v241
	v_lshlrev_b32_e32 v178, 16, v241
	v_lshlrev_b32_e32 v118, 16, v242
	v_lshlrev_b32_e32 v179, 16, v242
	v_lshlrev_b32_e32 v119, 16, v243
	v_lshlrev_b32_e32 v180, 16, v243
	v_lshlrev_b32_e32 v120, 16, v244
	v_lshlrev_b32_e32 v181, 16, v244
	v_lshlrev_b32_e32 v121, 16, v245
	v_lshlrev_b32_e32 v182, 16, v245
	v_lshlrev_b32_e32 v122, 16, v246
	v_lshlrev_b32_e32 v183, 16, v246
	v_lshlrev_b32_e32 v123, 16, v247
	v_lshlrev_b32_e32 v184, 16, v247
	ds_read_u16 v196, v65 offset:53248
	ds_read_u16 v197, v65 offset:54272
	ds_read_u16 v198, v65 offset:55296
	ds_read_u16 v199, v65 offset:56320
	ds_read_u16 v200, v65 offset:57344
	ds_read_u16 v201, v65 offset:58368
	ds_read_u16 v202, v65 offset:59392
	ds_read_u16 v203, v65 offset:60416
	ds_read_u16 v204, v65 offset:61440
	ds_read_u16 v205, v65 offset:62464
	s_waitcnt lgkmcnt(0)
; __device__ __forceinline__ void conv_phase(LAS unsigned char* lds, int tile, int tid, const bf16* __restrict__ U, const float* __restrict__ cw, const float* __restrict__ cb, ...
;     ...
;             for (int r = 0; r < UROWS; ++r) uc[r] = __uint_as_float((unsigned)ubuf[r * CH + tid] << 16);
; #pragma unroll
;             for (int tk = 0; tk < HT; ++tk) { float a = bias;
; #pragma unroll
;                 for (int j = 0; j < CKW; ++j) a += w[j] * uc[tk + j];
	v_lshlrev_b32_e32 v124, 16, v196
	v_lshlrev_b32_e32 v185, 16, v196
	v_lshlrev_b32_e32 v125, 16, v197
	v_lshlrev_b32_e32 v186, 16, v197
	v_lshlrev_b32_e32 v126, 16, v198
	v_lshlrev_b32_e32 v187, 16, v198
	v_lshlrev_b32_e32 v127, 16, v199
	v_lshlrev_b32_e32 v188, 16, v199
	v_lshlrev_b32_e32 v128, 16, v200
	v_lshlrev_b32_e32 v189, 16, v200
	v_lshlrev_b32_e32 v129, 16, v201
	v_lshlrev_b32_e32 v190, 16, v201
	v_lshlrev_b32_e32 v130, 16, v202
	v_lshlrev_b32_e32 v191, 16, v202
	v_lshlrev_b32_e32 v131, 16, v203
	v_lshlrev_b32_e32 v192, 16, v203
	v_lshlrev_b32_e32 v132, 16, v204
	v_lshlrev_b32_e32 v193, 16, v204
	v_lshlrev_b32_e32 v133, 16, v205
	s_waitcnt vmcnt(0)
	v_pk_fma_f32 v[198:199], v[72:73], v[42:43], v[58:59] op_sel:[0,1,0] op_sel_hi:[1,1,0]
	v_pk_fma_f32 v[200:201], v[74:75], v[42:43], v[58:59] op_sel:[0,1,0] op_sel_hi:[1,1,0]
	v_pk_fma_f32 v[202:203], v[76:77], v[42:43], v[58:59] op_sel:[0,1,0] op_sel_hi:[1,1,0]
	v_pk_fma_f32 v[204:205], v[78:79], v[42:43], v[58:59] op_sel:[0,1,0] op_sel_hi:[1,1,0]
	v_pk_fma_f32 v[198:199], v[134:135], v[44:45], v[198:199] op_sel:[0,0,0] op_sel_hi:[1,0,1]
	v_pk_fma_f32 v[200:201], v[136:137], v[44:45], v[200:201] op_sel:[0,0,0] op_sel_hi:[1,0,1]
	v_pk_fma_f32 v[202:203], v[138:139], v[44:45], v[202:203] op_sel:[0,0,0] op_sel_hi:[1,0,1]
	v_pk_fma_f32 v[204:205], v[140:141], v[44:45], v[204:205] op_sel:[0,0,0] op_sel_hi:[1,0,1]
	v_pk_fma_f32 v[198:199], v[74:75], v[18:19], v[198:199] op_sel:[0,1,0] op_sel_hi:[1,1,1]
	v_pk_fma_f32 v[200:201], v[76:77], v[18:19], v[200:201] op_sel:[0,1,0] op_sel_hi:[1,1,1]
	v_pk_fma_f32 v[202:203], v[78:79], v[18:19], v[202:203] op_sel:[0,1,0] op_sel_hi:[1,1,1]
	v_pk_fma_f32 v[204:205], v[80:81], v[18:19], v[204:205] op_sel:[0,1,0] op_sel_hi:[1,1,1]
	v_pk_fma_f32 v[198:199], v[136:137], v[44:45], v[198:199] op_sel:[0,1,0] op_sel_hi:[1,1,1]
	v_pk_fma_f32 v[200:201], v[138:139], v[44:45], v[200:201] op_sel:[0,1,0] op_sel_hi:[1,1,1]
	v_pk_fma_f32 v[202:203], v[140:141], v[44:45], v[202:203] op_sel:[0,1,0] op_sel_hi:[1,1,1]
	v_pk_fma_f32 v[204:205], v[142:143], v[44:45], v[204:205] op_sel:[0,1,0] op_sel_hi:[1,1,1]
	v_pk_fma_f32 v[198:199], v[76:77], v[28:29], v[198:199] op_sel:[0,0,0] op_sel_hi:[1,0,1]
	v_pk_fma_f32 v[200:201], v[78:79], v[28:29], v[200:201] op_sel:[0,0,0] op_sel_hi:[1,0,1]
	v_pk_fma_f32 v[202:203], v[80:81], v[28:29], v[202:203] op_sel:[0,0,0] op_sel_hi:[1,0,1]
	v_pk_fma_f32 v[204:205], v[82:83], v[28:29], v[204:205] op_sel:[0,0,0] op_sel_hi:[1,0,1]
	v_pk_fma_f32 v[198:199], v[138:139], v[28:29], v[198:199] op_sel:[0,1,0] op_sel_hi:[1,1,1]
	v_pk_fma_f32 v[200:201], v[140:141], v[28:29], v[200:201] op_sel:[0,1,0] op_sel_hi:[1,1,1]
	v_pk_fma_f32 v[202:203], v[142:143], v[28:29], v[202:203] op_sel:[0,1,0] op_sel_hi:[1,1,1]
	v_pk_fma_f32 v[204:205], v[144:145], v[28:29], v[204:205] op_sel:[0,1,0] op_sel_hi:[1,1,1]
	v_pk_fma_f32 v[198:199], v[78:79], v[30:31], v[198:199] op_sel:[0,0,0] op_sel_hi:[1,0,1]
	v_pk_fma_f32 v[200:201], v[80:81], v[30:31], v[200:201] op_sel:[0,0,0] op_sel_hi:[1,0,1]
	v_pk_fma_f32 v[202:203], v[82:83], v[30:31], v[202:203] op_sel:[0,0,0] op_sel_hi:[1,0,1]
	v_pk_fma_f32 v[204:205], v[84:85], v[30:31], v[204:205] op_sel:[0,0,0] op_sel_hi:[1,0,1]
	v_pk_fma_f32 v[198:199], v[140:141], v[46:47], v[198:199] op_sel:[0,0,0] op_sel_hi:[1,0,1]
	v_pk_fma_f32 v[200:201], v[142:143], v[46:47], v[200:201] op_sel:[0,0,0] op_sel_hi:[1,0,1]
	v_pk_fma_f32 v[202:203], v[144:145], v[46:47], v[202:203] op_sel:[0,0,0] op_sel_hi:[1,0,1]
	v_pk_fma_f32 v[204:205], v[146:147], v[46:47], v[204:205] op_sel:[0,0,0] op_sel_hi:[1,0,1]
	v_pk_fma_f32 v[198:199], v[80:81], v[30:31], v[198:199] op_sel:[0,1,0] op_sel_hi:[1,1,1]
	v_pk_fma_f32 v[200:201], v[82:83], v[30:31], v[200:201] op_sel:[0,1,0] op_sel_hi:[1,1,1]
	v_pk_fma_f32 v[202:203], v[84:85], v[30:31], v[202:203] op_sel:[0,1,0] op_sel_hi:[1,1,1]
	v_pk_fma_f32 v[204:205], v[86:87], v[30:31], v[204:205] op_sel:[0,1,0] op_sel_hi:[1,1,1]
	v_pk_fma_f32 v[198:199], v[142:143], v[32:33], v[198:199] op_sel:[0,0,0] op_sel_hi:[1,0,1]
	v_pk_fma_f32 v[200:201], v[144:145], v[32:33], v[200:201] op_sel:[0,0,0] op_sel_hi:[1,0,1]
	v_pk_fma_f32 v[202:203], v[146:147], v[32:33], v[202:203] op_sel:[0,0,0] op_sel_hi:[1,0,1]
	v_pk_fma_f32 v[204:205], v[148:149], v[32:33], v[204:205] op_sel:[0,0,0] op_sel_hi:[1,0,1]
	v_pk_fma_f32 v[198:199], v[82:83], v[32:33], v[198:199] op_sel:[0,1,0] op_sel_hi:[1,1,1]
	v_pk_fma_f32 v[200:201], v[84:85], v[32:33], v[200:201] op_sel:[0,1,0] op_sel_hi:[1,1,1]
	v_pk_fma_f32 v[202:203], v[86:87], v[32:33], v[202:203] op_sel:[0,1,0] op_sel_hi:[1,1,1]
	v_pk_fma_f32 v[204:205], v[88:89], v[32:33], v[204:205] op_sel:[0,1,0] op_sel_hi:[1,1,1]
	v_pk_fma_f32 v[198:199], v[144:145], v[46:47], v[198:199] op_sel:[0,1,0] op_sel_hi:[1,1,1]
	v_pk_fma_f32 v[200:201], v[146:147], v[46:47], v[200:201] op_sel:[0,1,0] op_sel_hi:[1,1,1]
	v_pk_fma_f32 v[202:203], v[148:149], v[46:47], v[202:203] op_sel:[0,1,0] op_sel_hi:[1,1,1]
	v_pk_fma_f32 v[204:205], v[150:151], v[46:47], v[204:205] op_sel:[0,1,0] op_sel_hi:[1,1,1]
	v_pk_fma_f32 v[198:199], v[84:85], v[34:35], v[198:199] op_sel:[0,0,0] op_sel_hi:[1,0,1]
	v_pk_fma_f32 v[200:201], v[86:87], v[34:35], v[200:201] op_sel:[0,0,0] op_sel_hi:[1,0,1]
	v_pk_fma_f32 v[202:203], v[88:89], v[34:35], v[202:203] op_sel:[0,0,0] op_sel_hi:[1,0,1]
	v_pk_fma_f32 v[204:205], v[90:91], v[34:35], v[204:205] op_sel:[0,0,0] op_sel_hi:[1,0,1]
	v_pk_fma_f32 v[198:199], v[146:147], v[34:35], v[198:199] op_sel:[0,1,0] op_sel_hi:[1,1,1]
	v_pk_fma_f32 v[200:201], v[148:149], v[34:35], v[200:201] op_sel:[0,1,0] op_sel_hi:[1,1,1]
	v_pk_fma_f32 v[202:203], v[150:151], v[34:35], v[202:203] op_sel:[0,1,0] op_sel_hi:[1,1,1]
; __device__ __forceinline__ void conv_phase(LAS unsigned char* lds, int tile, int tid, const bf16* __restrict__ U, const float* __restrict__ cw, const float* __restrict__ cb, ...
;     ...
;             for (int tk = 0; tk < HT; ++tk) { float a = bias;
; #pragma unroll
;                 for (int j = 0; j < CKW; ++j) a += w[j] * uc[tk + j];
;                 obuf[tk * CH + tid] = a; }
	v_pk_fma_f32 v[204:205], v[152:153], v[34:35], v[204:205] op_sel:[0,1,0] op_sel_hi:[1,1,1]
	v_pk_fma_f32 v[198:199], v[86:87], v[36:37], v[198:199] op_sel:[0,0,0] op_sel_hi:[1,0,1]
	v_pk_fma_f32 v[200:201], v[88:89], v[36:37], v[200:201] op_sel:[0,0,0] op_sel_hi:[1,0,1]
	v_pk_fma_f32 v[202:203], v[90:91], v[36:37], v[202:203] op_sel:[0,0,0] op_sel_hi:[1,0,1]
	v_pk_fma_f32 v[204:205], v[92:93], v[36:37], v[204:205] op_sel:[0,0,0] op_sel_hi:[1,0,1]
	v_pk_fma_f32 v[198:199], v[148:149], v[48:49], v[198:199] op_sel:[0,0,0] op_sel_hi:[1,0,1]
	v_pk_fma_f32 v[200:201], v[150:151], v[48:49], v[200:201] op_sel:[0,0,0] op_sel_hi:[1,0,1]
	v_pk_fma_f32 v[202:203], v[152:153], v[48:49], v[202:203] op_sel:[0,0,0] op_sel_hi:[1,0,1]
	v_pk_fma_f32 v[204:205], v[154:155], v[48:49], v[204:205] op_sel:[0,0,0] op_sel_hi:[1,0,1]
	v_pk_fma_f32 v[198:199], v[88:89], v[36:37], v[198:199] op_sel:[0,1,0] op_sel_hi:[1,1,1]
	v_pk_fma_f32 v[200:201], v[90:91], v[36:37], v[200:201] op_sel:[0,1,0] op_sel_hi:[1,1,1]
	v_pk_fma_f32 v[202:203], v[92:93], v[36:37], v[202:203] op_sel:[0,1,0] op_sel_hi:[1,1,1]
	v_pk_fma_f32 v[204:205], v[94:95], v[36:37], v[204:205] op_sel:[0,1,0] op_sel_hi:[1,1,1]
	v_pk_fma_f32 v[198:199], v[150:151], v[38:39], v[198:199] op_sel:[0,0,0] op_sel_hi:[1,0,1]
	v_pk_fma_f32 v[200:201], v[152:153], v[38:39], v[200:201] op_sel:[0,0,0] op_sel_hi:[1,0,1]
	v_pk_fma_f32 v[202:203], v[154:155], v[38:39], v[202:203] op_sel:[0,0,0] op_sel_hi:[1,0,1]
	v_pk_fma_f32 v[204:205], v[156:157], v[38:39], v[204:205] op_sel:[0,0,0] op_sel_hi:[1,0,1]
	v_pk_fma_f32 v[198:199], v[90:91], v[38:39], v[198:199] op_sel:[0,1,0] op_sel_hi:[1,1,1]
	v_pk_fma_f32 v[200:201], v[92:93], v[38:39], v[200:201] op_sel:[0,1,0] op_sel_hi:[1,1,1]
	v_pk_fma_f32 v[202:203], v[94:95], v[38:39], v[202:203] op_sel:[0,1,0] op_sel_hi:[1,1,1]
	v_pk_fma_f32 v[204:205], v[96:97], v[38:39], v[204:205] op_sel:[0,1,0] op_sel_hi:[1,1,1]
	v_pk_fma_f32 v[198:199], v[152:153], v[48:49], v[198:199] op_sel:[0,1,0] op_sel_hi:[1,1,1]
	v_pk_fma_f32 v[200:201], v[154:155], v[48:49], v[200:201] op_sel:[0,1,0] op_sel_hi:[1,1,1]
	v_pk_fma_f32 v[202:203], v[156:157], v[48:49], v[202:203] op_sel:[0,1,0] op_sel_hi:[1,1,1]
	v_pk_fma_f32 v[204:205], v[158:159], v[48:49], v[204:205] op_sel:[0,1,0] op_sel_hi:[1,1,1]
	v_pk_fma_f32 v[198:199], v[92:93], v[40:41], v[198:199] op_sel:[0,0,0] op_sel_hi:[1,0,1]
	v_pk_fma_f32 v[200:201], v[94:95], v[40:41], v[200:201] op_sel:[0,0,0] op_sel_hi:[1,0,1]
	v_pk_fma_f32 v[202:203], v[96:97], v[40:41], v[202:203] op_sel:[0,0,0] op_sel_hi:[1,0,1]
	v_pk_fma_f32 v[204:205], v[98:99], v[40:41], v[204:205] op_sel:[0,0,0] op_sel_hi:[1,0,1]
	v_pk_fma_f32 v[198:199], v[154:155], v[40:41], v[198:199] op_sel:[0,1,0] op_sel_hi:[1,1,1]
	v_pk_fma_f32 v[200:201], v[156:157], v[40:41], v[200:201] op_sel:[0,1,0] op_sel_hi:[1,1,1]
	v_pk_fma_f32 v[202:203], v[158:159], v[40:41], v[202:203] op_sel:[0,1,0] op_sel_hi:[1,1,1]
	v_pk_fma_f32 v[204:205], v[160:161], v[40:41], v[204:205] op_sel:[0,1,0] op_sel_hi:[1,1,1]
	v_pk_fma_f32 v[198:199], v[94:95], v[42:43], v[198:199] op_sel:[0,0,0] op_sel_hi:[1,0,1]
	v_pk_fma_f32 v[200:201], v[96:97], v[42:43], v[200:201] op_sel:[0,0,0] op_sel_hi:[1,0,1]
	v_pk_fma_f32 v[202:203], v[98:99], v[42:43], v[202:203] op_sel:[0,0,0] op_sel_hi:[1,0,1]
	v_pk_fma_f32 v[204:205], v[100:101], v[42:43], v[204:205] op_sel:[0,0,0] op_sel_hi:[1,0,1]
	v_pk_fma_f32 v[198:199], v[156:157], v[50:51], v[198:199] op_sel:[0,0,0] op_sel_hi:[1,0,1]
	v_pk_fma_f32 v[200:201], v[158:159], v[50:51], v[200:201] op_sel:[0,0,0] op_sel_hi:[1,0,1]
	v_pk_fma_f32 v[202:203], v[160:161], v[50:51], v[202:203] op_sel:[0,0,0] op_sel_hi:[1,0,1]
	v_pk_fma_f32 v[204:205], v[162:163], v[50:51], v[204:205] op_sel:[0,0,0] op_sel_hi:[1,0,1]
	v_pk_fma_f32 v[198:199], v[96:97], v[50:51], v[198:199] op_sel:[0,1,0] op_sel_hi:[1,1,1]
	v_pk_fma_f32 v[200:201], v[98:99], v[50:51], v[200:201] op_sel:[0,1,0] op_sel_hi:[1,1,1]
	v_pk_fma_f32 v[202:203], v[100:101], v[50:51], v[202:203] op_sel:[0,1,0] op_sel_hi:[1,1,1]
	v_pk_fma_f32 v[204:205], v[102:103], v[50:51], v[204:205] op_sel:[0,1,0] op_sel_hi:[1,1,1]
	v_pk_fma_f32 v[198:199], v[158:159], v[52:53], v[198:199] op_sel:[0,0,0] op_sel_hi:[1,0,1]
	v_pk_fma_f32 v[200:201], v[160:161], v[52:53], v[200:201] op_sel:[0,0,0] op_sel_hi:[1,0,1]
	v_pk_fma_f32 v[202:203], v[162:163], v[52:53], v[202:203] op_sel:[0,0,0] op_sel_hi:[1,0,1]
	v_pk_fma_f32 v[204:205], v[164:165], v[52:53], v[204:205] op_sel:[0,0,0] op_sel_hi:[1,0,1]
	v_pk_fma_f32 v[198:199], v[98:99], v[52:53], v[198:199] op_sel:[0,1,0] op_sel_hi:[1,1,1]
	v_pk_fma_f32 v[200:201], v[100:101], v[52:53], v[200:201] op_sel:[0,1,0] op_sel_hi:[1,1,1]
	v_pk_fma_f32 v[202:203], v[102:103], v[52:53], v[202:203] op_sel:[0,1,0] op_sel_hi:[1,1,1]
	v_pk_fma_f32 v[204:205], v[104:105], v[52:53], v[204:205] op_sel:[0,1,0] op_sel_hi:[1,1,1]
	v_pk_fma_f32 v[198:199], v[160:161], v[56:57], v[198:199] op_sel:[0,0,0] op_sel_hi:[1,0,1]
	v_pk_fma_f32 v[200:201], v[162:163], v[56:57], v[200:201] op_sel:[0,0,0] op_sel_hi:[1,0,1]
	v_pk_fma_f32 v[202:203], v[164:165], v[56:57], v[202:203] op_sel:[0,0,0] op_sel_hi:[1,0,1]
	v_pk_fma_f32 v[204:205], v[166:167], v[56:57], v[204:205] op_sel:[0,0,0] op_sel_hi:[1,0,1]
	v_pk_fma_f32 v[198:199], v[100:101], v[54:55], v[198:199] op_sel:[0,0,0] op_sel_hi:[1,0,1]
	v_pk_fma_f32 v[200:201], v[102:103], v[54:55], v[200:201] op_sel:[0,0,0] op_sel_hi:[1,0,1]
	v_pk_fma_f32 v[202:203], v[104:105], v[54:55], v[202:203] op_sel:[0,0,0] op_sel_hi:[1,0,1]
	v_pk_fma_f32 v[204:205], v[106:107], v[54:55], v[204:205] op_sel:[0,0,0] op_sel_hi:[1,0,1]
	v_pk_fma_f32 v[198:199], v[162:163], v[54:55], v[198:199] op_sel:[0,1,0] op_sel_hi:[1,1,1]
; __device__ __forceinline__ void conv_phase(LAS unsigned char* lds, int tile, int tid, const bf16* __restrict__ U, const float* __restrict__ cw, const float* __restrict__ cb, ...
;     ...
;             for (int tk = 0; tk < HT; ++tk) { float a = bias;
; #pragma unroll
;                 for (int j = 0; j < CKW; ++j) a += w[j] * uc[tk + j];
;                 obuf[tk * CH + tid] = a; }
	v_pk_fma_f32 v[200:201], v[164:165], v[54:55], v[200:201] op_sel:[0,1,0] op_sel_hi:[1,1,1]
	v_pk_fma_f32 v[202:203], v[166:167], v[54:55], v[202:203] op_sel:[0,1,0] op_sel_hi:[1,1,1]
	v_pk_fma_f32 v[204:205], v[168:169], v[54:55], v[204:205] op_sel:[0,1,0] op_sel_hi:[1,1,1]
	v_pk_fma_f32 v[198:199], v[102:103], v[56:57], v[198:199] op_sel:[0,1,0] op_sel_hi:[1,1,1]
	v_pk_fma_f32 v[200:201], v[104:105], v[56:57], v[200:201] op_sel:[0,1,0] op_sel_hi:[1,1,1]
	v_pk_fma_f32 v[202:203], v[106:107], v[56:57], v[202:203] op_sel:[0,1,0] op_sel_hi:[1,1,1]
	v_pk_fma_f32 v[204:205], v[108:109], v[56:57], v[204:205] op_sel:[0,1,0] op_sel_hi:[1,1,1]
	ds_write2st64_b32 v66, v198, v199 offset0:0 offset1:8
	ds_write2st64_b32 v66, v200, v201 offset0:16 offset1:24
	ds_write2st64_b32 v66, v202, v203 offset0:32 offset1:40
	ds_write2st64_b32 v66, v204, v205 offset0:48 offset1:56
	v_pk_fma_f32 v[198:199], v[80:81], v[42:43], v[58:59] op_sel:[0,1,0] op_sel_hi:[1,1,0]
	v_pk_fma_f32 v[200:201], v[82:83], v[42:43], v[58:59] op_sel:[0,1,0] op_sel_hi:[1,1,0]
	v_pk_fma_f32 v[202:203], v[84:85], v[42:43], v[58:59] op_sel:[0,1,0] op_sel_hi:[1,1,0]
	v_pk_fma_f32 v[204:205], v[86:87], v[42:43], v[58:59] op_sel:[0,1,0] op_sel_hi:[1,1,0]
	v_pk_fma_f32 v[198:199], v[142:143], v[44:45], v[198:199] op_sel:[0,0,0] op_sel_hi:[1,0,1]
	v_pk_fma_f32 v[200:201], v[144:145], v[44:45], v[200:201] op_sel:[0,0,0] op_sel_hi:[1,0,1]
	v_pk_fma_f32 v[202:203], v[146:147], v[44:45], v[202:203] op_sel:[0,0,0] op_sel_hi:[1,0,1]
	v_pk_fma_f32 v[204:205], v[148:149], v[44:45], v[204:205] op_sel:[0,0,0] op_sel_hi:[1,0,1]
	v_pk_fma_f32 v[198:199], v[82:83], v[18:19], v[198:199] op_sel:[0,1,0] op_sel_hi:[1,1,1]
	v_pk_fma_f32 v[200:201], v[84:85], v[18:19], v[200:201] op_sel:[0,1,0] op_sel_hi:[1,1,1]
	v_pk_fma_f32 v[202:203], v[86:87], v[18:19], v[202:203] op_sel:[0,1,0] op_sel_hi:[1,1,1]
	v_pk_fma_f32 v[204:205], v[88:89], v[18:19], v[204:205] op_sel:[0,1,0] op_sel_hi:[1,1,1]
	v_pk_fma_f32 v[198:199], v[144:145], v[44:45], v[198:199] op_sel:[0,1,0] op_sel_hi:[1,1,1]
	v_pk_fma_f32 v[200:201], v[146:147], v[44:45], v[200:201] op_sel:[0,1,0] op_sel_hi:[1,1,1]
	v_pk_fma_f32 v[202:203], v[148:149], v[44:45], v[202:203] op_sel:[0,1,0] op_sel_hi:[1,1,1]
	v_pk_fma_f32 v[204:205], v[150:151], v[44:45], v[204:205] op_sel:[0,1,0] op_sel_hi:[1,1,1]
	v_pk_fma_f32 v[198:199], v[84:85], v[28:29], v[198:199] op_sel:[0,0,0] op_sel_hi:[1,0,1]
	v_pk_fma_f32 v[200:201], v[86:87], v[28:29], v[200:201] op_sel:[0,0,0] op_sel_hi:[1,0,1]
	v_pk_fma_f32 v[202:203], v[88:89], v[28:29], v[202:203] op_sel:[0,0,0] op_sel_hi:[1,0,1]
	v_pk_fma_f32 v[204:205], v[90:91], v[28:29], v[204:205] op_sel:[0,0,0] op_sel_hi:[1,0,1]
	v_pk_fma_f32 v[198:199], v[146:147], v[28:29], v[198:199] op_sel:[0,1,0] op_sel_hi:[1,1,1]
	v_pk_fma_f32 v[200:201], v[148:149], v[28:29], v[200:201] op_sel:[0,1,0] op_sel_hi:[1,1,1]
	v_pk_fma_f32 v[202:203], v[150:151], v[28:29], v[202:203] op_sel:[0,1,0] op_sel_hi:[1,1,1]
	v_pk_fma_f32 v[204:205], v[152:153], v[28:29], v[204:205] op_sel:[0,1,0] op_sel_hi:[1,1,1]
	v_pk_fma_f32 v[198:199], v[86:87], v[30:31], v[198:199] op_sel:[0,0,0] op_sel_hi:[1,0,1]
	v_pk_fma_f32 v[200:201], v[88:89], v[30:31], v[200:201] op_sel:[0,0,0] op_sel_hi:[1,0,1]
	v_pk_fma_f32 v[202:203], v[90:91], v[30:31], v[202:203] op_sel:[0,0,0] op_sel_hi:[1,0,1]
	v_pk_fma_f32 v[204:205], v[92:93], v[30:31], v[204:205] op_sel:[0,0,0] op_sel_hi:[1,0,1]
	v_pk_fma_f32 v[198:199], v[148:149], v[46:47], v[198:199] op_sel:[0,0,0] op_sel_hi:[1,0,1]
	v_pk_fma_f32 v[200:201], v[150:151], v[46:47], v[200:201] op_sel:[0,0,0] op_sel_hi:[1,0,1]
	v_pk_fma_f32 v[202:203], v[152:153], v[46:47], v[202:203] op_sel:[0,0,0] op_sel_hi:[1,0,1]
	v_pk_fma_f32 v[204:205], v[154:155], v[46:47], v[204:205] op_sel:[0,0,0] op_sel_hi:[1,0,1]
	v_pk_fma_f32 v[198:199], v[88:89], v[30:31], v[198:199] op_sel:[0,1,0] op_sel_hi:[1,1,1]
	v_pk_fma_f32 v[200:201], v[90:91], v[30:31], v[200:201] op_sel:[0,1,0] op_sel_hi:[1,1,1]
	v_pk_fma_f32 v[202:203], v[92:93], v[30:31], v[202:203] op_sel:[0,1,0] op_sel_hi:[1,1,1]
	v_pk_fma_f32 v[204:205], v[94:95], v[30:31], v[204:205] op_sel:[0,1,0] op_sel_hi:[1,1,1]
	v_pk_fma_f32 v[198:199], v[150:151], v[32:33], v[198:199] op_sel:[0,0,0] op_sel_hi:[1,0,1]
	v_pk_fma_f32 v[200:201], v[152:153], v[32:33], v[200:201] op_sel:[0,0,0] op_sel_hi:[1,0,1]
	v_pk_fma_f32 v[202:203], v[154:155], v[32:33], v[202:203] op_sel:[0,0,0] op_sel_hi:[1,0,1]
	v_pk_fma_f32 v[204:205], v[156:157], v[32:33], v[204:205] op_sel:[0,0,0] op_sel_hi:[1,0,1]
	v_pk_fma_f32 v[198:199], v[90:91], v[32:33], v[198:199] op_sel:[0,1,0] op_sel_hi:[1,1,1]
	v_pk_fma_f32 v[200:201], v[92:93], v[32:33], v[200:201] op_sel:[0,1,0] op_sel_hi:[1,1,1]
	v_pk_fma_f32 v[202:203], v[94:95], v[32:33], v[202:203] op_sel:[0,1,0] op_sel_hi:[1,1,1]
	v_pk_fma_f32 v[204:205], v[96:97], v[32:33], v[204:205] op_sel:[0,1,0] op_sel_hi:[1,1,1]
	v_pk_fma_f32 v[198:199], v[152:153], v[46:47], v[198:199] op_sel:[0,1,0] op_sel_hi:[1,1,1]
	v_pk_fma_f32 v[200:201], v[154:155], v[46:47], v[200:201] op_sel:[0,1,0] op_sel_hi:[1,1,1]
	v_pk_fma_f32 v[202:203], v[156:157], v[46:47], v[202:203] op_sel:[0,1,0] op_sel_hi:[1,1,1]
	v_pk_fma_f32 v[204:205], v[158:159], v[46:47], v[204:205] op_sel:[0,1,0] op_sel_hi:[1,1,1]
	v_pk_fma_f32 v[198:199], v[92:93], v[34:35], v[198:199] op_sel:[0,0,0] op_sel_hi:[1,0,1]
	v_pk_fma_f32 v[200:201], v[94:95], v[34:35], v[200:201] op_sel:[0,0,0] op_sel_hi:[1,0,1]
	v_pk_fma_f32 v[202:203], v[96:97], v[34:35], v[202:203] op_sel:[0,0,0] op_sel_hi:[1,0,1]
	v_pk_fma_f32 v[204:205], v[98:99], v[34:35], v[204:205] op_sel:[0,0,0] op_sel_hi:[1,0,1]
	v_pk_fma_f32 v[198:199], v[154:155], v[34:35], v[198:199] op_sel:[0,1,0] op_sel_hi:[1,1,1]
; __device__ __forceinline__ void conv_phase(LAS unsigned char* lds, int tile, int tid, const bf16* __restrict__ U, const float* __restrict__ cw, const float* __restrict__ cb, ...
;     ...
;             for (int tk = 0; tk < HT; ++tk) { float a = bias;
; #pragma unroll
;                 for (int j = 0; j < CKW; ++j) a += w[j] * uc[tk + j];
;                 obuf[tk * CH + tid] = a; }
	v_pk_fma_f32 v[200:201], v[156:157], v[34:35], v[200:201] op_sel:[0,1,0] op_sel_hi:[1,1,1]
	v_pk_fma_f32 v[202:203], v[158:159], v[34:35], v[202:203] op_sel:[0,1,0] op_sel_hi:[1,1,1]
	v_pk_fma_f32 v[204:205], v[160:161], v[34:35], v[204:205] op_sel:[0,1,0] op_sel_hi:[1,1,1]
	v_pk_fma_f32 v[198:199], v[94:95], v[36:37], v[198:199] op_sel:[0,0,0] op_sel_hi:[1,0,1]
	v_pk_fma_f32 v[200:201], v[96:97], v[36:37], v[200:201] op_sel:[0,0,0] op_sel_hi:[1,0,1]
	v_pk_fma_f32 v[202:203], v[98:99], v[36:37], v[202:203] op_sel:[0,0,0] op_sel_hi:[1,0,1]
	v_pk_fma_f32 v[204:205], v[100:101], v[36:37], v[204:205] op_sel:[0,0,0] op_sel_hi:[1,0,1]
	v_pk_fma_f32 v[198:199], v[156:157], v[48:49], v[198:199] op_sel:[0,0,0] op_sel_hi:[1,0,1]
	v_pk_fma_f32 v[200:201], v[158:159], v[48:49], v[200:201] op_sel:[0,0,0] op_sel_hi:[1,0,1]
	v_pk_fma_f32 v[202:203], v[160:161], v[48:49], v[202:203] op_sel:[0,0,0] op_sel_hi:[1,0,1]
	v_pk_fma_f32 v[204:205], v[162:163], v[48:49], v[204:205] op_sel:[0,0,0] op_sel_hi:[1,0,1]
	v_pk_fma_f32 v[198:199], v[96:97], v[36:37], v[198:199] op_sel:[0,1,0] op_sel_hi:[1,1,1]
	v_pk_fma_f32 v[200:201], v[98:99], v[36:37], v[200:201] op_sel:[0,1,0] op_sel_hi:[1,1,1]
	v_pk_fma_f32 v[202:203], v[100:101], v[36:37], v[202:203] op_sel:[0,1,0] op_sel_hi:[1,1,1]
	v_pk_fma_f32 v[204:205], v[102:103], v[36:37], v[204:205] op_sel:[0,1,0] op_sel_hi:[1,1,1]
	v_pk_fma_f32 v[198:199], v[158:159], v[38:39], v[198:199] op_sel:[0,0,0] op_sel_hi:[1,0,1]
	v_pk_fma_f32 v[200:201], v[160:161], v[38:39], v[200:201] op_sel:[0,0,0] op_sel_hi:[1,0,1]
	v_pk_fma_f32 v[202:203], v[162:163], v[38:39], v[202:203] op_sel:[0,0,0] op_sel_hi:[1,0,1]
	v_pk_fma_f32 v[204:205], v[164:165], v[38:39], v[204:205] op_sel:[0,0,0] op_sel_hi:[1,0,1]
	v_pk_fma_f32 v[198:199], v[98:99], v[38:39], v[198:199] op_sel:[0,1,0] op_sel_hi:[1,1,1]
	v_pk_fma_f32 v[200:201], v[100:101], v[38:39], v[200:201] op_sel:[0,1,0] op_sel_hi:[1,1,1]
	v_pk_fma_f32 v[202:203], v[102:103], v[38:39], v[202:203] op_sel:[0,1,0] op_sel_hi:[1,1,1]
	v_pk_fma_f32 v[204:205], v[104:105], v[38:39], v[204:205] op_sel:[0,1,0] op_sel_hi:[1,1,1]
	v_pk_fma_f32 v[198:199], v[160:161], v[48:49], v[198:199] op_sel:[0,1,0] op_sel_hi:[1,1,1]
	v_pk_fma_f32 v[200:201], v[162:163], v[48:49], v[200:201] op_sel:[0,1,0] op_sel_hi:[1,1,1]
	v_pk_fma_f32 v[202:203], v[164:165], v[48:49], v[202:203] op_sel:[0,1,0] op_sel_hi:[1,1,1]
	v_pk_fma_f32 v[204:205], v[166:167], v[48:49], v[204:205] op_sel:[0,1,0] op_sel_hi:[1,1,1]
	v_pk_fma_f32 v[198:199], v[100:101], v[40:41], v[198:199] op_sel:[0,0,0] op_sel_hi:[1,0,1]
	v_pk_fma_f32 v[200:201], v[102:103], v[40:41], v[200:201] op_sel:[0,0,0] op_sel_hi:[1,0,1]
	v_pk_fma_f32 v[202:203], v[104:105], v[40:41], v[202:203] op_sel:[0,0,0] op_sel_hi:[1,0,1]
	v_pk_fma_f32 v[204:205], v[106:107], v[40:41], v[204:205] op_sel:[0,0,0] op_sel_hi:[1,0,1]
	v_pk_fma_f32 v[198:199], v[162:163], v[40:41], v[198:199] op_sel:[0,1,0] op_sel_hi:[1,1,1]
	v_pk_fma_f32 v[200:201], v[164:165], v[40:41], v[200:201] op_sel:[0,1,0] op_sel_hi:[1,1,1]
	v_pk_fma_f32 v[202:203], v[166:167], v[40:41], v[202:203] op_sel:[0,1,0] op_sel_hi:[1,1,1]
	v_pk_fma_f32 v[204:205], v[168:169], v[40:41], v[204:205] op_sel:[0,1,0] op_sel_hi:[1,1,1]
	v_pk_fma_f32 v[198:199], v[102:103], v[42:43], v[198:199] op_sel:[0,0,0] op_sel_hi:[1,0,1]
	v_pk_fma_f32 v[200:201], v[104:105], v[42:43], v[200:201] op_sel:[0,0,0] op_sel_hi:[1,0,1]
	v_pk_fma_f32 v[202:203], v[106:107], v[42:43], v[202:203] op_sel:[0,0,0] op_sel_hi:[1,0,1]
	v_pk_fma_f32 v[204:205], v[108:109], v[42:43], v[204:205] op_sel:[0,0,0] op_sel_hi:[1,0,1]
	v_pk_fma_f32 v[198:199], v[164:165], v[50:51], v[198:199] op_sel:[0,0,0] op_sel_hi:[1,0,1]
	v_pk_fma_f32 v[200:201], v[166:167], v[50:51], v[200:201] op_sel:[0,0,0] op_sel_hi:[1,0,1]
	v_pk_fma_f32 v[202:203], v[168:169], v[50:51], v[202:203] op_sel:[0,0,0] op_sel_hi:[1,0,1]
	v_pk_fma_f32 v[204:205], v[170:171], v[50:51], v[204:205] op_sel:[0,0,0] op_sel_hi:[1,0,1]
	v_pk_fma_f32 v[198:199], v[104:105], v[50:51], v[198:199] op_sel:[0,1,0] op_sel_hi:[1,1,1]
	v_pk_fma_f32 v[200:201], v[106:107], v[50:51], v[200:201] op_sel:[0,1,0] op_sel_hi:[1,1,1]
	v_pk_fma_f32 v[202:203], v[108:109], v[50:51], v[202:203] op_sel:[0,1,0] op_sel_hi:[1,1,1]
	v_pk_fma_f32 v[204:205], v[110:111], v[50:51], v[204:205] op_sel:[0,1,0] op_sel_hi:[1,1,1]
	v_pk_fma_f32 v[198:199], v[166:167], v[52:53], v[198:199] op_sel:[0,0,0] op_sel_hi:[1,0,1]
	v_pk_fma_f32 v[200:201], v[168:169], v[52:53], v[200:201] op_sel:[0,0,0] op_sel_hi:[1,0,1]
	v_pk_fma_f32 v[202:203], v[170:171], v[52:53], v[202:203] op_sel:[0,0,0] op_sel_hi:[1,0,1]
	v_pk_fma_f32 v[204:205], v[172:173], v[52:53], v[204:205] op_sel:[0,0,0] op_sel_hi:[1,0,1]
	v_pk_fma_f32 v[198:199], v[106:107], v[52:53], v[198:199] op_sel:[0,1,0] op_sel_hi:[1,1,1]
	v_pk_fma_f32 v[200:201], v[108:109], v[52:53], v[200:201] op_sel:[0,1,0] op_sel_hi:[1,1,1]
	v_pk_fma_f32 v[202:203], v[110:111], v[52:53], v[202:203] op_sel:[0,1,0] op_sel_hi:[1,1,1]
	v_pk_fma_f32 v[204:205], v[112:113], v[52:53], v[204:205] op_sel:[0,1,0] op_sel_hi:[1,1,1]
	v_pk_fma_f32 v[198:199], v[168:169], v[56:57], v[198:199] op_sel:[0,0,0] op_sel_hi:[1,0,1]
	v_pk_fma_f32 v[200:201], v[170:171], v[56:57], v[200:201] op_sel:[0,0,0] op_sel_hi:[1,0,1]
	v_pk_fma_f32 v[202:203], v[172:173], v[56:57], v[202:203] op_sel:[0,0,0] op_sel_hi:[1,0,1]
	v_pk_fma_f32 v[204:205], v[174:175], v[56:57], v[204:205] op_sel:[0,0,0] op_sel_hi:[1,0,1]
	v_pk_fma_f32 v[198:199], v[108:109], v[54:55], v[198:199] op_sel:[0,0,0] op_sel_hi:[1,0,1]
	v_pk_fma_f32 v[200:201], v[110:111], v[54:55], v[200:201] op_sel:[0,0,0] op_sel_hi:[1,0,1]
; __device__ __forceinline__ void conv_phase(LAS unsigned char* lds, int tile, int tid, const bf16* __restrict__ U, const float* __restrict__ cw, const float* __restrict__ cb, ...
;     ...
;             for (int tk = 0; tk < HT; ++tk) { float a = bias;
; #pragma unroll
;                 for (int j = 0; j < CKW; ++j) a += w[j] * uc[tk + j];
;                 obuf[tk * CH + tid] = a; }
	v_pk_fma_f32 v[202:203], v[112:113], v[54:55], v[202:203] op_sel:[0,0,0] op_sel_hi:[1,0,1]
	v_pk_fma_f32 v[204:205], v[114:115], v[54:55], v[204:205] op_sel:[0,0,0] op_sel_hi:[1,0,1]
	v_pk_fma_f32 v[198:199], v[170:171], v[54:55], v[198:199] op_sel:[0,1,0] op_sel_hi:[1,1,1]
	v_pk_fma_f32 v[200:201], v[172:173], v[54:55], v[200:201] op_sel:[0,1,0] op_sel_hi:[1,1,1]
	v_pk_fma_f32 v[202:203], v[174:175], v[54:55], v[202:203] op_sel:[0,1,0] op_sel_hi:[1,1,1]
	v_pk_fma_f32 v[204:205], v[176:177], v[54:55], v[204:205] op_sel:[0,1,0] op_sel_hi:[1,1,1]
	v_pk_fma_f32 v[198:199], v[110:111], v[56:57], v[198:199] op_sel:[0,1,0] op_sel_hi:[1,1,1]
	v_pk_fma_f32 v[200:201], v[112:113], v[56:57], v[200:201] op_sel:[0,1,0] op_sel_hi:[1,1,1]
	v_pk_fma_f32 v[202:203], v[114:115], v[56:57], v[202:203] op_sel:[0,1,0] op_sel_hi:[1,1,1]
	v_pk_fma_f32 v[204:205], v[116:117], v[56:57], v[204:205] op_sel:[0,1,0] op_sel_hi:[1,1,1]
	ds_write2st64_b32 v66, v198, v199 offset0:64 offset1:72
	ds_write2st64_b32 v66, v200, v201 offset0:80 offset1:88
	ds_write2st64_b32 v66, v202, v203 offset0:96 offset1:104
	ds_write2st64_b32 v66, v204, v205 offset0:112 offset1:120
	v_pk_fma_f32 v[198:199], v[88:89], v[42:43], v[58:59] op_sel:[0,1,0] op_sel_hi:[1,1,0]
	v_pk_fma_f32 v[200:201], v[90:91], v[42:43], v[58:59] op_sel:[0,1,0] op_sel_hi:[1,1,0]
	v_pk_fma_f32 v[202:203], v[92:93], v[42:43], v[58:59] op_sel:[0,1,0] op_sel_hi:[1,1,0]
	v_pk_fma_f32 v[204:205], v[94:95], v[42:43], v[58:59] op_sel:[0,1,0] op_sel_hi:[1,1,0]
	v_pk_fma_f32 v[198:199], v[150:151], v[44:45], v[198:199] op_sel:[0,0,0] op_sel_hi:[1,0,1]
	v_pk_fma_f32 v[200:201], v[152:153], v[44:45], v[200:201] op_sel:[0,0,0] op_sel_hi:[1,0,1]
	v_pk_fma_f32 v[202:203], v[154:155], v[44:45], v[202:203] op_sel:[0,0,0] op_sel_hi:[1,0,1]
	v_pk_fma_f32 v[204:205], v[156:157], v[44:45], v[204:205] op_sel:[0,0,0] op_sel_hi:[1,0,1]
	v_pk_fma_f32 v[198:199], v[90:91], v[18:19], v[198:199] op_sel:[0,1,0] op_sel_hi:[1,1,1]
	v_pk_fma_f32 v[200:201], v[92:93], v[18:19], v[200:201] op_sel:[0,1,0] op_sel_hi:[1,1,1]
	v_pk_fma_f32 v[202:203], v[94:95], v[18:19], v[202:203] op_sel:[0,1,0] op_sel_hi:[1,1,1]
	v_pk_fma_f32 v[204:205], v[96:97], v[18:19], v[204:205] op_sel:[0,1,0] op_sel_hi:[1,1,1]
	v_pk_fma_f32 v[198:199], v[152:153], v[44:45], v[198:199] op_sel:[0,1,0] op_sel_hi:[1,1,1]
	v_pk_fma_f32 v[200:201], v[154:155], v[44:45], v[200:201] op_sel:[0,1,0] op_sel_hi:[1,1,1]
	v_pk_fma_f32 v[202:203], v[156:157], v[44:45], v[202:203] op_sel:[0,1,0] op_sel_hi:[1,1,1]
	v_pk_fma_f32 v[204:205], v[158:159], v[44:45], v[204:205] op_sel:[0,1,0] op_sel_hi:[1,1,1]
	v_pk_fma_f32 v[198:199], v[92:93], v[28:29], v[198:199] op_sel:[0,0,0] op_sel_hi:[1,0,1]
	v_pk_fma_f32 v[200:201], v[94:95], v[28:29], v[200:201] op_sel:[0,0,0] op_sel_hi:[1,0,1]
	v_pk_fma_f32 v[202:203], v[96:97], v[28:29], v[202:203] op_sel:[0,0,0] op_sel_hi:[1,0,1]
	v_pk_fma_f32 v[204:205], v[98:99], v[28:29], v[204:205] op_sel:[0,0,0] op_sel_hi:[1,0,1]
	v_pk_fma_f32 v[198:199], v[154:155], v[28:29], v[198:199] op_sel:[0,1,0] op_sel_hi:[1,1,1]
	v_pk_fma_f32 v[200:201], v[156:157], v[28:29], v[200:201] op_sel:[0,1,0] op_sel_hi:[1,1,1]
	v_pk_fma_f32 v[202:203], v[158:159], v[28:29], v[202:203] op_sel:[0,1,0] op_sel_hi:[1,1,1]
	v_pk_fma_f32 v[204:205], v[160:161], v[28:29], v[204:205] op_sel:[0,1,0] op_sel_hi:[1,1,1]
	v_pk_fma_f32 v[198:199], v[94:95], v[30:31], v[198:199] op_sel:[0,0,0] op_sel_hi:[1,0,1]
	v_pk_fma_f32 v[200:201], v[96:97], v[30:31], v[200:201] op_sel:[0,0,0] op_sel_hi:[1,0,1]
	v_pk_fma_f32 v[202:203], v[98:99], v[30:31], v[202:203] op_sel:[0,0,0] op_sel_hi:[1,0,1]
	v_pk_fma_f32 v[204:205], v[100:101], v[30:31], v[204:205] op_sel:[0,0,0] op_sel_hi:[1,0,1]
	v_pk_fma_f32 v[198:199], v[156:157], v[46:47], v[198:199] op_sel:[0,0,0] op_sel_hi:[1,0,1]
	v_pk_fma_f32 v[200:201], v[158:159], v[46:47], v[200:201] op_sel:[0,0,0] op_sel_hi:[1,0,1]
	v_pk_fma_f32 v[202:203], v[160:161], v[46:47], v[202:203] op_sel:[0,0,0] op_sel_hi:[1,0,1]
	v_pk_fma_f32 v[204:205], v[162:163], v[46:47], v[204:205] op_sel:[0,0,0] op_sel_hi:[1,0,1]
	v_pk_fma_f32 v[198:199], v[96:97], v[30:31], v[198:199] op_sel:[0,1,0] op_sel_hi:[1,1,1]
	v_pk_fma_f32 v[200:201], v[98:99], v[30:31], v[200:201] op_sel:[0,1,0] op_sel_hi:[1,1,1]
	v_pk_fma_f32 v[202:203], v[100:101], v[30:31], v[202:203] op_sel:[0,1,0] op_sel_hi:[1,1,1]
	v_pk_fma_f32 v[204:205], v[102:103], v[30:31], v[204:205] op_sel:[0,1,0] op_sel_hi:[1,1,1]
	v_pk_fma_f32 v[198:199], v[158:159], v[32:33], v[198:199] op_sel:[0,0,0] op_sel_hi:[1,0,1]
	v_pk_fma_f32 v[200:201], v[160:161], v[32:33], v[200:201] op_sel:[0,0,0] op_sel_hi:[1,0,1]
	v_pk_fma_f32 v[202:203], v[162:163], v[32:33], v[202:203] op_sel:[0,0,0] op_sel_hi:[1,0,1]
	v_pk_fma_f32 v[204:205], v[164:165], v[32:33], v[204:205] op_sel:[0,0,0] op_sel_hi:[1,0,1]
	v_pk_fma_f32 v[198:199], v[98:99], v[32:33], v[198:199] op_sel:[0,1,0] op_sel_hi:[1,1,1]
	v_pk_fma_f32 v[200:201], v[100:101], v[32:33], v[200:201] op_sel:[0,1,0] op_sel_hi:[1,1,1]
	v_pk_fma_f32 v[202:203], v[102:103], v[32:33], v[202:203] op_sel:[0,1,0] op_sel_hi:[1,1,1]
	v_pk_fma_f32 v[204:205], v[104:105], v[32:33], v[204:205] op_sel:[0,1,0] op_sel_hi:[1,1,1]
	v_pk_fma_f32 v[198:199], v[160:161], v[46:47], v[198:199] op_sel:[0,1,0] op_sel_hi:[1,1,1]
	v_pk_fma_f32 v[200:201], v[162:163], v[46:47], v[200:201] op_sel:[0,1,0] op_sel_hi:[1,1,1]
	v_pk_fma_f32 v[202:203], v[164:165], v[46:47], v[202:203] op_sel:[0,1,0] op_sel_hi:[1,1,1]
	v_pk_fma_f32 v[204:205], v[166:167], v[46:47], v[204:205] op_sel:[0,1,0] op_sel_hi:[1,1,1]
	v_pk_fma_f32 v[198:199], v[100:101], v[34:35], v[198:199] op_sel:[0,0,0] op_sel_hi:[1,0,1]
; __device__ __forceinline__ void conv_phase(LAS unsigned char* lds, int tile, int tid, const bf16* __restrict__ U, const float* __restrict__ cw, const float* __restrict__ cb, ...
;     ...
;             for (int tk = 0; tk < HT; ++tk) { float a = bias;
; #pragma unroll
;                 for (int j = 0; j < CKW; ++j) a += w[j] * uc[tk + j];
;                 obuf[tk * CH + tid] = a; }
	v_pk_fma_f32 v[200:201], v[102:103], v[34:35], v[200:201] op_sel:[0,0,0] op_sel_hi:[1,0,1]
	v_pk_fma_f32 v[202:203], v[104:105], v[34:35], v[202:203] op_sel:[0,0,0] op_sel_hi:[1,0,1]
	v_pk_fma_f32 v[204:205], v[106:107], v[34:35], v[204:205] op_sel:[0,0,0] op_sel_hi:[1,0,1]
	v_pk_fma_f32 v[198:199], v[162:163], v[34:35], v[198:199] op_sel:[0,1,0] op_sel_hi:[1,1,1]
	v_pk_fma_f32 v[200:201], v[164:165], v[34:35], v[200:201] op_sel:[0,1,0] op_sel_hi:[1,1,1]
	v_pk_fma_f32 v[202:203], v[166:167], v[34:35], v[202:203] op_sel:[0,1,0] op_sel_hi:[1,1,1]
	v_pk_fma_f32 v[204:205], v[168:169], v[34:35], v[204:205] op_sel:[0,1,0] op_sel_hi:[1,1,1]
	v_pk_fma_f32 v[198:199], v[102:103], v[36:37], v[198:199] op_sel:[0,0,0] op_sel_hi:[1,0,1]
	v_pk_fma_f32 v[200:201], v[104:105], v[36:37], v[200:201] op_sel:[0,0,0] op_sel_hi:[1,0,1]
	v_pk_fma_f32 v[202:203], v[106:107], v[36:37], v[202:203] op_sel:[0,0,0] op_sel_hi:[1,0,1]
	v_pk_fma_f32 v[204:205], v[108:109], v[36:37], v[204:205] op_sel:[0,0,0] op_sel_hi:[1,0,1]
	v_pk_fma_f32 v[198:199], v[164:165], v[48:49], v[198:199] op_sel:[0,0,0] op_sel_hi:[1,0,1]
	v_pk_fma_f32 v[200:201], v[166:167], v[48:49], v[200:201] op_sel:[0,0,0] op_sel_hi:[1,0,1]
	v_pk_fma_f32 v[202:203], v[168:169], v[48:49], v[202:203] op_sel:[0,0,0] op_sel_hi:[1,0,1]
	v_pk_fma_f32 v[204:205], v[170:171], v[48:49], v[204:205] op_sel:[0,0,0] op_sel_hi:[1,0,1]
	v_pk_fma_f32 v[198:199], v[104:105], v[36:37], v[198:199] op_sel:[0,1,0] op_sel_hi:[1,1,1]
	v_pk_fma_f32 v[200:201], v[106:107], v[36:37], v[200:201] op_sel:[0,1,0] op_sel_hi:[1,1,1]
	v_pk_fma_f32 v[202:203], v[108:109], v[36:37], v[202:203] op_sel:[0,1,0] op_sel_hi:[1,1,1]
	v_pk_fma_f32 v[204:205], v[110:111], v[36:37], v[204:205] op_sel:[0,1,0] op_sel_hi:[1,1,1]
	v_pk_fma_f32 v[198:199], v[166:167], v[38:39], v[198:199] op_sel:[0,0,0] op_sel_hi:[1,0,1]
	v_pk_fma_f32 v[200:201], v[168:169], v[38:39], v[200:201] op_sel:[0,0,0] op_sel_hi:[1,0,1]
	v_pk_fma_f32 v[202:203], v[170:171], v[38:39], v[202:203] op_sel:[0,0,0] op_sel_hi:[1,0,1]
	v_pk_fma_f32 v[204:205], v[172:173], v[38:39], v[204:205] op_sel:[0,0,0] op_sel_hi:[1,0,1]
	v_pk_fma_f32 v[198:199], v[106:107], v[38:39], v[198:199] op_sel:[0,1,0] op_sel_hi:[1,1,1]
	v_pk_fma_f32 v[200:201], v[108:109], v[38:39], v[200:201] op_sel:[0,1,0] op_sel_hi:[1,1,1]
	v_pk_fma_f32 v[202:203], v[110:111], v[38:39], v[202:203] op_sel:[0,1,0] op_sel_hi:[1,1,1]
	v_pk_fma_f32 v[204:205], v[112:113], v[38:39], v[204:205] op_sel:[0,1,0] op_sel_hi:[1,1,1]
	v_pk_fma_f32 v[198:199], v[168:169], v[48:49], v[198:199] op_sel:[0,1,0] op_sel_hi:[1,1,1]
	v_pk_fma_f32 v[200:201], v[170:171], v[48:49], v[200:201] op_sel:[0,1,0] op_sel_hi:[1,1,1]
	v_pk_fma_f32 v[202:203], v[172:173], v[48:49], v[202:203] op_sel:[0,1,0] op_sel_hi:[1,1,1]
	v_pk_fma_f32 v[204:205], v[174:175], v[48:49], v[204:205] op_sel:[0,1,0] op_sel_hi:[1,1,1]
	v_pk_fma_f32 v[198:199], v[108:109], v[40:41], v[198:199] op_sel:[0,0,0] op_sel_hi:[1,0,1]
	v_pk_fma_f32 v[200:201], v[110:111], v[40:41], v[200:201] op_sel:[0,0,0] op_sel_hi:[1,0,1]
	v_pk_fma_f32 v[202:203], v[112:113], v[40:41], v[202:203] op_sel:[0,0,0] op_sel_hi:[1,0,1]
	v_pk_fma_f32 v[204:205], v[114:115], v[40:41], v[204:205] op_sel:[0,0,0] op_sel_hi:[1,0,1]
	v_pk_fma_f32 v[198:199], v[170:171], v[40:41], v[198:199] op_sel:[0,1,0] op_sel_hi:[1,1,1]
	v_pk_fma_f32 v[200:201], v[172:173], v[40:41], v[200:201] op_sel:[0,1,0] op_sel_hi:[1,1,1]
	v_pk_fma_f32 v[202:203], v[174:175], v[40:41], v[202:203] op_sel:[0,1,0] op_sel_hi:[1,1,1]
	v_pk_fma_f32 v[204:205], v[176:177], v[40:41], v[204:205] op_sel:[0,1,0] op_sel_hi:[1,1,1]
	v_pk_fma_f32 v[198:199], v[110:111], v[42:43], v[198:199] op_sel:[0,0,0] op_sel_hi:[1,0,1]
	v_pk_fma_f32 v[200:201], v[112:113], v[42:43], v[200:201] op_sel:[0,0,0] op_sel_hi:[1,0,1]
	v_pk_fma_f32 v[202:203], v[114:115], v[42:43], v[202:203] op_sel:[0,0,0] op_sel_hi:[1,0,1]
	v_pk_fma_f32 v[204:205], v[116:117], v[42:43], v[204:205] op_sel:[0,0,0] op_sel_hi:[1,0,1]
	v_pk_fma_f32 v[198:199], v[172:173], v[50:51], v[198:199] op_sel:[0,0,0] op_sel_hi:[1,0,1]
	v_pk_fma_f32 v[200:201], v[174:175], v[50:51], v[200:201] op_sel:[0,0,0] op_sel_hi:[1,0,1]
	v_pk_fma_f32 v[202:203], v[176:177], v[50:51], v[202:203] op_sel:[0,0,0] op_sel_hi:[1,0,1]
	v_pk_fma_f32 v[204:205], v[178:179], v[50:51], v[204:205] op_sel:[0,0,0] op_sel_hi:[1,0,1]
	v_pk_fma_f32 v[198:199], v[112:113], v[50:51], v[198:199] op_sel:[0,1,0] op_sel_hi:[1,1,1]
	v_pk_fma_f32 v[200:201], v[114:115], v[50:51], v[200:201] op_sel:[0,1,0] op_sel_hi:[1,1,1]
	v_pk_fma_f32 v[202:203], v[116:117], v[50:51], v[202:203] op_sel:[0,1,0] op_sel_hi:[1,1,1]
	v_pk_fma_f32 v[204:205], v[118:119], v[50:51], v[204:205] op_sel:[0,1,0] op_sel_hi:[1,1,1]
	v_pk_fma_f32 v[198:199], v[174:175], v[52:53], v[198:199] op_sel:[0,0,0] op_sel_hi:[1,0,1]
	v_pk_fma_f32 v[200:201], v[176:177], v[52:53], v[200:201] op_sel:[0,0,0] op_sel_hi:[1,0,1]
	v_pk_fma_f32 v[202:203], v[178:179], v[52:53], v[202:203] op_sel:[0,0,0] op_sel_hi:[1,0,1]
	v_pk_fma_f32 v[204:205], v[180:181], v[52:53], v[204:205] op_sel:[0,0,0] op_sel_hi:[1,0,1]
	v_pk_fma_f32 v[198:199], v[114:115], v[52:53], v[198:199] op_sel:[0,1,0] op_sel_hi:[1,1,1]
	v_pk_fma_f32 v[200:201], v[116:117], v[52:53], v[200:201] op_sel:[0,1,0] op_sel_hi:[1,1,1]
	v_pk_fma_f32 v[202:203], v[118:119], v[52:53], v[202:203] op_sel:[0,1,0] op_sel_hi:[1,1,1]
	v_pk_fma_f32 v[204:205], v[120:121], v[52:53], v[204:205] op_sel:[0,1,0] op_sel_hi:[1,1,1]
	v_pk_fma_f32 v[198:199], v[176:177], v[56:57], v[198:199] op_sel:[0,0,0] op_sel_hi:[1,0,1]
	v_pk_fma_f32 v[200:201], v[178:179], v[56:57], v[200:201] op_sel:[0,0,0] op_sel_hi:[1,0,1]
; __device__ __forceinline__ void conv_phase(LAS unsigned char* lds, int tile, int tid, const bf16* __restrict__ U, const float* __restrict__ cw, const float* __restrict__ cb, ...
;     ...
;             for (int tk = 0; tk < HT; ++tk) { float a = bias;
; #pragma unroll
;                 for (int j = 0; j < CKW; ++j) a += w[j] * uc[tk + j];
;                 obuf[tk * CH + tid] = a; }
	v_pk_fma_f32 v[202:203], v[180:181], v[56:57], v[202:203] op_sel:[0,0,0] op_sel_hi:[1,0,1]
	v_pk_fma_f32 v[204:205], v[182:183], v[56:57], v[204:205] op_sel:[0,0,0] op_sel_hi:[1,0,1]
	v_pk_fma_f32 v[198:199], v[116:117], v[54:55], v[198:199] op_sel:[0,0,0] op_sel_hi:[1,0,1]
	v_pk_fma_f32 v[200:201], v[118:119], v[54:55], v[200:201] op_sel:[0,0,0] op_sel_hi:[1,0,1]
	v_pk_fma_f32 v[202:203], v[120:121], v[54:55], v[202:203] op_sel:[0,0,0] op_sel_hi:[1,0,1]
	v_pk_fma_f32 v[204:205], v[122:123], v[54:55], v[204:205] op_sel:[0,0,0] op_sel_hi:[1,0,1]
	v_pk_fma_f32 v[198:199], v[178:179], v[54:55], v[198:199] op_sel:[0,1,0] op_sel_hi:[1,1,1]
	v_pk_fma_f32 v[200:201], v[180:181], v[54:55], v[200:201] op_sel:[0,1,0] op_sel_hi:[1,1,1]
	v_pk_fma_f32 v[202:203], v[182:183], v[54:55], v[202:203] op_sel:[0,1,0] op_sel_hi:[1,1,1]
	v_pk_fma_f32 v[204:205], v[184:185], v[54:55], v[204:205] op_sel:[0,1,0] op_sel_hi:[1,1,1]
	v_pk_fma_f32 v[198:199], v[118:119], v[56:57], v[198:199] op_sel:[0,1,0] op_sel_hi:[1,1,1]
	v_pk_fma_f32 v[200:201], v[120:121], v[56:57], v[200:201] op_sel:[0,1,0] op_sel_hi:[1,1,1]
	v_pk_fma_f32 v[202:203], v[122:123], v[56:57], v[202:203] op_sel:[0,1,0] op_sel_hi:[1,1,1]
	v_pk_fma_f32 v[204:205], v[124:125], v[56:57], v[204:205] op_sel:[0,1,0] op_sel_hi:[1,1,1]
	ds_write2st64_b32 v66, v198, v199 offset0:128 offset1:136
	ds_write2st64_b32 v66, v200, v201 offset0:144 offset1:152
	ds_write2st64_b32 v66, v202, v203 offset0:160 offset1:168
	ds_write2st64_b32 v66, v204, v205 offset0:176 offset1:184
	v_pk_fma_f32 v[198:199], v[96:97], v[42:43], v[58:59] op_sel:[0,1,0] op_sel_hi:[1,1,0]
	v_pk_fma_f32 v[200:201], v[98:99], v[42:43], v[58:59] op_sel:[0,1,0] op_sel_hi:[1,1,0]
	v_pk_fma_f32 v[202:203], v[100:101], v[42:43], v[58:59] op_sel:[0,1,0] op_sel_hi:[1,1,0]
	v_pk_fma_f32 v[204:205], v[102:103], v[42:43], v[58:59] op_sel:[0,1,0] op_sel_hi:[1,1,0]
	v_pk_fma_f32 v[198:199], v[158:159], v[44:45], v[198:199] op_sel:[0,0,0] op_sel_hi:[1,0,1]
	v_pk_fma_f32 v[200:201], v[160:161], v[44:45], v[200:201] op_sel:[0,0,0] op_sel_hi:[1,0,1]
	v_pk_fma_f32 v[202:203], v[162:163], v[44:45], v[202:203] op_sel:[0,0,0] op_sel_hi:[1,0,1]
	v_pk_fma_f32 v[204:205], v[164:165], v[44:45], v[204:205] op_sel:[0,0,0] op_sel_hi:[1,0,1]
	v_pk_fma_f32 v[198:199], v[98:99], v[18:19], v[198:199] op_sel:[0,1,0] op_sel_hi:[1,1,1]
	v_pk_fma_f32 v[200:201], v[100:101], v[18:19], v[200:201] op_sel:[0,1,0] op_sel_hi:[1,1,1]
	v_pk_fma_f32 v[202:203], v[102:103], v[18:19], v[202:203] op_sel:[0,1,0] op_sel_hi:[1,1,1]
	v_pk_fma_f32 v[204:205], v[104:105], v[18:19], v[204:205] op_sel:[0,1,0] op_sel_hi:[1,1,1]
	v_pk_fma_f32 v[198:199], v[160:161], v[44:45], v[198:199] op_sel:[0,1,0] op_sel_hi:[1,1,1]
	v_pk_fma_f32 v[200:201], v[162:163], v[44:45], v[200:201] op_sel:[0,1,0] op_sel_hi:[1,1,1]
	v_pk_fma_f32 v[202:203], v[164:165], v[44:45], v[202:203] op_sel:[0,1,0] op_sel_hi:[1,1,1]
	v_pk_fma_f32 v[204:205], v[166:167], v[44:45], v[204:205] op_sel:[0,1,0] op_sel_hi:[1,1,1]
	v_pk_fma_f32 v[198:199], v[100:101], v[28:29], v[198:199] op_sel:[0,0,0] op_sel_hi:[1,0,1]
	v_pk_fma_f32 v[200:201], v[102:103], v[28:29], v[200:201] op_sel:[0,0,0] op_sel_hi:[1,0,1]
	v_pk_fma_f32 v[202:203], v[104:105], v[28:29], v[202:203] op_sel:[0,0,0] op_sel_hi:[1,0,1]
	v_pk_fma_f32 v[204:205], v[106:107], v[28:29], v[204:205] op_sel:[0,0,0] op_sel_hi:[1,0,1]
	v_pk_fma_f32 v[198:199], v[162:163], v[28:29], v[198:199] op_sel:[0,1,0] op_sel_hi:[1,1,1]
	v_pk_fma_f32 v[200:201], v[164:165], v[28:29], v[200:201] op_sel:[0,1,0] op_sel_hi:[1,1,1]
	v_pk_fma_f32 v[202:203], v[166:167], v[28:29], v[202:203] op_sel:[0,1,0] op_sel_hi:[1,1,1]
	v_pk_fma_f32 v[204:205], v[168:169], v[28:29], v[204:205] op_sel:[0,1,0] op_sel_hi:[1,1,1]
	v_pk_fma_f32 v[198:199], v[102:103], v[30:31], v[198:199] op_sel:[0,0,0] op_sel_hi:[1,0,1]
	v_pk_fma_f32 v[200:201], v[104:105], v[30:31], v[200:201] op_sel:[0,0,0] op_sel_hi:[1,0,1]
	v_pk_fma_f32 v[202:203], v[106:107], v[30:31], v[202:203] op_sel:[0,0,0] op_sel_hi:[1,0,1]
	v_pk_fma_f32 v[204:205], v[108:109], v[30:31], v[204:205] op_sel:[0,0,0] op_sel_hi:[1,0,1]
	v_pk_fma_f32 v[198:199], v[164:165], v[46:47], v[198:199] op_sel:[0,0,0] op_sel_hi:[1,0,1]
	v_pk_fma_f32 v[200:201], v[166:167], v[46:47], v[200:201] op_sel:[0,0,0] op_sel_hi:[1,0,1]
	v_pk_fma_f32 v[202:203], v[168:169], v[46:47], v[202:203] op_sel:[0,0,0] op_sel_hi:[1,0,1]
	v_pk_fma_f32 v[204:205], v[170:171], v[46:47], v[204:205] op_sel:[0,0,0] op_sel_hi:[1,0,1]
	v_pk_fma_f32 v[198:199], v[104:105], v[30:31], v[198:199] op_sel:[0,1,0] op_sel_hi:[1,1,1]
	v_pk_fma_f32 v[200:201], v[106:107], v[30:31], v[200:201] op_sel:[0,1,0] op_sel_hi:[1,1,1]
	v_pk_fma_f32 v[202:203], v[108:109], v[30:31], v[202:203] op_sel:[0,1,0] op_sel_hi:[1,1,1]
	v_pk_fma_f32 v[204:205], v[110:111], v[30:31], v[204:205] op_sel:[0,1,0] op_sel_hi:[1,1,1]
	v_pk_fma_f32 v[198:199], v[166:167], v[32:33], v[198:199] op_sel:[0,0,0] op_sel_hi:[1,0,1]
	v_pk_fma_f32 v[200:201], v[168:169], v[32:33], v[200:201] op_sel:[0,0,0] op_sel_hi:[1,0,1]
	v_pk_fma_f32 v[202:203], v[170:171], v[32:33], v[202:203] op_sel:[0,0,0] op_sel_hi:[1,0,1]
	v_pk_fma_f32 v[204:205], v[172:173], v[32:33], v[204:205] op_sel:[0,0,0] op_sel_hi:[1,0,1]
	v_pk_fma_f32 v[198:199], v[106:107], v[32:33], v[198:199] op_sel:[0,1,0] op_sel_hi:[1,1,1]
	v_pk_fma_f32 v[200:201], v[108:109], v[32:33], v[200:201] op_sel:[0,1,0] op_sel_hi:[1,1,1]
	v_pk_fma_f32 v[202:203], v[110:111], v[32:33], v[202:203] op_sel:[0,1,0] op_sel_hi:[1,1,1]
	v_pk_fma_f32 v[204:205], v[112:113], v[32:33], v[204:205] op_sel:[0,1,0] op_sel_hi:[1,1,1]
	v_pk_fma_f32 v[198:199], v[168:169], v[46:47], v[198:199] op_sel:[0,1,0] op_sel_hi:[1,1,1]
; __device__ __forceinline__ void conv_phase(LAS unsigned char* lds, int tile, int tid, const bf16* __restrict__ U, const float* __restrict__ cw, const float* __restrict__ cb, ...
;     ...
;             for (int tk = 0; tk < HT; ++tk) { float a = bias;
; #pragma unroll
;                 for (int j = 0; j < CKW; ++j) a += w[j] * uc[tk + j];
;                 obuf[tk * CH + tid] = a; }
	v_pk_fma_f32 v[200:201], v[170:171], v[46:47], v[200:201] op_sel:[0,1,0] op_sel_hi:[1,1,1]
	v_pk_fma_f32 v[202:203], v[172:173], v[46:47], v[202:203] op_sel:[0,1,0] op_sel_hi:[1,1,1]
	v_pk_fma_f32 v[204:205], v[174:175], v[46:47], v[204:205] op_sel:[0,1,0] op_sel_hi:[1,1,1]
	v_pk_fma_f32 v[198:199], v[108:109], v[34:35], v[198:199] op_sel:[0,0,0] op_sel_hi:[1,0,1]
	v_pk_fma_f32 v[200:201], v[110:111], v[34:35], v[200:201] op_sel:[0,0,0] op_sel_hi:[1,0,1]
	v_pk_fma_f32 v[202:203], v[112:113], v[34:35], v[202:203] op_sel:[0,0,0] op_sel_hi:[1,0,1]
	v_pk_fma_f32 v[204:205], v[114:115], v[34:35], v[204:205] op_sel:[0,0,0] op_sel_hi:[1,0,1]
	v_pk_fma_f32 v[198:199], v[170:171], v[34:35], v[198:199] op_sel:[0,1,0] op_sel_hi:[1,1,1]
	v_pk_fma_f32 v[200:201], v[172:173], v[34:35], v[200:201] op_sel:[0,1,0] op_sel_hi:[1,1,1]
	v_pk_fma_f32 v[202:203], v[174:175], v[34:35], v[202:203] op_sel:[0,1,0] op_sel_hi:[1,1,1]
	v_pk_fma_f32 v[204:205], v[176:177], v[34:35], v[204:205] op_sel:[0,1,0] op_sel_hi:[1,1,1]
	v_pk_fma_f32 v[198:199], v[110:111], v[36:37], v[198:199] op_sel:[0,0,0] op_sel_hi:[1,0,1]
	v_pk_fma_f32 v[200:201], v[112:113], v[36:37], v[200:201] op_sel:[0,0,0] op_sel_hi:[1,0,1]
	v_pk_fma_f32 v[202:203], v[114:115], v[36:37], v[202:203] op_sel:[0,0,0] op_sel_hi:[1,0,1]
	v_pk_fma_f32 v[204:205], v[116:117], v[36:37], v[204:205] op_sel:[0,0,0] op_sel_hi:[1,0,1]
	v_pk_fma_f32 v[198:199], v[172:173], v[48:49], v[198:199] op_sel:[0,0,0] op_sel_hi:[1,0,1]
	v_pk_fma_f32 v[200:201], v[174:175], v[48:49], v[200:201] op_sel:[0,0,0] op_sel_hi:[1,0,1]
	v_pk_fma_f32 v[202:203], v[176:177], v[48:49], v[202:203] op_sel:[0,0,0] op_sel_hi:[1,0,1]
	v_pk_fma_f32 v[204:205], v[178:179], v[48:49], v[204:205] op_sel:[0,0,0] op_sel_hi:[1,0,1]
	v_pk_fma_f32 v[198:199], v[112:113], v[36:37], v[198:199] op_sel:[0,1,0] op_sel_hi:[1,1,1]
	v_pk_fma_f32 v[200:201], v[114:115], v[36:37], v[200:201] op_sel:[0,1,0] op_sel_hi:[1,1,1]
	v_pk_fma_f32 v[202:203], v[116:117], v[36:37], v[202:203] op_sel:[0,1,0] op_sel_hi:[1,1,1]
	v_pk_fma_f32 v[204:205], v[118:119], v[36:37], v[204:205] op_sel:[0,1,0] op_sel_hi:[1,1,1]
	v_pk_fma_f32 v[198:199], v[174:175], v[38:39], v[198:199] op_sel:[0,0,0] op_sel_hi:[1,0,1]
	v_pk_fma_f32 v[200:201], v[176:177], v[38:39], v[200:201] op_sel:[0,0,0] op_sel_hi:[1,0,1]
	v_pk_fma_f32 v[202:203], v[178:179], v[38:39], v[202:203] op_sel:[0,0,0] op_sel_hi:[1,0,1]
	v_pk_fma_f32 v[204:205], v[180:181], v[38:39], v[204:205] op_sel:[0,0,0] op_sel_hi:[1,0,1]
	v_pk_fma_f32 v[198:199], v[114:115], v[38:39], v[198:199] op_sel:[0,1,0] op_sel_hi:[1,1,1]
	v_pk_fma_f32 v[200:201], v[116:117], v[38:39], v[200:201] op_sel:[0,1,0] op_sel_hi:[1,1,1]
	v_pk_fma_f32 v[202:203], v[118:119], v[38:39], v[202:203] op_sel:[0,1,0] op_sel_hi:[1,1,1]
	v_pk_fma_f32 v[204:205], v[120:121], v[38:39], v[204:205] op_sel:[0,1,0] op_sel_hi:[1,1,1]
	v_pk_fma_f32 v[198:199], v[176:177], v[48:49], v[198:199] op_sel:[0,1,0] op_sel_hi:[1,1,1]
	v_pk_fma_f32 v[200:201], v[178:179], v[48:49], v[200:201] op_sel:[0,1,0] op_sel_hi:[1,1,1]
	v_pk_fma_f32 v[202:203], v[180:181], v[48:49], v[202:203] op_sel:[0,1,0] op_sel_hi:[1,1,1]
	v_pk_fma_f32 v[204:205], v[182:183], v[48:49], v[204:205] op_sel:[0,1,0] op_sel_hi:[1,1,1]
	v_pk_fma_f32 v[198:199], v[116:117], v[40:41], v[198:199] op_sel:[0,0,0] op_sel_hi:[1,0,1]
	v_pk_fma_f32 v[200:201], v[118:119], v[40:41], v[200:201] op_sel:[0,0,0] op_sel_hi:[1,0,1]
	v_pk_fma_f32 v[202:203], v[120:121], v[40:41], v[202:203] op_sel:[0,0,0] op_sel_hi:[1,0,1]
	v_pk_fma_f32 v[204:205], v[122:123], v[40:41], v[204:205] op_sel:[0,0,0] op_sel_hi:[1,0,1]
	v_pk_fma_f32 v[198:199], v[178:179], v[40:41], v[198:199] op_sel:[0,1,0] op_sel_hi:[1,1,1]
	v_pk_fma_f32 v[200:201], v[180:181], v[40:41], v[200:201] op_sel:[0,1,0] op_sel_hi:[1,1,1]
	v_pk_fma_f32 v[202:203], v[182:183], v[40:41], v[202:203] op_sel:[0,1,0] op_sel_hi:[1,1,1]
; __device__ __forceinline__ void conv_phase(LAS unsigned char* lds, int tile, int tid, const bf16* __restrict__ U, const float* __restrict__ cw, const float* __restrict__ cb, ...
;     ...
;             for (int r = 0; r < UROWS; ++r) uc[r] = __uint_as_float((unsigned)ubuf[r * CH + tid] << 16);
; #pragma unroll
;             for (int tk = 0; tk < HT; ++tk) { float a = bias;
; #pragma unroll
;                 for (int j = 0; j < CKW; ++j) a += w[j] * uc[tk + j];
;                 obuf[tk * CH + tid] = a; }
	v_pk_fma_f32 v[204:205], v[184:185], v[40:41], v[204:205] op_sel:[0,1,0] op_sel_hi:[1,1,1]
	v_pk_fma_f32 v[198:199], v[118:119], v[42:43], v[198:199] op_sel:[0,0,0] op_sel_hi:[1,0,1]
	v_pk_fma_f32 v[200:201], v[120:121], v[42:43], v[200:201] op_sel:[0,0,0] op_sel_hi:[1,0,1]
	v_pk_fma_f32 v[202:203], v[122:123], v[42:43], v[202:203] op_sel:[0,0,0] op_sel_hi:[1,0,1]
	v_pk_fma_f32 v[204:205], v[124:125], v[42:43], v[204:205] op_sel:[0,0,0] op_sel_hi:[1,0,1]
	v_pk_fma_f32 v[198:199], v[180:181], v[50:51], v[198:199] op_sel:[0,0,0] op_sel_hi:[1,0,1]
	v_pk_fma_f32 v[200:201], v[182:183], v[50:51], v[200:201] op_sel:[0,0,0] op_sel_hi:[1,0,1]
	v_pk_fma_f32 v[202:203], v[184:185], v[50:51], v[202:203] op_sel:[0,0,0] op_sel_hi:[1,0,1]
	v_pk_fma_f32 v[204:205], v[186:187], v[50:51], v[204:205] op_sel:[0,0,0] op_sel_hi:[1,0,1]
	v_pk_fma_f32 v[198:199], v[120:121], v[50:51], v[198:199] op_sel:[0,1,0] op_sel_hi:[1,1,1]
	v_pk_fma_f32 v[200:201], v[122:123], v[50:51], v[200:201] op_sel:[0,1,0] op_sel_hi:[1,1,1]
	v_pk_fma_f32 v[202:203], v[124:125], v[50:51], v[202:203] op_sel:[0,1,0] op_sel_hi:[1,1,1]
	v_pk_fma_f32 v[204:205], v[126:127], v[50:51], v[204:205] op_sel:[0,1,0] op_sel_hi:[1,1,1]
	v_pk_fma_f32 v[198:199], v[182:183], v[52:53], v[198:199] op_sel:[0,0,0] op_sel_hi:[1,0,1]
	v_pk_fma_f32 v[200:201], v[184:185], v[52:53], v[200:201] op_sel:[0,0,0] op_sel_hi:[1,0,1]
	v_pk_fma_f32 v[202:203], v[186:187], v[52:53], v[202:203] op_sel:[0,0,0] op_sel_hi:[1,0,1]
	v_pk_fma_f32 v[204:205], v[188:189], v[52:53], v[204:205] op_sel:[0,0,0] op_sel_hi:[1,0,1]
	v_pk_fma_f32 v[198:199], v[122:123], v[52:53], v[198:199] op_sel:[0,1,0] op_sel_hi:[1,1,1]
	v_pk_fma_f32 v[200:201], v[124:125], v[52:53], v[200:201] op_sel:[0,1,0] op_sel_hi:[1,1,1]
	v_pk_fma_f32 v[202:203], v[126:127], v[52:53], v[202:203] op_sel:[0,1,0] op_sel_hi:[1,1,1]
	v_pk_fma_f32 v[204:205], v[128:129], v[52:53], v[204:205] op_sel:[0,1,0] op_sel_hi:[1,1,1]
	v_pk_fma_f32 v[198:199], v[184:185], v[56:57], v[198:199] op_sel:[0,0,0] op_sel_hi:[1,0,1]
	v_pk_fma_f32 v[200:201], v[186:187], v[56:57], v[200:201] op_sel:[0,0,0] op_sel_hi:[1,0,1]
	v_pk_fma_f32 v[202:203], v[188:189], v[56:57], v[202:203] op_sel:[0,0,0] op_sel_hi:[1,0,1]
	v_pk_fma_f32 v[204:205], v[190:191], v[56:57], v[204:205] op_sel:[0,0,0] op_sel_hi:[1,0,1]
	v_pk_fma_f32 v[198:199], v[124:125], v[54:55], v[198:199] op_sel:[0,0,0] op_sel_hi:[1,0,1]
	v_pk_fma_f32 v[200:201], v[126:127], v[54:55], v[200:201] op_sel:[0,0,0] op_sel_hi:[1,0,1]
	v_pk_fma_f32 v[202:203], v[128:129], v[54:55], v[202:203] op_sel:[0,0,0] op_sel_hi:[1,0,1]
	v_pk_fma_f32 v[204:205], v[130:131], v[54:55], v[204:205] op_sel:[0,0,0] op_sel_hi:[1,0,1]
	v_pk_fma_f32 v[198:199], v[186:187], v[54:55], v[198:199] op_sel:[0,1,0] op_sel_hi:[1,1,1]
	v_pk_fma_f32 v[200:201], v[188:189], v[54:55], v[200:201] op_sel:[0,1,0] op_sel_hi:[1,1,1]
	v_pk_fma_f32 v[202:203], v[190:191], v[54:55], v[202:203] op_sel:[0,1,0] op_sel_hi:[1,1,1]
	v_pk_fma_f32 v[204:205], v[192:193], v[54:55], v[204:205] op_sel:[0,1,0] op_sel_hi:[1,1,1]
	v_pk_fma_f32 v[198:199], v[126:127], v[56:57], v[198:199] op_sel:[0,1,0] op_sel_hi:[1,1,1]
	v_pk_fma_f32 v[200:201], v[128:129], v[56:57], v[200:201] op_sel:[0,1,0] op_sel_hi:[1,1,1]
	v_pk_fma_f32 v[202:203], v[130:131], v[56:57], v[202:203] op_sel:[0,1,0] op_sel_hi:[1,1,1]
	v_pk_fma_f32 v[204:205], v[132:133], v[56:57], v[204:205] op_sel:[0,1,0] op_sel_hi:[1,1,1]
	ds_write2st64_b32 v66, v198, v199 offset0:192 offset1:200
	ds_write2st64_b32 v66, v200, v201 offset0:208 offset1:216
	ds_write2st64_b32 v66, v202, v203 offset0:224 offset1:232
	ds_write2st64_b32 v66, v204, v205 offset0:240 offset1:248
	v_add_u32_e32 v6, s21, v68
	v_ashrrev_i32_e32 v7, 31, v6
	v_lshlrev_b64 v[6:7], 11, v[6:7]
	s_xor_b64 s[10:11], s[6:7], -1
	v_lshl_add_u64 v[6:7], v[2:3], 0, v[6:7]
	s_mov_b32 s12, 0
	s_waitcnt lgkmcnt(0)
	s_barrier

.LBB0_956:
	s_and_b32 s8, s3, 0x78
	s_add_i32 s8, s8, s4
	s_ashr_i32 s9, s8, 31
	s_lshl_b64 s[10:11], s[8:9], 15
	s_add_u32 s10, s12, s10
	s_addc_u32 s11, s13, s11
	s_and_b32 s17, s16, 0x1000
	s_lshl_b32 s17, s17, 2
	s_add_u32 s10, s10, s17
	s_addc_u32 s11, s11, 0
	v_lshl_add_u64 v[54:55], s[10:11], 0, v[2:3]
	v_lshl_add_u64 v[126:127], v[54:55], 0, s[6:7]
	v_add_co_u32_e32 v128, vcc, s14, v54
	s_mov_b32 s17, s18
	s_nop 0
	v_addc_co_u32_e32 v129, vcc, 0, v55, vcc
	global_load_dword v104, v[126:127], off offset:256
	global_load_dword v106, v[126:127], off offset:512
	global_load_dword v108, v[126:127], off offset:768
	global_load_dword v110, v[126:127], off offset:1024
	global_load_dword v112, v[126:127], off offset:1280
	global_load_dword v114, v[126:127], off offset:1536
	global_load_dword v98, v[126:127], off offset:1792
	global_load_dword v100, v[126:127], off offset:2048
	global_load_dword v116, v[128:129], off offset:-4096
	global_load_dword v102, v[126:127], off offset:2304
	global_load_dword v78, v[126:127], off offset:2560
	global_load_dword v80, v[126:127], off offset:2816
	global_load_dword v82, v[126:127], off offset:3072
	global_load_dword v84, v[126:127], off offset:3328
	global_load_dword v86, v[126:127], off offset:3584
	global_load_dword v88, v[126:127], off offset:3840
	global_load_dword v90, v[128:129], off
	global_load_dword v92, v[128:129], off offset:256
	global_load_dword v94, v[128:129], off offset:512
	global_load_dword v96, v[128:129], off offset:768
	global_load_dword v76, v[128:129], off offset:1024
	global_load_dword v77, v[128:129], off offset:1280
	global_load_dword v56, v[128:129], off offset:1536
	global_load_dword v57, v[128:129], off offset:1792
	global_load_dword v58, v[128:129], off offset:2048
	global_load_dword v59, v[128:129], off offset:2304
	global_load_dword v60, v[128:129], off offset:2560
	global_load_dword v61, v[128:129], off offset:2816
	global_load_dword v62, v[128:129], off offset:3072
	global_load_dword v63, v[128:129], off offset:3328
	global_load_dword v54, v[128:129], off offset:3584
	global_load_dword v55, v[128:129], off offset:3840
	s_waitcnt vmcnt(56)
	v_and_b32_e32 v9, 0x1fff8, v64
	v_and_b32_e32 v11, 0x1fff8, v66
	v_and_b32_e32 v13, 0x1fff8, v68
	v_and_b32_e32 v15, 0x1fff8, v70
	ds_read_b64 v[126:127], v9
	ds_read_b64 v[128:129], v11
	ds_read_b64 v[130:131], v13
	ds_read_b64 v[132:133], v15
	v_and_b32_e32 v9, 0x1fff8, v72
	v_and_b32_e32 v11, 0x1fff8, v74
	v_and_b32_e32 v13, 0x1fff8, v48
	v_and_b32_e32 v15, 0x1fff8, v50
	ds_read_b64 v[134:135], v9
	ds_read_b64 v[136:137], v11
	ds_read_b64 v[138:139], v13
	ds_read_b64 v[140:141], v15
	s_setprio 1
	s_waitcnt lgkmcnt(7)
	v_cvt_pk_f32_fp8_e32 v[142:143], v126
	v_cvt_pk_f32_fp8_sdwa v[144:145], v126 src0_sel:WORD_1
	v_cvt_pk_f32_fp8_e32 v[146:147], v127
	v_cvt_pk_f32_fp8_sdwa v[126:127], v127 src0_sel:WORD_1
	s_waitcnt lgkmcnt(6)
	v_cvt_pk_f32_fp8_e32 v[148:149], v128
	v_cvt_pk_f32_fp8_sdwa v[150:151], v128 src0_sel:WORD_1
	v_cvt_pk_f32_fp8_e32 v[152:153], v129
	v_cvt_pk_f32_fp8_sdwa v[128:129], v129 src0_sel:WORD_1
	s_waitcnt lgkmcnt(5)
	v_cvt_pk_f32_fp8_e32 v[154:155], v130
	v_cvt_pk_f32_fp8_sdwa v[156:157], v130 src0_sel:WORD_1
	v_cvt_pk_f32_fp8_e32 v[158:159], v131
	v_cvt_pk_f32_fp8_sdwa v[130:131], v131 src0_sel:WORD_1
	s_waitcnt lgkmcnt(4)
	v_cvt_pk_f32_fp8_e32 v[160:161], v132
	v_cvt_pk_f32_fp8_sdwa v[162:163], v132 src0_sel:WORD_1
	v_cvt_pk_f32_fp8_e32 v[164:165], v133
	v_cvt_pk_f32_fp8_sdwa v[132:133], v133 src0_sel:WORD_1
	s_waitcnt lgkmcnt(3)
	v_cvt_pk_f32_fp8_e32 v[166:167], v134
	v_cvt_pk_f32_fp8_sdwa v[168:169], v134 src0_sel:WORD_1
	v_cvt_pk_f32_fp8_e32 v[170:171], v135
	v_cvt_pk_f32_fp8_sdwa v[134:135], v135 src0_sel:WORD_1
	s_waitcnt lgkmcnt(2)
	v_cvt_pk_f32_fp8_e32 v[172:173], v136
	v_cvt_pk_f32_fp8_sdwa v[174:175], v136 src0_sel:WORD_1
	v_cvt_pk_f32_fp8_e32 v[176:177], v137
	v_cvt_pk_f32_fp8_sdwa v[136:137], v137 src0_sel:WORD_1
	s_waitcnt lgkmcnt(1)
	v_cvt_pk_f32_fp8_e32 v[178:179], v138
	v_cvt_pk_f32_fp8_sdwa v[180:181], v138 src0_sel:WORD_1
	v_cvt_pk_f32_fp8_e32 v[182:183], v139
	v_cvt_pk_f32_fp8_sdwa v[138:139], v139 src0_sel:WORD_1
	s_waitcnt lgkmcnt(0)
	v_cvt_pk_f32_fp8_e32 v[184:185], v140
	v_cvt_pk_f32_fp8_sdwa v[186:187], v140 src0_sel:WORD_1
	v_cvt_pk_f32_fp8_e32 v[188:189], v141
	v_cvt_pk_f32_fp8_sdwa v[140:141], v141 src0_sel:WORD_1
	s_setprio 0
	s_waitcnt vmcnt(48)
	v_and_b32_e32 v9, 0x1fff8, v52
	v_and_b32_e32 v11, 0x1fff8, v32
	v_and_b32_e32 v13, 0x1fff8, v34
	v_and_b32_e32 v15, 0x1fff8, v36
	ds_read_b64 v[190:191], v9
	ds_read_b64 v[192:193], v11
	ds_read_b64 v[194:195], v13
	ds_read_b64 v[196:197], v15
	v_and_b32_e32 v9, 0x1fff8, v38
	v_and_b32_e32 v11, 0x1fff8, v40
	v_and_b32_e32 v13, 0x1fff8, v42
	v_and_b32_e32 v15, 0x1fff8, v44
	ds_read_b64 v[198:199], v9
	ds_read_b64 v[200:201], v11
	ds_read_b64 v[202:203], v13
	ds_read_b64 v[204:205], v15
	s_setprio 1
	v_pk_fma_f32 v[118:119], v[142:143], v[64:65], v[118:119] op_sel_hi:[1,0,1]
	v_pk_fma_f32 v[122:123], v[144:145], v[64:65], v[122:123] op_sel_hi:[1,0,1]
	v_pk_fma_f32 v[120:121], v[146:147], v[64:65], v[120:121] op_sel_hi:[1,0,1]
	v_pk_fma_f32 v[64:65], v[126:127], v[64:65], v[124:125] op_sel_hi:[1,0,1]
	v_pk_fma_f32 v[118:119], v[148:149], v[66:67], v[118:119] op_sel_hi:[1,0,1]
	v_pk_fma_f32 v[122:123], v[150:151], v[66:67], v[122:123] op_sel_hi:[1,0,1]
	v_pk_fma_f32 v[120:121], v[152:153], v[66:67], v[120:121] op_sel_hi:[1,0,1]
	v_pk_fma_f32 v[64:65], v[128:129], v[66:67], v[64:65] op_sel_hi:[1,0,1]
	v_pk_fma_f32 v[118:119], v[154:155], v[68:69], v[118:119] op_sel_hi:[1,0,1]
	v_pk_fma_f32 v[122:123], v[156:157], v[68:69], v[122:123] op_sel_hi:[1,0,1]
	v_pk_fma_f32 v[120:121], v[158:159], v[68:69], v[120:121] op_sel_hi:[1,0,1]
	v_pk_fma_f32 v[64:65], v[130:131], v[68:69], v[64:65] op_sel_hi:[1,0,1]
	v_pk_fma_f32 v[118:119], v[160:161], v[70:71], v[118:119] op_sel_hi:[1,0,1]
	v_pk_fma_f32 v[122:123], v[162:163], v[70:71], v[122:123] op_sel_hi:[1,0,1]
	v_pk_fma_f32 v[120:121], v[164:165], v[70:71], v[120:121] op_sel_hi:[1,0,1]
	v_pk_fma_f32 v[64:65], v[132:133], v[70:71], v[64:65] op_sel_hi:[1,0,1]
	s_waitcnt lgkmcnt(7)
	v_cvt_pk_f32_fp8_e32 v[206:207], v190
	v_cvt_pk_f32_fp8_sdwa v[208:209], v190 src0_sel:WORD_1
	v_cvt_pk_f32_fp8_e32 v[210:211], v191
	v_cvt_pk_f32_fp8_sdwa v[190:191], v191 src0_sel:WORD_1
	v_pk_fma_f32 v[118:119], v[166:167], v[72:73], v[118:119] op_sel_hi:[1,0,1]
	v_pk_fma_f32 v[122:123], v[168:169], v[72:73], v[122:123] op_sel_hi:[1,0,1]
	v_pk_fma_f32 v[120:121], v[170:171], v[72:73], v[120:121] op_sel_hi:[1,0,1]
	v_pk_fma_f32 v[64:65], v[134:135], v[72:73], v[64:65] op_sel_hi:[1,0,1]
	v_pk_fma_f32 v[118:119], v[172:173], v[74:75], v[118:119] op_sel_hi:[1,0,1]
	v_pk_fma_f32 v[122:123], v[174:175], v[74:75], v[122:123] op_sel_hi:[1,0,1]
	v_pk_fma_f32 v[120:121], v[176:177], v[74:75], v[120:121] op_sel_hi:[1,0,1]
	v_pk_fma_f32 v[64:65], v[136:137], v[74:75], v[64:65] op_sel_hi:[1,0,1]
	s_waitcnt lgkmcnt(6)
	v_cvt_pk_f32_fp8_e32 v[66:67], v192
	v_cvt_pk_f32_fp8_sdwa v[68:69], v192 src0_sel:WORD_1
	v_cvt_pk_f32_fp8_e32 v[70:71], v193
	v_cvt_pk_f32_fp8_sdwa v[72:73], v193 src0_sel:WORD_1
	s_waitcnt lgkmcnt(5)
	v_cvt_pk_f32_fp8_e32 v[74:75], v194
	v_cvt_pk_f32_fp8_sdwa v[124:125], v194 src0_sel:WORD_1
	v_pk_fma_f32 v[118:119], v[178:179], v[48:49], v[118:119] op_sel_hi:[1,0,1]
	v_pk_fma_f32 v[122:123], v[180:181], v[48:49], v[122:123] op_sel_hi:[1,0,1]
	v_pk_fma_f32 v[120:121], v[182:183], v[48:49], v[120:121] op_sel_hi:[1,0,1]
	v_pk_fma_f32 v[48:49], v[138:139], v[48:49], v[64:65] op_sel_hi:[1,0,1]
	v_pk_fma_f32 v[118:119], v[184:185], v[50:51], v[118:119] op_sel_hi:[1,0,1]
	v_pk_fma_f32 v[122:123], v[186:187], v[50:51], v[122:123] op_sel_hi:[1,0,1]
	v_pk_fma_f32 v[120:121], v[188:189], v[50:51], v[120:121] op_sel_hi:[1,0,1]
	v_pk_fma_f32 v[48:49], v[140:141], v[50:51], v[48:49] op_sel_hi:[1,0,1]
	v_pk_fma_f32 v[118:119], v[206:207], v[52:53], v[118:119] op_sel_hi:[1,0,1]
	v_pk_fma_f32 v[122:123], v[208:209], v[52:53], v[122:123] op_sel_hi:[1,0,1]
	v_pk_fma_f32 v[120:121], v[210:211], v[52:53], v[120:121] op_sel_hi:[1,0,1]
	v_pk_fma_f32 v[48:49], v[190:191], v[52:53], v[48:49] op_sel_hi:[1,0,1]
	v_cvt_pk_f32_fp8_e32 v[126:127], v195
	v_cvt_pk_f32_fp8_sdwa v[128:129], v195 src0_sel:WORD_1
	s_waitcnt lgkmcnt(4)
	v_cvt_pk_f32_fp8_e32 v[130:131], v196
	v_cvt_pk_f32_fp8_sdwa v[132:133], v196 src0_sel:WORD_1
	v_cvt_pk_f32_fp8_e32 v[134:135], v197
	v_cvt_pk_f32_fp8_sdwa v[136:137], v197 src0_sel:WORD_1
	s_waitcnt lgkmcnt(3)
	v_cvt_pk_f32_fp8_e32 v[142:143], v198
	v_cvt_pk_f32_fp8_sdwa v[144:145], v198 src0_sel:WORD_1
	v_cvt_pk_f32_fp8_e32 v[146:147], v199
	v_cvt_pk_f32_fp8_sdwa v[148:149], v199 src0_sel:WORD_1
	s_waitcnt lgkmcnt(2)
	v_cvt_pk_f32_fp8_e32 v[150:151], v200
	v_cvt_pk_f32_fp8_sdwa v[152:153], v200 src0_sel:WORD_1
	v_cvt_pk_f32_fp8_e32 v[154:155], v201
	v_cvt_pk_f32_fp8_sdwa v[156:157], v201 src0_sel:WORD_1
	s_waitcnt lgkmcnt(1)
	v_cvt_pk_f32_fp8_e32 v[158:159], v202
	v_cvt_pk_f32_fp8_sdwa v[160:161], v202 src0_sel:WORD_1
	v_cvt_pk_f32_fp8_e32 v[162:163], v203
	v_cvt_pk_f32_fp8_sdwa v[164:165], v203 src0_sel:WORD_1
	s_waitcnt lgkmcnt(0)
	v_cvt_pk_f32_fp8_e32 v[166:167], v204
	v_cvt_pk_f32_fp8_sdwa v[168:169], v204 src0_sel:WORD_1
	v_cvt_pk_f32_fp8_e32 v[170:171], v205
	v_cvt_pk_f32_fp8_sdwa v[172:173], v205 src0_sel:WORD_1
	s_setprio 0
	s_waitcnt vmcnt(40)
	v_and_b32_e32 v9, 0x1fff8, v46
	v_and_b32_e32 v11, 0x1fff8, v26
	v_and_b32_e32 v13, 0x1fff8, v28
	v_and_b32_e32 v15, 0x1fff8, v30
	ds_read_b64 v[50:51], v9
	ds_read_b64 v[52:53], v11
	ds_read_b64 v[64:65], v13
	ds_read_b64 v[138:139], v15
	v_and_b32_e32 v9, 0x1fff8, v4
	v_and_b32_e32 v11, 0x1fff8, v6
	v_and_b32_e32 v13, 0x1fff8, v8
	v_and_b32_e32 v15, 0x1fff8, v10
	ds_read_b64 v[140:141], v9
	ds_read_b64 v[174:175], v11
	ds_read_b64 v[176:177], v13
	ds_read_b64 v[178:179], v15
	s_setprio 1
	v_pk_fma_f32 v[66:67], v[66:67], v[32:33], v[118:119] op_sel_hi:[1,0,1]
	v_pk_fma_f32 v[68:69], v[68:69], v[32:33], v[122:123] op_sel_hi:[1,0,1]
	v_pk_fma_f32 v[70:71], v[70:71], v[32:33], v[120:121] op_sel_hi:[1,0,1]
	v_pk_fma_f32 v[32:33], v[72:73], v[32:33], v[48:49] op_sel_hi:[1,0,1]
	v_pk_fma_f32 v[66:67], v[74:75], v[34:35], v[66:67] op_sel_hi:[1,0,1]
	v_pk_fma_f32 v[68:69], v[124:125], v[34:35], v[68:69] op_sel_hi:[1,0,1]
	v_pk_fma_f32 v[70:71], v[126:127], v[34:35], v[70:71] op_sel_hi:[1,0,1]
	v_pk_fma_f32 v[32:33], v[128:129], v[34:35], v[32:33] op_sel_hi:[1,0,1]
	v_pk_fma_f32 v[66:67], v[130:131], v[36:37], v[66:67] op_sel_hi:[1,0,1]
	v_pk_fma_f32 v[68:69], v[132:133], v[36:37], v[68:69] op_sel_hi:[1,0,1]
	v_pk_fma_f32 v[70:71], v[134:135], v[36:37], v[70:71] op_sel_hi:[1,0,1]
	v_pk_fma_f32 v[32:33], v[136:137], v[36:37], v[32:33] op_sel_hi:[1,0,1]
	s_waitcnt lgkmcnt(7)
	v_cvt_pk_f32_fp8_e32 v[180:181], v50
	v_cvt_pk_f32_fp8_sdwa v[182:183], v50 src0_sel:WORD_1
	v_cvt_pk_f32_fp8_e32 v[184:185], v51
	v_cvt_pk_f32_fp8_sdwa v[50:51], v51 src0_sel:WORD_1
	v_pk_fma_f32 v[66:67], v[142:143], v[38:39], v[66:67] op_sel_hi:[1,0,1]
	v_pk_fma_f32 v[68:69], v[144:145], v[38:39], v[68:69] op_sel_hi:[1,0,1]
	v_pk_fma_f32 v[70:71], v[146:147], v[38:39], v[70:71] op_sel_hi:[1,0,1]
	v_pk_fma_f32 v[32:33], v[148:149], v[38:39], v[32:33] op_sel_hi:[1,0,1]
	s_waitcnt lgkmcnt(6)
	v_cvt_pk_f32_fp8_e32 v[186:187], v52
	v_cvt_pk_f32_fp8_sdwa v[188:189], v52 src0_sel:WORD_1
	v_cvt_pk_f32_fp8_e32 v[190:191], v53
	v_cvt_pk_f32_fp8_sdwa v[52:53], v53 src0_sel:WORD_1
	v_pk_fma_f32 v[66:67], v[150:151], v[40:41], v[66:67] op_sel_hi:[1,0,1]
	v_pk_fma_f32 v[68:69], v[152:153], v[40:41], v[68:69] op_sel_hi:[1,0,1]
	v_pk_fma_f32 v[70:71], v[154:155], v[40:41], v[70:71] op_sel_hi:[1,0,1]
	v_pk_fma_f32 v[32:33], v[156:157], v[40:41], v[32:33] op_sel_hi:[1,0,1]
	s_waitcnt lgkmcnt(5)
	v_cvt_pk_f32_fp8_e32 v[192:193], v64
	v_cvt_pk_f32_fp8_sdwa v[194:195], v64 src0_sel:WORD_1
	v_cvt_pk_f32_fp8_e32 v[196:197], v65
	v_cvt_pk_f32_fp8_sdwa v[64:65], v65 src0_sel:WORD_1
	v_pk_fma_f32 v[66:67], v[158:159], v[42:43], v[66:67] op_sel_hi:[1,0,1]
	v_pk_fma_f32 v[68:69], v[160:161], v[42:43], v[68:69] op_sel_hi:[1,0,1]
	v_pk_fma_f32 v[70:71], v[162:163], v[42:43], v[70:71] op_sel_hi:[1,0,1]
	v_pk_fma_f32 v[32:33], v[164:165], v[42:43], v[32:33] op_sel_hi:[1,0,1]
	s_waitcnt lgkmcnt(4)
	v_cvt_pk_f32_fp8_e32 v[198:199], v138
	v_cvt_pk_f32_fp8_sdwa v[200:201], v138 src0_sel:WORD_1
	v_cvt_pk_f32_fp8_e32 v[202:203], v139
	v_cvt_pk_f32_fp8_sdwa v[138:139], v139 src0_sel:WORD_1
	v_pk_fma_f32 v[66:67], v[166:167], v[44:45], v[66:67] op_sel_hi:[1,0,1]
	v_pk_fma_f32 v[68:69], v[168:169], v[44:45], v[68:69] op_sel_hi:[1,0,1]
	v_pk_fma_f32 v[70:71], v[170:171], v[44:45], v[70:71] op_sel_hi:[1,0,1]
	v_pk_fma_f32 v[32:33], v[172:173], v[44:45], v[32:33] op_sel_hi:[1,0,1]
	v_pk_fma_f32 v[66:67], v[180:181], v[46:47], v[66:67] op_sel_hi:[1,0,1]
	v_pk_fma_f32 v[68:69], v[182:183], v[46:47], v[68:69] op_sel_hi:[1,0,1]
	v_pk_fma_f32 v[70:71], v[184:185], v[46:47], v[70:71] op_sel_hi:[1,0,1]
	v_pk_fma_f32 v[32:33], v[50:51], v[46:47], v[32:33] op_sel_hi:[1,0,1]
	s_waitcnt lgkmcnt(3)
	v_cvt_pk_f32_fp8_e32 v[34:35], v140
	v_cvt_pk_f32_fp8_sdwa v[36:37], v140 src0_sel:WORD_1
	v_cvt_pk_f32_fp8_e32 v[38:39], v141
	v_cvt_pk_f32_fp8_sdwa v[40:41], v141 src0_sel:WORD_1
	s_waitcnt lgkmcnt(2)
	v_cvt_pk_f32_fp8_e32 v[42:43], v174
	v_cvt_pk_f32_fp8_sdwa v[44:45], v174 src0_sel:WORD_1
	v_cvt_pk_f32_fp8_e32 v[46:47], v175
	v_cvt_pk_f32_fp8_sdwa v[48:49], v175 src0_sel:WORD_1
	s_waitcnt lgkmcnt(1)
	v_cvt_pk_f32_fp8_e32 v[50:51], v176
	v_cvt_pk_f32_fp8_sdwa v[72:73], v176 src0_sel:WORD_1
	v_cvt_pk_f32_fp8_e32 v[74:75], v177
	v_cvt_pk_f32_fp8_sdwa v[118:119], v177 src0_sel:WORD_1
	s_waitcnt lgkmcnt(0)
	v_cvt_pk_f32_fp8_e32 v[120:121], v178
	v_cvt_pk_f32_fp8_sdwa v[122:123], v178 src0_sel:WORD_1
	v_cvt_pk_f32_fp8_e32 v[124:125], v179
	v_pk_fma_f32 v[66:67], v[186:187], v[26:27], v[66:67] op_sel_hi:[1,0,1]
	v_pk_fma_f32 v[68:69], v[188:189], v[26:27], v[68:69] op_sel_hi:[1,0,1]
	v_pk_fma_f32 v[70:71], v[190:191], v[26:27], v[70:71] op_sel_hi:[1,0,1]
	v_pk_fma_f32 v[26:27], v[52:53], v[26:27], v[32:33] op_sel_hi:[1,0,1]
	v_pk_fma_f32 v[66:67], v[192:193], v[28:29], v[66:67] op_sel_hi:[1,0,1]
	v_pk_fma_f32 v[68:69], v[194:195], v[28:29], v[68:69] op_sel_hi:[1,0,1]
	v_pk_fma_f32 v[70:71], v[196:197], v[28:29], v[70:71] op_sel_hi:[1,0,1]
	v_pk_fma_f32 v[26:27], v[64:65], v[28:29], v[26:27] op_sel_hi:[1,0,1]
	v_pk_fma_f32 v[66:67], v[198:199], v[30:31], v[66:67] op_sel_hi:[1,0,1]
	v_pk_fma_f32 v[68:69], v[200:201], v[30:31], v[68:69] op_sel_hi:[1,0,1]
	v_pk_fma_f32 v[70:71], v[202:203], v[30:31], v[70:71] op_sel_hi:[1,0,1]
	v_pk_fma_f32 v[26:27], v[138:139], v[30:31], v[26:27] op_sel_hi:[1,0,1]
	v_cvt_pk_f32_fp8_sdwa v[126:127], v179 src0_sel:WORD_1
	s_setprio 0
	s_waitcnt vmcnt(32)
	v_and_b32_e32 v9, 0x1fff8, v14
	v_and_b32_e32 v11, 0x1fff8, v18
	v_and_b32_e32 v13, 0x1fff8, v20
	v_and_b32_e32 v15, 0x1fff8, v22
	ds_read_b64 v[28:29], v9
	ds_read_b64 v[30:31], v11
	ds_read_b64 v[32:33], v13
	ds_read_b64 v[52:53], v15
	v_and_b32_e32 v9, 0x1fff8, v24
	v_and_b32_e32 v11, 0x1fff8, v12
	v_and_b32_e32 v13, 0x1fff8, v16
	v_and_b32_e32 v15, 0x1fff8, v7
	ds_read_b64 v[64:65], v9
	ds_read_b64 v[128:129], v11
	ds_read_b64 v[130:131], v13
	ds_read_b64 v[132:133], v15
	s_setprio 1
	s_waitcnt lgkmcnt(7)
	v_cvt_pk_f32_fp8_e32 v[134:135], v28
	v_pk_fma_f32 v[34:35], v[34:35], v[4:5], v[66:67] op_sel_hi:[1,0,1]
	s_waitcnt lgkmcnt(6)
	v_cvt_pk_f32_fp8_e32 v[140:141], v30
	v_pk_fma_f32 v[34:35], v[42:43], v[6:7], v[34:35] op_sel_hi:[1,0,1]
	s_waitcnt lgkmcnt(5)
	v_cvt_pk_f32_fp8_e32 v[146:147], v32
	v_pk_fma_f32 v[34:35], v[50:51], v[8:9], v[34:35] op_sel_hi:[1,0,1]
	s_waitcnt lgkmcnt(4)
	v_cvt_pk_f32_fp8_e32 v[152:153], v52
	v_pk_fma_f32 v[34:35], v[120:121], v[10:11], v[34:35] op_sel_hi:[1,0,1]
	s_waitcnt lgkmcnt(3)
	v_cvt_pk_f32_fp8_e32 v[158:159], v64
	v_pk_fma_f32 v[34:35], v[134:135], v[14:15], v[34:35] op_sel_hi:[1,0,1]
	s_waitcnt lgkmcnt(2)
	v_cvt_pk_f32_fp8_e32 v[164:165], v128
	v_pk_fma_f32 v[34:35], v[140:141], v[18:19], v[34:35] op_sel_hi:[1,0,1]
	s_waitcnt lgkmcnt(1)
	v_cvt_pk_f32_fp8_e32 v[170:171], v130
	v_pk_fma_f32 v[34:35], v[146:147], v[20:21], v[34:35] op_sel_hi:[1,0,1]
	v_cvt_pk_f32_fp8_sdwa v[136:137], v28 src0_sel:WORD_1
	v_pk_fma_f32 v[34:35], v[152:153], v[22:23], v[34:35] op_sel_hi:[1,0,1]
	v_cvt_pk_f32_fp8_sdwa v[142:143], v30 src0_sel:WORD_1
	v_pk_fma_f32 v[34:35], v[158:159], v[24:25], v[34:35] op_sel_hi:[1,0,1]
	v_cvt_pk_f32_fp8_sdwa v[148:149], v32 src0_sel:WORD_1
	v_pk_fma_f32 v[34:35], v[164:165], v[12:13], v[34:35] op_sel_hi:[1,0,1]
	v_cvt_pk_f32_fp8_sdwa v[154:155], v52 src0_sel:WORD_1
	v_pk_fma_f32 v[120:121], v[170:171], v[16:17], v[34:35] op_sel_hi:[1,0,1]
	v_pk_fma_f32 v[34:35], v[36:37], v[4:5], v[68:69] op_sel_hi:[1,0,1]
	v_cvt_pk_f32_fp8_sdwa v[160:161], v64 src0_sel:WORD_1
	v_pk_fma_f32 v[34:35], v[44:45], v[6:7], v[34:35] op_sel_hi:[1,0,1]
	v_cvt_pk_f32_fp8_sdwa v[166:167], v128 src0_sel:WORD_1
	v_pk_fma_f32 v[34:35], v[72:73], v[8:9], v[34:35] op_sel_hi:[1,0,1]
	v_cvt_pk_f32_fp8_sdwa v[172:173], v130 src0_sel:WORD_1
	v_pk_fma_f32 v[34:35], v[122:123], v[10:11], v[34:35] op_sel_hi:[1,0,1]
	v_cvt_pk_f32_fp8_e32 v[138:139], v29
	v_pk_fma_f32 v[34:35], v[136:137], v[14:15], v[34:35] op_sel_hi:[1,0,1]
	v_cvt_pk_f32_fp8_sdwa v[28:29], v29 src0_sel:WORD_1
	v_pk_fma_f32 v[34:35], v[142:143], v[18:19], v[34:35] op_sel_hi:[1,0,1]
	v_cvt_pk_f32_fp8_e32 v[144:145], v31
	v_pk_fma_f32 v[34:35], v[148:149], v[20:21], v[34:35] op_sel_hi:[1,0,1]
	v_pk_fma_f32 v[26:27], v[40:41], v[4:5], v[26:27] op_sel_hi:[1,0,1]
	v_pk_fma_f32 v[34:35], v[154:155], v[22:23], v[34:35] op_sel_hi:[1,0,1]
	v_cvt_pk_f32_fp8_sdwa v[30:31], v31 src0_sel:WORD_1
	v_pk_fma_f32 v[34:35], v[160:161], v[24:25], v[34:35] op_sel_hi:[1,0,1]
	v_cvt_pk_f32_fp8_e32 v[150:151], v33
	v_pk_fma_f32 v[34:35], v[166:167], v[12:13], v[34:35] op_sel_hi:[1,0,1]
	v_pk_fma_f32 v[26:27], v[48:49], v[6:7], v[26:27] op_sel_hi:[1,0,1]
	v_pk_fma_f32 v[122:123], v[172:173], v[16:17], v[34:35] op_sel_hi:[1,0,1]
	v_pk_fma_f32 v[34:35], v[38:39], v[4:5], v[70:71] op_sel_hi:[1,0,1]
	v_cvt_pk_f32_fp8_sdwa v[32:33], v33 src0_sel:WORD_1
	v_pk_fma_f32 v[34:35], v[46:47], v[6:7], v[34:35] op_sel_hi:[1,0,1]
	v_cvt_pk_f32_fp8_e32 v[156:157], v53
	v_pk_fma_f32 v[34:35], v[74:75], v[8:9], v[34:35] op_sel_hi:[1,0,1]
	v_pk_fma_f32 v[8:9], v[118:119], v[8:9], v[26:27] op_sel_hi:[1,0,1]
	v_pk_fma_f32 v[34:35], v[124:125], v[10:11], v[34:35] op_sel_hi:[1,0,1]
	v_cvt_pk_f32_fp8_sdwa v[52:53], v53 src0_sel:WORD_1
	v_cvt_pk_f32_fp8_e32 v[162:163], v65
	v_pk_fma_f32 v[34:35], v[138:139], v[14:15], v[34:35] op_sel_hi:[1,0,1]
	v_pk_fma_f32 v[8:9], v[126:127], v[10:11], v[8:9] op_sel_hi:[1,0,1]
	v_cvt_pk_f32_fp8_sdwa v[64:65], v65 src0_sel:WORD_1
	v_cvt_pk_f32_fp8_e32 v[168:169], v129
	v_pk_fma_f32 v[34:35], v[144:145], v[18:19], v[34:35] op_sel_hi:[1,0,1]
	v_pk_fma_f32 v[8:9], v[28:29], v[14:15], v[8:9] op_sel_hi:[1,0,1]
	v_cvt_pk_f32_fp8_sdwa v[128:129], v129 src0_sel:WORD_1
	v_cvt_pk_f32_fp8_e32 v[174:175], v131
	v_pk_fma_f32 v[34:35], v[150:151], v[20:21], v[34:35] op_sel_hi:[1,0,1]
	v_pk_fma_f32 v[8:9], v[30:31], v[18:19], v[8:9] op_sel_hi:[1,0,1]
	v_cvt_pk_f32_fp8_sdwa v[130:131], v131 src0_sel:WORD_1
	v_pk_fma_f32 v[34:35], v[156:157], v[22:23], v[34:35] op_sel_hi:[1,0,1]
	v_pk_fma_f32 v[8:9], v[32:33], v[20:21], v[8:9] op_sel_hi:[1,0,1]
	s_waitcnt lgkmcnt(0)
	v_cvt_pk_f32_fp8_e32 v[118:119], v132
	v_pk_fma_f32 v[34:35], v[162:163], v[24:25], v[34:35] op_sel_hi:[1,0,1]
	v_pk_fma_f32 v[8:9], v[52:53], v[22:23], v[8:9] op_sel_hi:[1,0,1]
	v_pk_fma_f32 v[34:35], v[168:169], v[12:13], v[34:35] op_sel_hi:[1,0,1]
	v_pk_fma_f32 v[8:9], v[64:65], v[24:25], v[8:9] op_sel_hi:[1,0,1]
	v_pk_fma_f32 v[124:125], v[174:175], v[16:17], v[34:35] op_sel_hi:[1,0,1]
	v_pk_fma_f32 v[8:9], v[128:129], v[12:13], v[8:9] op_sel_hi:[1,0,1]
	v_cvt_pk_f32_fp8_sdwa v[126:127], v132 src0_sel:WORD_1
	v_cvt_pk_f32_fp8_e32 v[134:135], v133
	v_cvt_pk_f32_fp8_sdwa v[132:133], v133 src0_sel:WORD_1
	v_pk_fma_f32 v[128:129], v[130:131], v[16:17], v[8:9] op_sel_hi:[1,0,1]
	v_mov_b32_e32 v130, v7
	s_setprio 0
	s_add_i32 s18, s18, 2
	s_cmp_gt_u32 s17, 61
	s_cselect_b64 s[10:11], -1, 0
	s_cmp_lt_u32 s17, 62
	s_cselect_b32 s19, s18, 63
	s_lshl_b32 s20, s19, 1
	s_and_b32 s20, s20, 0xf8
	s_add_i32 s20, s20, s4
	s_ashr_i32 s21, s20, 31
	s_lshl_b64 s[20:21], s[20:21], 15
	s_add_u32 s20, s12, s20
	s_addc_u32 s21, s13, s21
	s_lshl_b32 s19, s19, 13
	s_and_b32 s19, s19, 0x6000
	s_add_u32 s20, s20, s19
	s_addc_u32 s21, s21, 0
	v_lshl_add_u64 v[6:7], s[20:21], 0, v[2:3]
	v_add_co_u32_e32 v136, vcc, s5, v6
	global_load_dword v64, v[6:7], off
	global_load_dword v66, v[6:7], off offset:256
	global_load_dword v68, v[6:7], off offset:512
	global_load_dword v70, v[6:7], off offset:768
	global_load_dword v72, v[6:7], off offset:1024
	global_load_dword v74, v[6:7], off offset:1280
	global_load_dword v48, v[6:7], off offset:1536
	global_load_dword v50, v[6:7], off offset:1792
	global_load_dword v52, v[6:7], off offset:2048
	global_load_dword v32, v[6:7], off offset:2304
	global_load_dword v34, v[6:7], off offset:2560
	global_load_dword v36, v[6:7], off offset:2816
	global_load_dword v38, v[6:7], off offset:3072
	global_load_dword v40, v[6:7], off offset:3328
	global_load_dword v42, v[6:7], off offset:3584
	global_load_dword v44, v[6:7], off offset:3840
	v_addc_co_u32_e32 v137, vcc, 0, v7, vcc
	global_load_dword v46, v[136:137], off
	global_load_dword v26, v[136:137], off offset:256
	global_load_dword v28, v[136:137], off offset:512
	global_load_dword v30, v[136:137], off offset:768
	global_load_dword v4, v[136:137], off offset:1024
	global_load_dword v6, v[136:137], off offset:1280
	global_load_dword v8, v[136:137], off offset:1536
	global_load_dword v10, v[136:137], off offset:1792
	global_load_dword v14, v[136:137], off offset:2048
	global_load_dword v18, v[136:137], off offset:2304
	global_load_dword v20, v[136:137], off offset:2560
	global_load_dword v22, v[136:137], off offset:2816
	global_load_dword v24, v[136:137], off offset:3072
	global_load_dword v12, v[136:137], off offset:3328
	global_load_dword v16, v[136:137], off offset:3584
	global_load_dword v7, v[136:137], off offset:3840
	s_waitcnt vmcnt(55)
	v_and_b32_e32 v9, 0x1fff8, v116
	v_and_b32_e32 v11, 0x1fff8, v104
	v_and_b32_e32 v13, 0x1fff8, v106
	v_and_b32_e32 v15, 0x1fff8, v108
	ds_read_b64 v[136:137], v9
	ds_read_b64 v[138:139], v11
	ds_read_b64 v[140:141], v13
	ds_read_b64 v[142:143], v15
	v_and_b32_e32 v9, 0x1fff8, v110
	v_and_b32_e32 v11, 0x1fff8, v112
	v_and_b32_e32 v13, 0x1fff8, v114
	v_and_b32_e32 v15, 0x1fff8, v98
	ds_read_b64 v[144:145], v9
	ds_read_b64 v[146:147], v11
	ds_read_b64 v[148:149], v13
	ds_read_b64 v[150:151], v15
	s_setprio 1
	s_waitcnt lgkmcnt(7)
	v_cvt_pk_f32_fp8_e32 v[152:153], v136
	v_cvt_pk_f32_fp8_sdwa v[154:155], v136 src0_sel:WORD_1
	v_cvt_pk_f32_fp8_e32 v[156:157], v137
	v_cvt_pk_f32_fp8_sdwa v[136:137], v137 src0_sel:WORD_1
	s_waitcnt lgkmcnt(6)
	v_cvt_pk_f32_fp8_e32 v[158:159], v138
	v_cvt_pk_f32_fp8_sdwa v[160:161], v138 src0_sel:WORD_1
	v_cvt_pk_f32_fp8_e32 v[162:163], v139
	v_cvt_pk_f32_fp8_sdwa v[138:139], v139 src0_sel:WORD_1
	s_waitcnt lgkmcnt(5)
	v_cvt_pk_f32_fp8_e32 v[164:165], v140
	v_cvt_pk_f32_fp8_sdwa v[166:167], v140 src0_sel:WORD_1
	v_cvt_pk_f32_fp8_e32 v[168:169], v141
	v_cvt_pk_f32_fp8_sdwa v[140:141], v141 src0_sel:WORD_1
	s_waitcnt lgkmcnt(4)
	v_cvt_pk_f32_fp8_e32 v[170:171], v142
	v_cvt_pk_f32_fp8_sdwa v[172:173], v142 src0_sel:WORD_1
	v_cvt_pk_f32_fp8_e32 v[174:175], v143
	v_cvt_pk_f32_fp8_sdwa v[142:143], v143 src0_sel:WORD_1
	s_waitcnt lgkmcnt(3)
	v_cvt_pk_f32_fp8_e32 v[176:177], v144
	v_cvt_pk_f32_fp8_sdwa v[178:179], v144 src0_sel:WORD_1
	v_cvt_pk_f32_fp8_e32 v[180:181], v145
	v_cvt_pk_f32_fp8_sdwa v[144:145], v145 src0_sel:WORD_1
	s_waitcnt lgkmcnt(2)
	v_cvt_pk_f32_fp8_e32 v[182:183], v146
	v_cvt_pk_f32_fp8_sdwa v[184:185], v146 src0_sel:WORD_1
	v_cvt_pk_f32_fp8_e32 v[186:187], v147
	v_cvt_pk_f32_fp8_sdwa v[146:147], v147 src0_sel:WORD_1
	s_waitcnt lgkmcnt(1)
	v_cvt_pk_f32_fp8_e32 v[188:189], v148
	v_cvt_pk_f32_fp8_sdwa v[190:191], v148 src0_sel:WORD_1
	v_cvt_pk_f32_fp8_e32 v[192:193], v149
	v_cvt_pk_f32_fp8_sdwa v[148:149], v149 src0_sel:WORD_1
	s_waitcnt lgkmcnt(0)
	v_cvt_pk_f32_fp8_e32 v[194:195], v150
	v_cvt_pk_f32_fp8_sdwa v[196:197], v150 src0_sel:WORD_1
	v_cvt_pk_f32_fp8_e32 v[198:199], v151
	v_cvt_pk_f32_fp8_sdwa v[150:151], v151 src0_sel:WORD_1
	s_setprio 0
	v_and_b32_e32 v9, 0x1fff8, v100
	s_waitcnt vmcnt(48)
	v_and_b32_e32 v11, 0x1fff8, v102
	v_and_b32_e32 v13, 0x1fff8, v78
	v_and_b32_e32 v15, 0x1fff8, v80
	ds_read_b64 v[200:201], v9
	ds_read_b64 v[202:203], v11
	ds_read_b64 v[204:205], v13
	ds_read_b64 v[206:207], v15
	v_and_b32_e32 v9, 0x1fff8, v82
	v_and_b32_e32 v11, 0x1fff8, v84
	v_and_b32_e32 v13, 0x1fff8, v86
	v_and_b32_e32 v15, 0x1fff8, v88
	ds_read_b64 v[208:209], v9
	ds_read_b64 v[210:211], v11
	ds_read_b64 v[212:213], v13
	ds_read_b64 v[214:215], v15
	s_setprio 1
	v_pk_fma_f32 v[118:119], v[118:119], v[130:131], v[120:121] op_sel_hi:[1,0,1]
	v_pk_fma_f32 v[120:121], v[126:127], v[130:131], v[122:123] op_sel_hi:[1,0,1]
	v_pk_fma_f32 v[122:123], v[134:135], v[130:131], v[124:125] op_sel_hi:[1,0,1]
	v_pk_fma_f32 v[118:119], v[152:153], v[116:117], v[118:119] op_sel_hi:[1,0,1]
	v_pk_fma_f32 v[120:121], v[154:155], v[116:117], v[120:121] op_sel_hi:[1,0,1]
	v_pk_fma_f32 v[122:123], v[156:157], v[116:117], v[122:123] op_sel_hi:[1,0,1]
	v_pk_fma_f32 v[124:125], v[132:133], v[130:131], v[128:129] op_sel_hi:[1,0,1]
	v_pk_fma_f32 v[118:119], v[158:159], v[104:105], v[118:119] op_sel_hi:[1,0,1]
	v_pk_fma_f32 v[120:121], v[160:161], v[104:105], v[120:121] op_sel_hi:[1,0,1]
	v_pk_fma_f32 v[122:123], v[162:163], v[104:105], v[122:123] op_sel_hi:[1,0,1]
	v_pk_fma_f32 v[116:117], v[136:137], v[116:117], v[124:125] op_sel_hi:[1,0,1]
	v_pk_fma_f32 v[118:119], v[164:165], v[106:107], v[118:119] op_sel_hi:[1,0,1]
	v_pk_fma_f32 v[120:121], v[166:167], v[106:107], v[120:121] op_sel_hi:[1,0,1]
	v_pk_fma_f32 v[122:123], v[168:169], v[106:107], v[122:123] op_sel_hi:[1,0,1]
	v_pk_fma_f32 v[104:105], v[138:139], v[104:105], v[116:117] op_sel_hi:[1,0,1]
	v_pk_fma_f32 v[118:119], v[170:171], v[108:109], v[118:119] op_sel_hi:[1,0,1]
	v_pk_fma_f32 v[120:121], v[172:173], v[108:109], v[120:121] op_sel_hi:[1,0,1]
	v_pk_fma_f32 v[122:123], v[174:175], v[108:109], v[122:123] op_sel_hi:[1,0,1]
	v_pk_fma_f32 v[104:105], v[140:141], v[106:107], v[104:105] op_sel_hi:[1,0,1]
	s_waitcnt lgkmcnt(7)
	v_cvt_pk_f32_fp8_e32 v[216:217], v200
	v_cvt_pk_f32_fp8_sdwa v[218:219], v200 src0_sel:WORD_1
	v_cvt_pk_f32_fp8_e32 v[220:221], v201
	v_pk_fma_f32 v[118:119], v[176:177], v[110:111], v[118:119] op_sel_hi:[1,0,1]
	v_pk_fma_f32 v[120:121], v[178:179], v[110:111], v[120:121] op_sel_hi:[1,0,1]
	v_pk_fma_f32 v[122:123], v[180:181], v[110:111], v[122:123] op_sel_hi:[1,0,1]
	v_pk_fma_f32 v[104:105], v[142:143], v[108:109], v[104:105] op_sel_hi:[1,0,1]
	v_cvt_pk_f32_fp8_sdwa v[200:201], v201 src0_sel:WORD_1
	s_waitcnt lgkmcnt(6)
	v_cvt_pk_f32_fp8_e32 v[222:223], v202
	v_cvt_pk_f32_fp8_sdwa v[224:225], v202 src0_sel:WORD_1
	v_cvt_pk_f32_fp8_e32 v[226:227], v203
	v_pk_fma_f32 v[118:119], v[182:183], v[112:113], v[118:119] op_sel_hi:[1,0,1]
	v_pk_fma_f32 v[120:121], v[184:185], v[112:113], v[120:121] op_sel_hi:[1,0,1]
	v_pk_fma_f32 v[122:123], v[186:187], v[112:113], v[122:123] op_sel_hi:[1,0,1]
	v_pk_fma_f32 v[104:105], v[144:145], v[110:111], v[104:105] op_sel_hi:[1,0,1]
	v_cvt_pk_f32_fp8_sdwa v[202:203], v203 src0_sel:WORD_1
	v_pk_fma_f32 v[118:119], v[188:189], v[114:115], v[118:119] op_sel_hi:[1,0,1]
	v_pk_fma_f32 v[120:121], v[190:191], v[114:115], v[120:121] op_sel_hi:[1,0,1]
	v_pk_fma_f32 v[122:123], v[192:193], v[114:115], v[122:123] op_sel_hi:[1,0,1]
	v_pk_fma_f32 v[104:105], v[146:147], v[112:113], v[104:105] op_sel_hi:[1,0,1]
	s_waitcnt lgkmcnt(4)
	v_cvt_pk_f32_fp8_e32 v[124:125], v207
	v_pk_fma_f32 v[118:119], v[194:195], v[98:99], v[118:119] op_sel_hi:[1,0,1]
	v_pk_fma_f32 v[120:121], v[196:197], v[98:99], v[120:121] op_sel_hi:[1,0,1]
	v_pk_fma_f32 v[122:123], v[198:199], v[98:99], v[122:123] op_sel_hi:[1,0,1]
	v_pk_fma_f32 v[104:105], v[148:149], v[114:115], v[104:105] op_sel_hi:[1,0,1]
	v_pk_fma_f32 v[118:119], v[216:217], v[100:101], v[118:119] op_sel_hi:[1,0,1]
	v_pk_fma_f32 v[120:121], v[218:219], v[100:101], v[120:121] op_sel_hi:[1,0,1]
	v_pk_fma_f32 v[122:123], v[220:221], v[100:101], v[122:123] op_sel_hi:[1,0,1]
	v_pk_fma_f32 v[98:99], v[150:151], v[98:99], v[104:105] op_sel_hi:[1,0,1]
	v_pk_fma_f32 v[118:119], v[222:223], v[102:103], v[118:119] op_sel_hi:[1,0,1]
	v_pk_fma_f32 v[120:121], v[224:225], v[102:103], v[120:121] op_sel_hi:[1,0,1]
	v_pk_fma_f32 v[122:123], v[226:227], v[102:103], v[122:123] op_sel_hi:[1,0,1]
	v_pk_fma_f32 v[98:99], v[200:201], v[100:101], v[98:99] op_sel_hi:[1,0,1]
	v_cvt_pk_f32_fp8_e32 v[106:107], v204
	v_cvt_pk_f32_fp8_sdwa v[108:109], v204 src0_sel:WORD_1
	v_cvt_pk_f32_fp8_e32 v[110:111], v205
	v_cvt_pk_f32_fp8_sdwa v[112:113], v205 src0_sel:WORD_1
	v_cvt_pk_f32_fp8_e32 v[114:115], v206
	v_cvt_pk_f32_fp8_sdwa v[116:117], v206 src0_sel:WORD_1
	v_cvt_pk_f32_fp8_sdwa v[126:127], v207 src0_sel:WORD_1
	s_waitcnt lgkmcnt(3)
	v_cvt_pk_f32_fp8_e32 v[128:129], v208
	v_cvt_pk_f32_fp8_sdwa v[130:131], v208 src0_sel:WORD_1
	v_cvt_pk_f32_fp8_e32 v[132:133], v209
	v_cvt_pk_f32_fp8_sdwa v[134:135], v209 src0_sel:WORD_1
	s_waitcnt lgkmcnt(2)
	v_cvt_pk_f32_fp8_e32 v[136:137], v210
	v_cvt_pk_f32_fp8_sdwa v[138:139], v210 src0_sel:WORD_1
	v_cvt_pk_f32_fp8_e32 v[140:141], v211
	v_cvt_pk_f32_fp8_sdwa v[142:143], v211 src0_sel:WORD_1
	s_waitcnt lgkmcnt(1)
	v_cvt_pk_f32_fp8_e32 v[144:145], v212
	v_cvt_pk_f32_fp8_sdwa v[146:147], v212 src0_sel:WORD_1
	v_cvt_pk_f32_fp8_e32 v[148:149], v213
	v_cvt_pk_f32_fp8_sdwa v[152:153], v213 src0_sel:WORD_1
	s_waitcnt lgkmcnt(0)
	v_cvt_pk_f32_fp8_e32 v[154:155], v214
	v_cvt_pk_f32_fp8_sdwa v[156:157], v214 src0_sel:WORD_1
	v_cvt_pk_f32_fp8_e32 v[158:159], v215
	v_cvt_pk_f32_fp8_sdwa v[160:161], v215 src0_sel:WORD_1
	v_pk_fma_f32 v[98:99], v[202:203], v[102:103], v[98:99] op_sel_hi:[1,0,1]
	s_setprio 0
	s_waitcnt vmcnt(40)
	v_and_b32_e32 v9, 0x1fff8, v90
	v_and_b32_e32 v11, 0x1fff8, v92
	v_and_b32_e32 v13, 0x1fff8, v94
	v_and_b32_e32 v15, 0x1fff8, v96
	ds_read_b64 v[100:101], v9
	ds_read_b64 v[102:103], v11
	ds_read_b64 v[104:105], v13
	ds_read_b64 v[150:151], v15
	v_and_b32_e32 v9, 0x1fff8, v76
	v_and_b32_e32 v11, 0x1fff8, v77
	v_and_b32_e32 v13, 0x1fff8, v56
	v_and_b32_e32 v15, 0x1fff8, v57
	ds_read_b64 v[162:163], v9
	ds_read_b64 v[164:165], v11
	ds_read_b64 v[166:167], v13
	ds_read_b64 v[168:169], v15
	s_setprio 1
	v_pk_fma_f32 v[106:107], v[106:107], v[78:79], v[118:119] op_sel_hi:[1,0,1]
	v_pk_fma_f32 v[108:109], v[108:109], v[78:79], v[120:121] op_sel_hi:[1,0,1]
	v_pk_fma_f32 v[110:111], v[110:111], v[78:79], v[122:123] op_sel_hi:[1,0,1]
	v_pk_fma_f32 v[78:79], v[112:113], v[78:79], v[98:99] op_sel_hi:[1,0,1]
	v_pk_fma_f32 v[106:107], v[114:115], v[80:81], v[106:107] op_sel_hi:[1,0,1]
	v_pk_fma_f32 v[108:109], v[116:117], v[80:81], v[108:109] op_sel_hi:[1,0,1]
	v_pk_fma_f32 v[110:111], v[124:125], v[80:81], v[110:111] op_sel_hi:[1,0,1]
	v_pk_fma_f32 v[78:79], v[126:127], v[80:81], v[78:79] op_sel_hi:[1,0,1]
	s_waitcnt lgkmcnt(7)
	v_cvt_pk_f32_fp8_e32 v[170:171], v100
	v_cvt_pk_f32_fp8_sdwa v[172:173], v100 src0_sel:WORD_1
	v_cvt_pk_f32_fp8_e32 v[174:175], v101
	v_cvt_pk_f32_fp8_sdwa v[100:101], v101 src0_sel:WORD_1
	v_pk_fma_f32 v[106:107], v[128:129], v[82:83], v[106:107] op_sel_hi:[1,0,1]
	v_pk_fma_f32 v[108:109], v[130:131], v[82:83], v[108:109] op_sel_hi:[1,0,1]
	v_pk_fma_f32 v[110:111], v[132:133], v[82:83], v[110:111] op_sel_hi:[1,0,1]
	v_pk_fma_f32 v[78:79], v[134:135], v[82:83], v[78:79] op_sel_hi:[1,0,1]
	s_waitcnt lgkmcnt(6)
	v_cvt_pk_f32_fp8_e32 v[176:177], v102
	v_cvt_pk_f32_fp8_sdwa v[178:179], v102 src0_sel:WORD_1
	v_cvt_pk_f32_fp8_e32 v[180:181], v103
	v_cvt_pk_f32_fp8_sdwa v[102:103], v103 src0_sel:WORD_1
	v_pk_fma_f32 v[106:107], v[136:137], v[84:85], v[106:107] op_sel_hi:[1,0,1]
	v_pk_fma_f32 v[108:109], v[138:139], v[84:85], v[108:109] op_sel_hi:[1,0,1]
	v_pk_fma_f32 v[110:111], v[140:141], v[84:85], v[110:111] op_sel_hi:[1,0,1]
	v_pk_fma_f32 v[78:79], v[142:143], v[84:85], v[78:79] op_sel_hi:[1,0,1]
	s_waitcnt lgkmcnt(5)
	v_cvt_pk_f32_fp8_e32 v[182:183], v104
	v_cvt_pk_f32_fp8_sdwa v[184:185], v104 src0_sel:WORD_1
	v_cvt_pk_f32_fp8_e32 v[186:187], v105
	v_cvt_pk_f32_fp8_sdwa v[104:105], v105 src0_sel:WORD_1
	v_pk_fma_f32 v[106:107], v[144:145], v[86:87], v[106:107] op_sel_hi:[1,0,1]
	v_pk_fma_f32 v[108:109], v[146:147], v[86:87], v[108:109] op_sel_hi:[1,0,1]
	v_pk_fma_f32 v[110:111], v[148:149], v[86:87], v[110:111] op_sel_hi:[1,0,1]
	v_pk_fma_f32 v[78:79], v[152:153], v[86:87], v[78:79] op_sel_hi:[1,0,1]
	v_pk_fma_f32 v[106:107], v[154:155], v[88:89], v[106:107] op_sel_hi:[1,0,1]
	v_pk_fma_f32 v[108:109], v[156:157], v[88:89], v[108:109] op_sel_hi:[1,0,1]
	v_pk_fma_f32 v[110:111], v[158:159], v[88:89], v[110:111] op_sel_hi:[1,0,1]
	v_pk_fma_f32 v[78:79], v[160:161], v[88:89], v[78:79] op_sel_hi:[1,0,1]
	s_waitcnt lgkmcnt(3)
	v_cvt_pk_f32_fp8_e32 v[194:195], v162
	v_cvt_pk_f32_fp8_sdwa v[196:197], v162 src0_sel:WORD_1
	v_cvt_pk_f32_fp8_e32 v[198:199], v163
	v_cvt_pk_f32_fp8_sdwa v[162:163], v163 src0_sel:WORD_1
	s_waitcnt lgkmcnt(2)
	v_cvt_pk_f32_fp8_e32 v[200:201], v164
	v_cvt_pk_f32_fp8_sdwa v[202:203], v164 src0_sel:WORD_1
	v_cvt_pk_f32_fp8_e32 v[204:205], v165
	v_cvt_pk_f32_fp8_sdwa v[164:165], v165 src0_sel:WORD_1
	v_pk_fma_f32 v[106:107], v[170:171], v[90:91], v[106:107] op_sel_hi:[1,0,1]
	v_pk_fma_f32 v[108:109], v[172:173], v[90:91], v[108:109] op_sel_hi:[1,0,1]
	v_pk_fma_f32 v[110:111], v[174:175], v[90:91], v[110:111] op_sel_hi:[1,0,1]
	v_pk_fma_f32 v[78:79], v[100:101], v[90:91], v[78:79] op_sel_hi:[1,0,1]
	v_pk_fma_f32 v[106:107], v[176:177], v[92:93], v[106:107] op_sel_hi:[1,0,1]
	v_pk_fma_f32 v[108:109], v[178:179], v[92:93], v[108:109] op_sel_hi:[1,0,1]
	v_pk_fma_f32 v[110:111], v[180:181], v[92:93], v[110:111] op_sel_hi:[1,0,1]
	v_pk_fma_f32 v[78:79], v[102:103], v[92:93], v[78:79] op_sel_hi:[1,0,1]
	v_cvt_pk_f32_fp8_e32 v[188:189], v150
	v_cvt_pk_f32_fp8_sdwa v[190:191], v150 src0_sel:WORD_1
	v_cvt_pk_f32_fp8_e32 v[192:193], v151
	v_cvt_pk_f32_fp8_sdwa v[150:151], v151 src0_sel:WORD_1
	v_pk_fma_f32 v[106:107], v[182:183], v[94:95], v[106:107] op_sel_hi:[1,0,1]
	v_pk_fma_f32 v[108:109], v[184:185], v[94:95], v[108:109] op_sel_hi:[1,0,1]
	v_pk_fma_f32 v[110:111], v[186:187], v[94:95], v[110:111] op_sel_hi:[1,0,1]
	v_pk_fma_f32 v[78:79], v[104:105], v[94:95], v[78:79] op_sel_hi:[1,0,1]
	s_waitcnt lgkmcnt(1)
	v_cvt_pk_f32_fp8_sdwa v[88:89], v167 src0_sel:WORD_1
	s_waitcnt lgkmcnt(0)
	v_cvt_pk_f32_fp8_sdwa v[94:95], v169 src0_sel:WORD_1
	v_pk_fma_f32 v[78:79], v[162:163], v[76:77], v[78:79] op_sel_hi:[1,0,1]
	v_pk_fma_f32 v[106:107], v[188:189], v[96:97], v[106:107] op_sel_hi:[1,0,1]
	v_pk_fma_f32 v[108:109], v[190:191], v[96:97], v[108:109] op_sel_hi:[1,0,1]
	v_pk_fma_f32 v[110:111], v[192:193], v[96:97], v[110:111] op_sel_hi:[1,0,1]
	v_pk_fma_f32 v[78:79], v[150:151], v[96:97], v[78:79] op_sel_hi:[1,0,1]
	v_pk_fma_f32 v[78:79], v[88:89], v[56:57], v[78:79] op_sel_hi:[1,0,1]
	v_pk_fma_f32 v[106:107], v[194:195], v[76:77], v[106:107] op_sel_hi:[1,0,1]
	v_pk_fma_f32 v[108:109], v[196:197], v[76:77], v[108:109] op_sel_hi:[1,0,1]
	v_pk_fma_f32 v[110:111], v[198:199], v[76:77], v[110:111] op_sel_hi:[1,0,1]
	v_mov_b32_e32 v76, v77
	v_pk_fma_f32 v[78:79], v[164:165], v[76:77], v[78:79] op_sel:[0,1,0] op_sel_hi:[1,1,1]
	v_cvt_pk_f32_fp8_e32 v[82:83], v166
	v_cvt_pk_f32_fp8_sdwa v[84:85], v166 src0_sel:WORD_1
	v_cvt_pk_f32_fp8_e32 v[86:87], v167
	v_cvt_pk_f32_fp8_e32 v[90:91], v168
	v_cvt_pk_f32_fp8_sdwa v[92:93], v168 src0_sel:WORD_1
	v_cvt_pk_f32_fp8_e32 v[96:97], v169
	v_pk_fma_f32 v[78:79], v[94:95], v[56:57], v[78:79] op_sel:[0,1,0] op_sel_hi:[1,1,1]
	s_setprio 0
	s_waitcnt vmcnt(32)
	v_and_b32_e32 v9, 0x1fff8, v58
	v_and_b32_e32 v11, 0x1fff8, v59
	v_and_b32_e32 v13, 0x1fff8, v60
	v_and_b32_e32 v15, 0x1fff8, v61
	ds_read_b64 v[100:101], v9
	ds_read_b64 v[102:103], v11
	ds_read_b64 v[104:105], v13
	ds_read_b64 v[112:113], v15
	v_and_b32_e32 v9, 0x1fff8, v62
	v_and_b32_e32 v11, 0x1fff8, v63
	v_and_b32_e32 v13, 0x1fff8, v54
	v_and_b32_e32 v15, 0x1fff8, v55
	ds_read_b64 v[114:115], v9
	ds_read_b64 v[118:119], v11
	ds_read_b64 v[120:121], v13
	ds_read_b64 v[122:123], v15
	s_setprio 1
	s_waitcnt lgkmcnt(7)
	v_cvt_pk_f32_fp8_e32 v[124:125], v100
	v_cvt_pk_f32_fp8_sdwa v[126:127], v100 src0_sel:WORD_1
	v_cvt_pk_f32_fp8_e32 v[128:129], v101
	v_cvt_pk_f32_fp8_sdwa v[100:101], v101 src0_sel:WORD_1
	s_waitcnt lgkmcnt(6)
	v_cvt_pk_f32_fp8_sdwa v[134:135], v103 src0_sel:WORD_1
	v_cvt_pk_f32_fp8_e32 v[130:131], v102
	s_waitcnt lgkmcnt(5)
	v_cvt_pk_f32_fp8_e32 v[138:139], v104
	v_cvt_pk_f32_fp8_sdwa v[140:141], v104 src0_sel:WORD_1
	v_cvt_pk_f32_fp8_e32 v[142:143], v105
	v_cvt_pk_f32_fp8_sdwa v[104:105], v105 src0_sel:WORD_1
	s_waitcnt lgkmcnt(4)
	v_cvt_pk_f32_fp8_sdwa v[148:149], v113 src0_sel:WORD_1
	v_pk_fma_f32 v[106:107], v[200:201], v[76:77], v[106:107] op_sel_hi:[1,0,1]
	s_waitcnt lgkmcnt(3)
	v_cvt_pk_f32_fp8_e32 v[152:153], v114
	v_cvt_pk_f32_fp8_sdwa v[154:155], v114 src0_sel:WORD_1
	v_cvt_pk_f32_fp8_e32 v[156:157], v115
	v_cvt_pk_f32_fp8_sdwa v[114:115], v115 src0_sel:WORD_1
	s_waitcnt lgkmcnt(2)
	v_cvt_pk_f32_fp8_sdwa v[162:163], v119 src0_sel:WORD_1
	v_pk_fma_f32 v[82:83], v[82:83], v[56:57], v[106:107] op_sel_hi:[1,0,1]
	v_mov_b32_e32 v106, v57
	v_cvt_pk_f32_fp8_e32 v[144:145], v112
	v_cvt_pk_f32_fp8_e32 v[158:159], v118
	v_cvt_pk_f32_fp8_sdwa v[160:161], v118 src0_sel:WORD_1
	v_cvt_pk_f32_fp8_e32 v[164:165], v119
	s_waitcnt lgkmcnt(1)
; #define GAS __attribute__((address_space(1)))
; __device__ __forceinline__ unsigned f2bf(float f) { unsigned u = __builtin_bit_cast(unsigned, f); return (u + 0x7fffu + ((u >> 16) & 1u)) >> 16; }
; template <int VVAR> __device__ __forceinline__ void peer_v_phase(LAS unsigned char* lds, int wave, int vcu, const unsigned char* __restrict__ VS_l, const unsigned* __restrict__ PW, bf16* __restrict__ Y) {
;     ...
;         if ((it & 3) == 2) {
;             const int blk = th * 128 + wave + 8 * (it >> 2);
;             bf16* yp = Y + ((size_t)blk * 1024 + cs * 8) * 64 + lane;
; #pragma unroll
;             for (int c = 0; c < 8; ++c) ((GAS unsigned short*)yp)[c * 64] = (unsigned short)f2bf(acc[c]);
; #pragma unroll
;             for (int c = 0; c < 8; ++c) acc[c] = 0.f;
;         }
	v_cvt_pk_f32_fp8_e32 v[118:119], v120
	v_cvt_pk_f32_fp8_sdwa v[168:169], v120 src0_sel:WORD_1
	v_cvt_pk_f32_fp8_e32 v[170:171], v121
	v_cvt_pk_f32_fp8_sdwa v[120:121], v121 src0_sel:WORD_1
	s_waitcnt lgkmcnt(0)
	v_cvt_pk_f32_fp8_sdwa v[176:177], v123 src0_sel:WORD_1
	v_pk_fma_f32 v[82:83], v[90:91], v[106:107], v[82:83] op_sel_hi:[1,0,1]
	v_pk_fma_f32 v[78:79], v[100:101], v[58:59], v[78:79] op_sel_hi:[1,0,1]
	v_pk_fma_f32 v[78:79], v[134:135], v[58:59], v[78:79] op_sel:[0,1,0] op_sel_hi:[1,1,1]
	v_pk_fma_f32 v[82:83], v[124:125], v[58:59], v[82:83] op_sel_hi:[1,0,1]
	v_mov_b32_e32 v90, v59
	v_pk_fma_f32 v[78:79], v[104:105], v[60:61], v[78:79] op_sel_hi:[1,0,1]
	v_pk_fma_f32 v[78:79], v[148:149], v[60:61], v[78:79] op_sel:[0,1,0] op_sel_hi:[1,1,1]
	v_pk_fma_f32 v[82:83], v[130:131], v[90:91], v[82:83] op_sel_hi:[1,0,1]
	v_pk_fma_f32 v[78:79], v[114:115], v[62:63], v[78:79] op_sel_hi:[1,0,1]
	v_pk_fma_f32 v[78:79], v[162:163], v[62:63], v[78:79] op_sel:[0,1,0] op_sel_hi:[1,1,1]
	v_pk_fma_f32 v[82:83], v[138:139], v[60:61], v[82:83] op_sel_hi:[1,0,1]
	v_mov_b32_e32 v116, v61
	v_cvt_pk_f32_fp8_e32 v[172:173], v122
	v_pk_fma_f32 v[78:79], v[120:121], v[54:55], v[78:79] op_sel_hi:[1,0,1]
	v_pk_fma_f32 v[82:83], v[144:145], v[116:117], v[82:83] op_sel_hi:[1,0,1]
	v_pk_fma_f32 v[78:79], v[176:177], v[54:55], v[78:79] op_sel:[0,1,0] op_sel_hi:[1,1,1]
	v_pk_fma_f32 v[82:83], v[152:153], v[62:63], v[82:83] op_sel_hi:[1,0,1]
	v_mov_b32_e32 v120, v63
	v_pk_fma_f32 v[82:83], v[158:159], v[120:121], v[82:83] op_sel_hi:[1,0,1]
	v_mov_b32_e32 v124, v55
	v_pk_fma_f32 v[82:83], v[118:119], v[54:55], v[82:83] op_sel_hi:[1,0,1]
	v_cvt_pk_f32_fp8_sdwa v[132:133], v102 src0_sel:WORD_1
	v_cvt_pk_f32_fp8_e32 v[102:103], v103
	v_pk_fma_f32 v[118:119], v[172:173], v[124:125], v[82:83] op_sel_hi:[1,0,1]
	v_pk_fma_f32 v[82:83], v[202:203], v[76:77], v[108:109] op_sel_hi:[1,0,1]
	v_pk_fma_f32 v[76:77], v[204:205], v[76:77], v[110:111] op_sel_hi:[1,0,1]
	v_pk_fma_f32 v[82:83], v[84:85], v[56:57], v[82:83] op_sel_hi:[1,0,1]
	v_pk_fma_f32 v[56:57], v[86:87], v[56:57], v[76:77] op_sel_hi:[1,0,1]
	v_cvt_pk_f32_fp8_sdwa v[146:147], v112 src0_sel:WORD_1
	v_cvt_pk_f32_fp8_e32 v[112:113], v113
	v_pk_fma_f32 v[56:57], v[96:97], v[106:107], v[56:57] op_sel_hi:[1,0,1]
	v_pk_fma_f32 v[82:83], v[92:93], v[106:107], v[82:83] op_sel_hi:[1,0,1]
	v_pk_fma_f32 v[56:57], v[128:129], v[58:59], v[56:57] op_sel_hi:[1,0,1]
	v_pk_fma_f32 v[82:83], v[126:127], v[58:59], v[82:83] op_sel_hi:[1,0,1]
	v_pk_fma_f32 v[56:57], v[102:103], v[90:91], v[56:57] op_sel_hi:[1,0,1]
	v_cvt_pk_f32_fp8_e32 v[178:179], v123
	v_pk_fma_f32 v[56:57], v[142:143], v[60:61], v[56:57] op_sel_hi:[1,0,1]
	v_pk_fma_f32 v[82:83], v[132:133], v[90:91], v[82:83] op_sel_hi:[1,0,1]
	v_pk_fma_f32 v[56:57], v[112:113], v[116:117], v[56:57] op_sel_hi:[1,0,1]
	v_pk_fma_f32 v[82:83], v[140:141], v[60:61], v[82:83] op_sel_hi:[1,0,1]
	v_pk_fma_f32 v[56:57], v[156:157], v[62:63], v[56:57] op_sel_hi:[1,0,1]
	v_pk_fma_f32 v[82:83], v[146:147], v[116:117], v[82:83] op_sel_hi:[1,0,1]
	v_pk_fma_f32 v[56:57], v[164:165], v[120:121], v[56:57] op_sel_hi:[1,0,1]
	v_pk_fma_f32 v[82:83], v[154:155], v[62:63], v[82:83] op_sel_hi:[1,0,1]
	v_pk_fma_f32 v[56:57], v[170:171], v[54:55], v[56:57] op_sel_hi:[1,0,1]
	v_pk_fma_f32 v[82:83], v[160:161], v[120:121], v[82:83] op_sel_hi:[1,0,1]
	v_pk_fma_f32 v[120:121], v[178:179], v[124:125], v[56:57] op_sel_hi:[1,0,1]
	v_cvt_pk_f32_fp8_sdwa v[174:175], v122 src0_sel:WORD_1
	v_pk_fma_f32 v[82:83], v[168:169], v[54:55], v[82:83] op_sel_hi:[1,0,1]
	v_pk_fma_f32 v[122:123], v[174:175], v[124:125], v[82:83] op_sel_hi:[1,0,1]
	v_mov_b32_e32 v124, v78
	v_mov_b32_e32 v125, v79
	s_setprio 0
	s_bitcmp0_b32 s17, 1
	s_cbranch_scc1 .LBB0_955
	s_lshl_b64 s[8:9], s[8:9], 17
	v_lshl_add_u64 v[54:55], v[0:1], 0, s[8:9]
	v_cvt_pk_bf16_f32 v9, v118, v119
	v_cvt_pk_bf16_f32 v11, v122, v123
	v_cvt_pk_bf16_f32 v13, v120, v121
	v_cvt_pk_bf16_f32 v15, v124, v125
	global_store_short v[54:55], v9, off
	global_store_short_d16_hi v[54:55], v9, off offset:128
	global_store_short v[54:55], v11, off offset:256
	global_store_short_d16_hi v[54:55], v11, off offset:384
	global_store_short v[54:55], v13, off offset:512
	global_store_short_d16_hi v[54:55], v13, off offset:640
	global_store_short v[54:55], v15, off offset:768
	global_store_short_d16_hi v[54:55], v15, off offset:896
	v_mov_b64_e32 v[118:119], 0
	v_mov_b64_e32 v[122:123], 0
	v_mov_b64_e32 v[120:121], 0
	v_mov_b64_e32 v[124:125], 0
	s_branch .LBB0_955

; __device__ __forceinline__ void conv_phase(LAS unsigned char* lds, int tile, int tid, const bf16* __restrict__ U, const float* __restrict__ cw, const float* __restrict__ cb, ...
;     ...
;             for (int r = 0; r < UROWS; ++r) uc[r] = __uint_as_float((unsigned)ubuf[r * CH + tid] << 16);
.LBB0_1369:
	s_or_b64 exec, exec, s[10:11]
	s_waitcnt lgkmcnt(0)
	s_barrier
	ds_read_u16 v196, v63
	ds_read_u16 v197, v63 offset:1024
	ds_read_u16 v198, v63 offset:2048
	ds_read_u16 v199, v63 offset:3072
	ds_read_u16 v200, v63 offset:4096
	ds_read_u16 v201, v63 offset:5120
	ds_read_u16 v202, v63 offset:6144
	ds_read_u16 v203, v63 offset:7168
	ds_read_u16 v204, v63 offset:8192
	ds_read_u16 v205, v63 offset:9216
	ds_read_u16 v206, v63 offset:10240
	ds_read_u16 v207, v63 offset:11264
	ds_read_u16 v208, v63 offset:12288
	ds_read_u16 v209, v63 offset:13312
	ds_read_u16 v210, v63 offset:14336
	ds_read_u16 v211, v63 offset:15360
	ds_read_u16 v212, v63 offset:16384
	ds_read_u16 v213, v63 offset:17408
	ds_read_u16 v214, v63 offset:18432
	ds_read_u16 v215, v63 offset:19456
	ds_read_u16 v216, v63 offset:20480
	ds_read_u16 v217, v63 offset:21504
	ds_read_u16 v218, v63 offset:22528
	ds_read_u16 v219, v63 offset:23552
	ds_read_u16 v220, v63 offset:24576
	ds_read_u16 v221, v63 offset:25600
	ds_read_u16 v222, v63 offset:26624
	ds_read_u16 v223, v63 offset:27648
	ds_read_u16 v224, v63 offset:28672
	ds_read_u16 v225, v63 offset:29696
	ds_read_u16 v226, v63 offset:30720
	ds_read_u16 v227, v63 offset:31744
	ds_read_u16 v228, v63 offset:32768
	ds_read_u16 v229, v63 offset:33792
	ds_read_u16 v230, v63 offset:34816
	ds_read_u16 v231, v63 offset:35840
	ds_read_u16 v232, v63 offset:36864
	ds_read_u16 v233, v63 offset:37888
	ds_read_u16 v234, v63 offset:38912
	ds_read_u16 v235, v63 offset:39936
	ds_read_u16 v236, v63 offset:40960
	ds_read_u16 v237, v63 offset:41984
	ds_read_u16 v238, v63 offset:43008
	ds_read_u16 v239, v63 offset:44032
	ds_read_u16 v240, v63 offset:45056
	ds_read_u16 v241, v63 offset:46080
	ds_read_u16 v242, v63 offset:47104
	ds_read_u16 v243, v63 offset:48128
	ds_read_u16 v244, v63 offset:49152
	ds_read_u16 v245, v63 offset:50176
	ds_read_u16 v246, v63 offset:51200
	ds_read_u16 v247, v63 offset:52224
	s_waitcnt lgkmcnt(0)
	v_lshlrev_b32_e32 v72, 16, v196
	v_lshlrev_b32_e32 v73, 16, v197
	v_lshlrev_b32_e32 v134, 16, v197
	v_lshlrev_b32_e32 v74, 16, v198
	v_lshlrev_b32_e32 v135, 16, v198
	v_lshlrev_b32_e32 v75, 16, v199
	v_lshlrev_b32_e32 v136, 16, v199
	v_lshlrev_b32_e32 v76, 16, v200
	v_lshlrev_b32_e32 v137, 16, v200
	v_lshlrev_b32_e32 v77, 16, v201
	v_lshlrev_b32_e32 v138, 16, v201
	v_lshlrev_b32_e32 v78, 16, v202
	v_lshlrev_b32_e32 v139, 16, v202
	v_lshlrev_b32_e32 v79, 16, v203
	v_lshlrev_b32_e32 v140, 16, v203
	v_lshlrev_b32_e32 v80, 16, v204
	v_lshlrev_b32_e32 v141, 16, v204
	v_lshlrev_b32_e32 v81, 16, v205
	v_lshlrev_b32_e32 v142, 16, v205
	v_lshlrev_b32_e32 v82, 16, v206
	v_lshlrev_b32_e32 v143, 16, v206
	v_lshlrev_b32_e32 v83, 16, v207
	v_lshlrev_b32_e32 v144, 16, v207
	v_lshlrev_b32_e32 v84, 16, v208
	v_lshlrev_b32_e32 v145, 16, v208
	v_lshlrev_b32_e32 v85, 16, v209
	v_lshlrev_b32_e32 v146, 16, v209
	v_lshlrev_b32_e32 v86, 16, v210
	v_lshlrev_b32_e32 v147, 16, v210
	v_lshlrev_b32_e32 v87, 16, v211
	v_lshlrev_b32_e32 v148, 16, v211
	v_lshlrev_b32_e32 v88, 16, v212
	v_lshlrev_b32_e32 v149, 16, v212
	v_lshlrev_b32_e32 v89, 16, v213
	v_lshlrev_b32_e32 v150, 16, v213
	v_lshlrev_b32_e32 v90, 16, v214
	v_lshlrev_b32_e32 v151, 16, v214
	v_lshlrev_b32_e32 v91, 16, v215
	v_lshlrev_b32_e32 v152, 16, v215
	v_lshlrev_b32_e32 v92, 16, v216
	v_lshlrev_b32_e32 v153, 16, v216
	v_lshlrev_b32_e32 v93, 16, v217
	v_lshlrev_b32_e32 v154, 16, v217
	v_lshlrev_b32_e32 v94, 16, v218
	v_lshlrev_b32_e32 v155, 16, v218
	v_lshlrev_b32_e32 v95, 16, v219
	v_lshlrev_b32_e32 v156, 16, v219
	v_lshlrev_b32_e32 v96, 16, v220
	v_lshlrev_b32_e32 v157, 16, v220
	v_lshlrev_b32_e32 v97, 16, v221
	v_lshlrev_b32_e32 v158, 16, v221
	v_lshlrev_b32_e32 v98, 16, v222
	v_lshlrev_b32_e32 v159, 16, v222
	v_lshlrev_b32_e32 v99, 16, v223
	v_lshlrev_b32_e32 v160, 16, v223
	v_lshlrev_b32_e32 v100, 16, v224
	v_lshlrev_b32_e32 v161, 16, v224
	v_lshlrev_b32_e32 v101, 16, v225
	v_lshlrev_b32_e32 v162, 16, v225
	v_lshlrev_b32_e32 v102, 16, v226
	v_lshlrev_b32_e32 v163, 16, v226
	v_lshlrev_b32_e32 v103, 16, v227
	v_lshlrev_b32_e32 v164, 16, v227
	v_lshlrev_b32_e32 v104, 16, v228
	v_lshlrev_b32_e32 v165, 16, v228
	v_lshlrev_b32_e32 v105, 16, v229
	v_lshlrev_b32_e32 v166, 16, v229
	v_lshlrev_b32_e32 v106, 16, v230
	v_lshlrev_b32_e32 v167, 16, v230
	v_lshlrev_b32_e32 v107, 16, v231
	v_lshlrev_b32_e32 v168, 16, v231
	v_lshlrev_b32_e32 v108, 16, v232
	v_lshlrev_b32_e32 v169, 16, v232
	v_lshlrev_b32_e32 v109, 16, v233
	v_lshlrev_b32_e32 v170, 16, v233
	v_lshlrev_b32_e32 v110, 16, v234
	v_lshlrev_b32_e32 v171, 16, v234
	v_lshlrev_b32_e32 v111, 16, v235
	v_lshlrev_b32_e32 v172, 16, v235
	v_lshlrev_b32_e32 v112, 16, v236
	v_lshlrev_b32_e32 v173, 16, v236
	v_lshlrev_b32_e32 v113, 16, v237
	v_lshlrev_b32_e32 v174, 16, v237
	v_lshlrev_b32_e32 v114, 16, v238
	v_lshlrev_b32_e32 v175, 16, v238
	v_lshlrev_b32_e32 v115, 16, v239
	v_lshlrev_b32_e32 v176, 16, v239
	v_lshlrev_b32_e32 v116, 16, v240
	v_lshlrev_b32_e32 v177, 16, v240
	v_lshlrev_b32_e32 v117, 16, v241
	v_lshlrev_b32_e32 v178, 16, v241
	v_lshlrev_b32_e32 v118, 16, v242
	v_lshlrev_b32_e32 v179, 16, v242
	v_lshlrev_b32_e32 v119, 16, v243
	v_lshlrev_b32_e32 v180, 16, v243
	v_lshlrev_b32_e32 v120, 16, v244
	v_lshlrev_b32_e32 v181, 16, v244
	v_lshlrev_b32_e32 v121, 16, v245
	v_lshlrev_b32_e32 v182, 16, v245
	v_lshlrev_b32_e32 v122, 16, v246
	v_lshlrev_b32_e32 v183, 16, v246
	v_lshlrev_b32_e32 v123, 16, v247
	v_lshlrev_b32_e32 v184, 16, v247
	ds_read_u16 v196, v63 offset:53248
	ds_read_u16 v197, v63 offset:54272
	ds_read_u16 v198, v63 offset:55296
	ds_read_u16 v199, v63 offset:56320
	ds_read_u16 v200, v63 offset:57344
	ds_read_u16 v201, v63 offset:58368
	ds_read_u16 v202, v63 offset:59392
	ds_read_u16 v203, v63 offset:60416
	ds_read_u16 v204, v63 offset:61440
	ds_read_u16 v205, v63 offset:62464
	s_waitcnt lgkmcnt(0)
; __device__ __forceinline__ void conv_phase(LAS unsigned char* lds, int tile, int tid, const bf16* __restrict__ U, const float* __restrict__ cw, const float* __restrict__ cb, ...
;     ...
;             for (int r = 0; r < UROWS; ++r) uc[r] = __uint_as_float((unsigned)ubuf[r * CH + tid] << 16);
; #pragma unroll
;             for (int tk = 0; tk < HT; ++tk) { float a = bias;
; #pragma unroll
;                 for (int j = 0; j < CKW; ++j) a += w[j] * uc[tk + j];
;                 obuf[tk * CH + tid] = a; }
	v_lshlrev_b32_e32 v124, 16, v196
	v_lshlrev_b32_e32 v185, 16, v196
	v_lshlrev_b32_e32 v125, 16, v197
	v_lshlrev_b32_e32 v186, 16, v197
	v_lshlrev_b32_e32 v126, 16, v198
	v_lshlrev_b32_e32 v187, 16, v198
	v_lshlrev_b32_e32 v127, 16, v199
	v_lshlrev_b32_e32 v188, 16, v199
	v_lshlrev_b32_e32 v128, 16, v200
	v_lshlrev_b32_e32 v189, 16, v200
	v_lshlrev_b32_e32 v129, 16, v201
	v_lshlrev_b32_e32 v190, 16, v201
	v_lshlrev_b32_e32 v130, 16, v202
	v_lshlrev_b32_e32 v191, 16, v202
	v_lshlrev_b32_e32 v131, 16, v203
	v_lshlrev_b32_e32 v192, 16, v203
	v_lshlrev_b32_e32 v132, 16, v204
	v_lshlrev_b32_e32 v193, 16, v204
	v_lshlrev_b32_e32 v133, 16, v205
	s_waitcnt vmcnt(0)
	v_pk_fma_f32 v[198:199], v[72:73], v[18:19], v[56:57] op_sel:[0,1,0] op_sel_hi:[1,1,0]
	v_pk_fma_f32 v[200:201], v[74:75], v[18:19], v[56:57] op_sel:[0,1,0] op_sel_hi:[1,1,0]
	v_pk_fma_f32 v[202:203], v[76:77], v[18:19], v[56:57] op_sel:[0,1,0] op_sel_hi:[1,1,0]
	v_pk_fma_f32 v[204:205], v[78:79], v[18:19], v[56:57] op_sel:[0,1,0] op_sel_hi:[1,1,0]
	v_pk_fma_f32 v[198:199], v[134:135], v[32:33], v[198:199] op_sel:[0,0,0] op_sel_hi:[1,0,1]
	v_pk_fma_f32 v[200:201], v[136:137], v[32:33], v[200:201] op_sel:[0,0,0] op_sel_hi:[1,0,1]
	v_pk_fma_f32 v[202:203], v[138:139], v[32:33], v[202:203] op_sel:[0,0,0] op_sel_hi:[1,0,1]
	v_pk_fma_f32 v[204:205], v[140:141], v[32:33], v[204:205] op_sel:[0,0,0] op_sel_hi:[1,0,1]
	v_pk_fma_f32 v[198:199], v[74:75], v[26:27], v[198:199] op_sel:[0,0,0] op_sel_hi:[1,0,1]
	v_pk_fma_f32 v[200:201], v[76:77], v[26:27], v[200:201] op_sel:[0,0,0] op_sel_hi:[1,0,1]
	v_pk_fma_f32 v[202:203], v[78:79], v[26:27], v[202:203] op_sel:[0,0,0] op_sel_hi:[1,0,1]
	v_pk_fma_f32 v[204:205], v[80:81], v[26:27], v[204:205] op_sel:[0,0,0] op_sel_hi:[1,0,1]
	v_pk_fma_f32 v[198:199], v[136:137], v[32:33], v[198:199] op_sel:[0,1,0] op_sel_hi:[1,1,1]
	v_pk_fma_f32 v[200:201], v[138:139], v[32:33], v[200:201] op_sel:[0,1,0] op_sel_hi:[1,1,1]
	v_pk_fma_f32 v[202:203], v[140:141], v[32:33], v[202:203] op_sel:[0,1,0] op_sel_hi:[1,1,1]
	v_pk_fma_f32 v[204:205], v[142:143], v[32:33], v[204:205] op_sel:[0,1,0] op_sel_hi:[1,1,1]
	v_pk_fma_f32 v[198:199], v[76:77], v[26:27], v[198:199] op_sel:[0,1,0] op_sel_hi:[1,1,1]
	v_pk_fma_f32 v[200:201], v[78:79], v[26:27], v[200:201] op_sel:[0,1,0] op_sel_hi:[1,1,1]
	v_pk_fma_f32 v[202:203], v[80:81], v[26:27], v[202:203] op_sel:[0,1,0] op_sel_hi:[1,1,1]
	v_pk_fma_f32 v[204:205], v[82:83], v[26:27], v[204:205] op_sel:[0,1,0] op_sel_hi:[1,1,1]
	v_pk_fma_f32 v[198:199], v[138:139], v[34:35], v[198:199] op_sel:[0,0,0] op_sel_hi:[1,0,1]
	v_pk_fma_f32 v[200:201], v[140:141], v[34:35], v[200:201] op_sel:[0,0,0] op_sel_hi:[1,0,1]
	v_pk_fma_f32 v[202:203], v[142:143], v[34:35], v[202:203] op_sel:[0,0,0] op_sel_hi:[1,0,1]
	v_pk_fma_f32 v[204:205], v[144:145], v[34:35], v[204:205] op_sel:[0,0,0] op_sel_hi:[1,0,1]
	v_pk_fma_f32 v[198:199], v[78:79], v[34:35], v[198:199] op_sel:[0,1,0] op_sel_hi:[1,1,1]
	v_pk_fma_f32 v[200:201], v[80:81], v[34:35], v[200:201] op_sel:[0,1,0] op_sel_hi:[1,1,1]
	v_pk_fma_f32 v[202:203], v[82:83], v[34:35], v[202:203] op_sel:[0,1,0] op_sel_hi:[1,1,1]
	v_pk_fma_f32 v[204:205], v[84:85], v[34:35], v[204:205] op_sel:[0,1,0] op_sel_hi:[1,1,1]
	v_pk_fma_f32 v[198:199], v[140:141], v[36:37], v[198:199] op_sel:[0,0,0] op_sel_hi:[1,0,1]
	v_pk_fma_f32 v[200:201], v[142:143], v[36:37], v[200:201] op_sel:[0,0,0] op_sel_hi:[1,0,1]
	v_pk_fma_f32 v[202:203], v[144:145], v[36:37], v[202:203] op_sel:[0,0,0] op_sel_hi:[1,0,1]
	v_pk_fma_f32 v[204:205], v[146:147], v[36:37], v[204:205] op_sel:[0,0,0] op_sel_hi:[1,0,1]
	v_pk_fma_f32 v[198:199], v[80:81], v[28:29], v[198:199] op_sel:[0,0,0] op_sel_hi:[1,0,1]
	v_pk_fma_f32 v[200:201], v[82:83], v[28:29], v[200:201] op_sel:[0,0,0] op_sel_hi:[1,0,1]
	v_pk_fma_f32 v[202:203], v[84:85], v[28:29], v[202:203] op_sel:[0,0,0] op_sel_hi:[1,0,1]
	v_pk_fma_f32 v[204:205], v[86:87], v[28:29], v[204:205] op_sel:[0,0,0] op_sel_hi:[1,0,1]
	v_pk_fma_f32 v[198:199], v[142:143], v[36:37], v[198:199] op_sel:[0,1,0] op_sel_hi:[1,1,1]
	v_pk_fma_f32 v[200:201], v[144:145], v[36:37], v[200:201] op_sel:[0,1,0] op_sel_hi:[1,1,1]
	v_pk_fma_f32 v[202:203], v[146:147], v[36:37], v[202:203] op_sel:[0,1,0] op_sel_hi:[1,1,1]
	v_pk_fma_f32 v[204:205], v[148:149], v[36:37], v[204:205] op_sel:[0,1,0] op_sel_hi:[1,1,1]
	v_pk_fma_f32 v[198:199], v[82:83], v[38:39], v[198:199] op_sel:[0,0,0] op_sel_hi:[1,0,1]
	v_pk_fma_f32 v[200:201], v[84:85], v[38:39], v[200:201] op_sel:[0,0,0] op_sel_hi:[1,0,1]
	v_pk_fma_f32 v[202:203], v[86:87], v[38:39], v[202:203] op_sel:[0,0,0] op_sel_hi:[1,0,1]
	v_pk_fma_f32 v[204:205], v[88:89], v[38:39], v[204:205] op_sel:[0,0,0] op_sel_hi:[1,0,1]
	v_pk_fma_f32 v[198:199], v[144:145], v[38:39], v[198:199] op_sel:[0,1,0] op_sel_hi:[1,1,1]
	v_pk_fma_f32 v[200:201], v[146:147], v[38:39], v[200:201] op_sel:[0,1,0] op_sel_hi:[1,1,1]
	v_pk_fma_f32 v[202:203], v[148:149], v[38:39], v[202:203] op_sel:[0,1,0] op_sel_hi:[1,1,1]
	v_pk_fma_f32 v[204:205], v[150:151], v[38:39], v[204:205] op_sel:[0,1,0] op_sel_hi:[1,1,1]
	v_pk_fma_f32 v[198:199], v[84:85], v[28:29], v[198:199] op_sel:[0,1,0] op_sel_hi:[1,1,1]
	v_pk_fma_f32 v[200:201], v[86:87], v[28:29], v[200:201] op_sel:[0,1,0] op_sel_hi:[1,1,1]
	v_pk_fma_f32 v[202:203], v[88:89], v[28:29], v[202:203] op_sel:[0,1,0] op_sel_hi:[1,1,1]
	v_pk_fma_f32 v[204:205], v[90:91], v[28:29], v[204:205] op_sel:[0,1,0] op_sel_hi:[1,1,1]
	v_pk_fma_f32 v[198:199], v[146:147], v[40:41], v[198:199] op_sel:[0,0,0] op_sel_hi:[1,0,1]
	v_pk_fma_f32 v[200:201], v[148:149], v[40:41], v[200:201] op_sel:[0,0,0] op_sel_hi:[1,0,1]
	v_pk_fma_f32 v[202:203], v[150:151], v[40:41], v[202:203] op_sel:[0,0,0] op_sel_hi:[1,0,1]
; __device__ __forceinline__ void conv_phase(LAS unsigned char* lds, int tile, int tid, const bf16* __restrict__ U, const float* __restrict__ cw, const float* __restrict__ cb, ...
;     ...
;             for (int tk = 0; tk < HT; ++tk) { float a = bias;
; #pragma unroll
;                 for (int j = 0; j < CKW; ++j) a += w[j] * uc[tk + j];
;                 obuf[tk * CH + tid] = a; }
	v_pk_fma_f32 v[204:205], v[152:153], v[40:41], v[204:205] op_sel:[0,0,0] op_sel_hi:[1,0,1]
	v_pk_fma_f32 v[198:199], v[86:87], v[40:41], v[198:199] op_sel:[0,1,0] op_sel_hi:[1,1,1]
	v_pk_fma_f32 v[200:201], v[88:89], v[40:41], v[200:201] op_sel:[0,1,0] op_sel_hi:[1,1,1]
	v_pk_fma_f32 v[202:203], v[90:91], v[40:41], v[202:203] op_sel:[0,1,0] op_sel_hi:[1,1,1]
	v_pk_fma_f32 v[204:205], v[92:93], v[40:41], v[204:205] op_sel:[0,1,0] op_sel_hi:[1,1,1]
	v_pk_fma_f32 v[198:199], v[148:149], v[42:43], v[198:199] op_sel:[0,0,0] op_sel_hi:[1,0,1]
	v_pk_fma_f32 v[200:201], v[150:151], v[42:43], v[200:201] op_sel:[0,0,0] op_sel_hi:[1,0,1]
	v_pk_fma_f32 v[202:203], v[152:153], v[42:43], v[202:203] op_sel:[0,0,0] op_sel_hi:[1,0,1]
	v_pk_fma_f32 v[204:205], v[154:155], v[42:43], v[204:205] op_sel:[0,0,0] op_sel_hi:[1,0,1]
	v_pk_fma_f32 v[198:199], v[88:89], v[30:31], v[198:199] op_sel:[0,0,0] op_sel_hi:[1,0,1]
	v_pk_fma_f32 v[200:201], v[90:91], v[30:31], v[200:201] op_sel:[0,0,0] op_sel_hi:[1,0,1]
	v_pk_fma_f32 v[202:203], v[92:93], v[30:31], v[202:203] op_sel:[0,0,0] op_sel_hi:[1,0,1]
	v_pk_fma_f32 v[204:205], v[94:95], v[30:31], v[204:205] op_sel:[0,0,0] op_sel_hi:[1,0,1]
	v_pk_fma_f32 v[198:199], v[150:151], v[42:43], v[198:199] op_sel:[0,1,0] op_sel_hi:[1,1,1]
	v_pk_fma_f32 v[200:201], v[152:153], v[42:43], v[200:201] op_sel:[0,1,0] op_sel_hi:[1,1,1]
	v_pk_fma_f32 v[202:203], v[154:155], v[42:43], v[202:203] op_sel:[0,1,0] op_sel_hi:[1,1,1]
	v_pk_fma_f32 v[204:205], v[156:157], v[42:43], v[204:205] op_sel:[0,1,0] op_sel_hi:[1,1,1]
	v_pk_fma_f32 v[198:199], v[90:91], v[44:45], v[198:199] op_sel:[0,0,0] op_sel_hi:[1,0,1]
	v_pk_fma_f32 v[200:201], v[92:93], v[44:45], v[200:201] op_sel:[0,0,0] op_sel_hi:[1,0,1]
	v_pk_fma_f32 v[202:203], v[94:95], v[44:45], v[202:203] op_sel:[0,0,0] op_sel_hi:[1,0,1]
	v_pk_fma_f32 v[204:205], v[96:97], v[44:45], v[204:205] op_sel:[0,0,0] op_sel_hi:[1,0,1]
	v_pk_fma_f32 v[198:199], v[152:153], v[44:45], v[198:199] op_sel:[0,1,0] op_sel_hi:[1,1,1]
	v_pk_fma_f32 v[200:201], v[154:155], v[44:45], v[200:201] op_sel:[0,1,0] op_sel_hi:[1,1,1]
	v_pk_fma_f32 v[202:203], v[156:157], v[44:45], v[202:203] op_sel:[0,1,0] op_sel_hi:[1,1,1]
	v_pk_fma_f32 v[204:205], v[158:159], v[44:45], v[204:205] op_sel:[0,1,0] op_sel_hi:[1,1,1]
	v_pk_fma_f32 v[198:199], v[92:93], v[30:31], v[198:199] op_sel:[0,1,0] op_sel_hi:[1,1,1]
	v_pk_fma_f32 v[200:201], v[94:95], v[30:31], v[200:201] op_sel:[0,1,0] op_sel_hi:[1,1,1]
	v_pk_fma_f32 v[202:203], v[96:97], v[30:31], v[202:203] op_sel:[0,1,0] op_sel_hi:[1,1,1]
	v_pk_fma_f32 v[204:205], v[98:99], v[30:31], v[204:205] op_sel:[0,1,0] op_sel_hi:[1,1,1]
	v_pk_fma_f32 v[198:199], v[154:155], v[46:47], v[198:199] op_sel:[0,0,0] op_sel_hi:[1,0,1]
	v_pk_fma_f32 v[200:201], v[156:157], v[46:47], v[200:201] op_sel:[0,0,0] op_sel_hi:[1,0,1]
	v_pk_fma_f32 v[202:203], v[158:159], v[46:47], v[202:203] op_sel:[0,0,0] op_sel_hi:[1,0,1]
	v_pk_fma_f32 v[204:205], v[160:161], v[46:47], v[204:205] op_sel:[0,0,0] op_sel_hi:[1,0,1]
	v_pk_fma_f32 v[198:199], v[94:95], v[46:47], v[198:199] op_sel:[0,1,0] op_sel_hi:[1,1,1]
	v_pk_fma_f32 v[200:201], v[96:97], v[46:47], v[200:201] op_sel:[0,1,0] op_sel_hi:[1,1,1]
	v_pk_fma_f32 v[202:203], v[98:99], v[46:47], v[202:203] op_sel:[0,1,0] op_sel_hi:[1,1,1]
	v_pk_fma_f32 v[204:205], v[100:101], v[46:47], v[204:205] op_sel:[0,1,0] op_sel_hi:[1,1,1]
	v_pk_fma_f32 v[198:199], v[156:157], v[48:49], v[198:199] op_sel:[0,0,0] op_sel_hi:[1,0,1]
	v_pk_fma_f32 v[200:201], v[158:159], v[48:49], v[200:201] op_sel:[0,0,0] op_sel_hi:[1,0,1]
	v_pk_fma_f32 v[202:203], v[160:161], v[48:49], v[202:203] op_sel:[0,0,0] op_sel_hi:[1,0,1]
	v_pk_fma_f32 v[204:205], v[162:163], v[48:49], v[204:205] op_sel:[0,0,0] op_sel_hi:[1,0,1]
	v_pk_fma_f32 v[198:199], v[96:97], v[48:49], v[198:199] op_sel:[0,1,0] op_sel_hi:[1,1,1]
	v_pk_fma_f32 v[200:201], v[98:99], v[48:49], v[200:201] op_sel:[0,1,0] op_sel_hi:[1,1,1]
	v_pk_fma_f32 v[202:203], v[100:101], v[48:49], v[202:203] op_sel:[0,1,0] op_sel_hi:[1,1,1]
	v_pk_fma_f32 v[204:205], v[102:103], v[48:49], v[204:205] op_sel:[0,1,0] op_sel_hi:[1,1,1]
	v_pk_fma_f32 v[198:199], v[158:159], v[50:51], v[198:199] op_sel:[0,1,0] op_sel_hi:[1,1,1]
	v_pk_fma_f32 v[200:201], v[160:161], v[50:51], v[200:201] op_sel:[0,1,0] op_sel_hi:[1,1,1]
	v_pk_fma_f32 v[202:203], v[162:163], v[50:51], v[202:203] op_sel:[0,1,0] op_sel_hi:[1,1,1]
	v_pk_fma_f32 v[204:205], v[164:165], v[50:51], v[204:205] op_sel:[0,1,0] op_sel_hi:[1,1,1]
	v_pk_fma_f32 v[198:199], v[98:99], v[52:53], v[198:199] op_sel:[0,0,0] op_sel_hi:[1,0,1]
	v_pk_fma_f32 v[200:201], v[100:101], v[52:53], v[200:201] op_sel:[0,0,0] op_sel_hi:[1,0,1]
	v_pk_fma_f32 v[202:203], v[102:103], v[52:53], v[202:203] op_sel:[0,0,0] op_sel_hi:[1,0,1]
	v_pk_fma_f32 v[204:205], v[104:105], v[52:53], v[204:205] op_sel:[0,0,0] op_sel_hi:[1,0,1]
	v_pk_fma_f32 v[198:199], v[160:161], v[52:53], v[198:199] op_sel:[0,1,0] op_sel_hi:[1,1,1]
	v_pk_fma_f32 v[200:201], v[162:163], v[52:53], v[200:201] op_sel:[0,1,0] op_sel_hi:[1,1,1]
	v_pk_fma_f32 v[202:203], v[164:165], v[52:53], v[202:203] op_sel:[0,1,0] op_sel_hi:[1,1,1]
	v_pk_fma_f32 v[204:205], v[166:167], v[52:53], v[204:205] op_sel:[0,1,0] op_sel_hi:[1,1,1]
	v_pk_fma_f32 v[198:199], v[100:101], v[50:51], v[198:199] op_sel:[0,0,0] op_sel_hi:[1,0,1]
	v_pk_fma_f32 v[200:201], v[102:103], v[50:51], v[200:201] op_sel:[0,0,0] op_sel_hi:[1,0,1]
	v_pk_fma_f32 v[202:203], v[104:105], v[50:51], v[202:203] op_sel:[0,0,0] op_sel_hi:[1,0,1]
	v_pk_fma_f32 v[204:205], v[106:107], v[50:51], v[204:205] op_sel:[0,0,0] op_sel_hi:[1,0,1]
	v_pk_fma_f32 v[198:199], v[162:163], v[54:55], v[198:199] op_sel:[0,0,0] op_sel_hi:[1,0,1]
; __device__ __forceinline__ void conv_phase(LAS unsigned char* lds, int tile, int tid, const bf16* __restrict__ U, const float* __restrict__ cw, const float* __restrict__ cb, ...
;     ...
;             for (int tk = 0; tk < HT; ++tk) { float a = bias;
; #pragma unroll
;                 for (int j = 0; j < CKW; ++j) a += w[j] * uc[tk + j];
;                 obuf[tk * CH + tid] = a; }
	v_pk_fma_f32 v[200:201], v[164:165], v[54:55], v[200:201] op_sel:[0,0,0] op_sel_hi:[1,0,1]
	v_pk_fma_f32 v[202:203], v[166:167], v[54:55], v[202:203] op_sel:[0,0,0] op_sel_hi:[1,0,1]
	v_pk_fma_f32 v[204:205], v[168:169], v[54:55], v[204:205] op_sel:[0,0,0] op_sel_hi:[1,0,1]
	v_pk_fma_f32 v[198:199], v[102:103], v[54:55], v[198:199] op_sel:[0,1,0] op_sel_hi:[1,1,1]
	v_pk_fma_f32 v[200:201], v[104:105], v[54:55], v[200:201] op_sel:[0,1,0] op_sel_hi:[1,1,1]
	v_pk_fma_f32 v[202:203], v[106:107], v[54:55], v[202:203] op_sel:[0,1,0] op_sel_hi:[1,1,1]
	v_pk_fma_f32 v[204:205], v[108:109], v[54:55], v[204:205] op_sel:[0,1,0] op_sel_hi:[1,1,1]
	ds_write2st64_b32 v64, v198, v199 offset0:0 offset1:8
	ds_write2st64_b32 v64, v200, v201 offset0:16 offset1:24
	ds_write2st64_b32 v64, v202, v203 offset0:32 offset1:40
	ds_write2st64_b32 v64, v204, v205 offset0:48 offset1:56
	v_pk_fma_f32 v[198:199], v[80:81], v[18:19], v[56:57] op_sel:[0,1,0] op_sel_hi:[1,1,0]
	v_pk_fma_f32 v[200:201], v[82:83], v[18:19], v[56:57] op_sel:[0,1,0] op_sel_hi:[1,1,0]
	v_pk_fma_f32 v[202:203], v[84:85], v[18:19], v[56:57] op_sel:[0,1,0] op_sel_hi:[1,1,0]
	v_pk_fma_f32 v[204:205], v[86:87], v[18:19], v[56:57] op_sel:[0,1,0] op_sel_hi:[1,1,0]
	v_pk_fma_f32 v[198:199], v[142:143], v[32:33], v[198:199] op_sel:[0,0,0] op_sel_hi:[1,0,1]
	v_pk_fma_f32 v[200:201], v[144:145], v[32:33], v[200:201] op_sel:[0,0,0] op_sel_hi:[1,0,1]
	v_pk_fma_f32 v[202:203], v[146:147], v[32:33], v[202:203] op_sel:[0,0,0] op_sel_hi:[1,0,1]
	v_pk_fma_f32 v[204:205], v[148:149], v[32:33], v[204:205] op_sel:[0,0,0] op_sel_hi:[1,0,1]
	v_pk_fma_f32 v[198:199], v[82:83], v[26:27], v[198:199] op_sel:[0,0,0] op_sel_hi:[1,0,1]
	v_pk_fma_f32 v[200:201], v[84:85], v[26:27], v[200:201] op_sel:[0,0,0] op_sel_hi:[1,0,1]
	v_pk_fma_f32 v[202:203], v[86:87], v[26:27], v[202:203] op_sel:[0,0,0] op_sel_hi:[1,0,1]
	v_pk_fma_f32 v[204:205], v[88:89], v[26:27], v[204:205] op_sel:[0,0,0] op_sel_hi:[1,0,1]
	v_pk_fma_f32 v[198:199], v[144:145], v[32:33], v[198:199] op_sel:[0,1,0] op_sel_hi:[1,1,1]
	v_pk_fma_f32 v[200:201], v[146:147], v[32:33], v[200:201] op_sel:[0,1,0] op_sel_hi:[1,1,1]
	v_pk_fma_f32 v[202:203], v[148:149], v[32:33], v[202:203] op_sel:[0,1,0] op_sel_hi:[1,1,1]
	v_pk_fma_f32 v[204:205], v[150:151], v[32:33], v[204:205] op_sel:[0,1,0] op_sel_hi:[1,1,1]
	v_pk_fma_f32 v[198:199], v[84:85], v[26:27], v[198:199] op_sel:[0,1,0] op_sel_hi:[1,1,1]
	v_pk_fma_f32 v[200:201], v[86:87], v[26:27], v[200:201] op_sel:[0,1,0] op_sel_hi:[1,1,1]
	v_pk_fma_f32 v[202:203], v[88:89], v[26:27], v[202:203] op_sel:[0,1,0] op_sel_hi:[1,1,1]
	v_pk_fma_f32 v[204:205], v[90:91], v[26:27], v[204:205] op_sel:[0,1,0] op_sel_hi:[1,1,1]
	v_pk_fma_f32 v[198:199], v[146:147], v[34:35], v[198:199] op_sel:[0,0,0] op_sel_hi:[1,0,1]
	v_pk_fma_f32 v[200:201], v[148:149], v[34:35], v[200:201] op_sel:[0,0,0] op_sel_hi:[1,0,1]
	v_pk_fma_f32 v[202:203], v[150:151], v[34:35], v[202:203] op_sel:[0,0,0] op_sel_hi:[1,0,1]
	v_pk_fma_f32 v[204:205], v[152:153], v[34:35], v[204:205] op_sel:[0,0,0] op_sel_hi:[1,0,1]
	v_pk_fma_f32 v[198:199], v[86:87], v[34:35], v[198:199] op_sel:[0,1,0] op_sel_hi:[1,1,1]
	v_pk_fma_f32 v[200:201], v[88:89], v[34:35], v[200:201] op_sel:[0,1,0] op_sel_hi:[1,1,1]
	v_pk_fma_f32 v[202:203], v[90:91], v[34:35], v[202:203] op_sel:[0,1,0] op_sel_hi:[1,1,1]
	v_pk_fma_f32 v[204:205], v[92:93], v[34:35], v[204:205] op_sel:[0,1,0] op_sel_hi:[1,1,1]
	v_pk_fma_f32 v[198:199], v[148:149], v[36:37], v[198:199] op_sel:[0,0,0] op_sel_hi:[1,0,1]
	v_pk_fma_f32 v[200:201], v[150:151], v[36:37], v[200:201] op_sel:[0,0,0] op_sel_hi:[1,0,1]
	v_pk_fma_f32 v[202:203], v[152:153], v[36:37], v[202:203] op_sel:[0,0,0] op_sel_hi:[1,0,1]
	v_pk_fma_f32 v[204:205], v[154:155], v[36:37], v[204:205] op_sel:[0,0,0] op_sel_hi:[1,0,1]
	v_pk_fma_f32 v[198:199], v[88:89], v[28:29], v[198:199] op_sel:[0,0,0] op_sel_hi:[1,0,1]
	v_pk_fma_f32 v[200:201], v[90:91], v[28:29], v[200:201] op_sel:[0,0,0] op_sel_hi:[1,0,1]
	v_pk_fma_f32 v[202:203], v[92:93], v[28:29], v[202:203] op_sel:[0,0,0] op_sel_hi:[1,0,1]
	v_pk_fma_f32 v[204:205], v[94:95], v[28:29], v[204:205] op_sel:[0,0,0] op_sel_hi:[1,0,1]
	v_pk_fma_f32 v[198:199], v[150:151], v[36:37], v[198:199] op_sel:[0,1,0] op_sel_hi:[1,1,1]
	v_pk_fma_f32 v[200:201], v[152:153], v[36:37], v[200:201] op_sel:[0,1,0] op_sel_hi:[1,1,1]
	v_pk_fma_f32 v[202:203], v[154:155], v[36:37], v[202:203] op_sel:[0,1,0] op_sel_hi:[1,1,1]
	v_pk_fma_f32 v[204:205], v[156:157], v[36:37], v[204:205] op_sel:[0,1,0] op_sel_hi:[1,1,1]
	v_pk_fma_f32 v[198:199], v[90:91], v[38:39], v[198:199] op_sel:[0,0,0] op_sel_hi:[1,0,1]
	v_pk_fma_f32 v[200:201], v[92:93], v[38:39], v[200:201] op_sel:[0,0,0] op_sel_hi:[1,0,1]
	v_pk_fma_f32 v[202:203], v[94:95], v[38:39], v[202:203] op_sel:[0,0,0] op_sel_hi:[1,0,1]
	v_pk_fma_f32 v[204:205], v[96:97], v[38:39], v[204:205] op_sel:[0,0,0] op_sel_hi:[1,0,1]
	v_pk_fma_f32 v[198:199], v[152:153], v[38:39], v[198:199] op_sel:[0,1,0] op_sel_hi:[1,1,1]
	v_pk_fma_f32 v[200:201], v[154:155], v[38:39], v[200:201] op_sel:[0,1,0] op_sel_hi:[1,1,1]
	v_pk_fma_f32 v[202:203], v[156:157], v[38:39], v[202:203] op_sel:[0,1,0] op_sel_hi:[1,1,1]
	v_pk_fma_f32 v[204:205], v[158:159], v[38:39], v[204:205] op_sel:[0,1,0] op_sel_hi:[1,1,1]
	v_pk_fma_f32 v[198:199], v[92:93], v[28:29], v[198:199] op_sel:[0,1,0] op_sel_hi:[1,1,1]
	v_pk_fma_f32 v[200:201], v[94:95], v[28:29], v[200:201] op_sel:[0,1,0] op_sel_hi:[1,1,1]
	v_pk_fma_f32 v[202:203], v[96:97], v[28:29], v[202:203] op_sel:[0,1,0] op_sel_hi:[1,1,1]
	v_pk_fma_f32 v[204:205], v[98:99], v[28:29], v[204:205] op_sel:[0,1,0] op_sel_hi:[1,1,1]
	v_pk_fma_f32 v[198:199], v[154:155], v[40:41], v[198:199] op_sel:[0,0,0] op_sel_hi:[1,0,1]
; __device__ __forceinline__ void conv_phase(LAS unsigned char* lds, int tile, int tid, const bf16* __restrict__ U, const float* __restrict__ cw, const float* __restrict__ cb, ...
;     ...
;             for (int tk = 0; tk < HT; ++tk) { float a = bias;
; #pragma unroll
;                 for (int j = 0; j < CKW; ++j) a += w[j] * uc[tk + j];
;                 obuf[tk * CH + tid] = a; }
	v_pk_fma_f32 v[200:201], v[156:157], v[40:41], v[200:201] op_sel:[0,0,0] op_sel_hi:[1,0,1]
	v_pk_fma_f32 v[202:203], v[158:159], v[40:41], v[202:203] op_sel:[0,0,0] op_sel_hi:[1,0,1]
	v_pk_fma_f32 v[204:205], v[160:161], v[40:41], v[204:205] op_sel:[0,0,0] op_sel_hi:[1,0,1]
	v_pk_fma_f32 v[198:199], v[94:95], v[40:41], v[198:199] op_sel:[0,1,0] op_sel_hi:[1,1,1]
	v_pk_fma_f32 v[200:201], v[96:97], v[40:41], v[200:201] op_sel:[0,1,0] op_sel_hi:[1,1,1]
	v_pk_fma_f32 v[202:203], v[98:99], v[40:41], v[202:203] op_sel:[0,1,0] op_sel_hi:[1,1,1]
	v_pk_fma_f32 v[204:205], v[100:101], v[40:41], v[204:205] op_sel:[0,1,0] op_sel_hi:[1,1,1]
	v_pk_fma_f32 v[198:199], v[156:157], v[42:43], v[198:199] op_sel:[0,0,0] op_sel_hi:[1,0,1]
	v_pk_fma_f32 v[200:201], v[158:159], v[42:43], v[200:201] op_sel:[0,0,0] op_sel_hi:[1,0,1]
	v_pk_fma_f32 v[202:203], v[160:161], v[42:43], v[202:203] op_sel:[0,0,0] op_sel_hi:[1,0,1]
	v_pk_fma_f32 v[204:205], v[162:163], v[42:43], v[204:205] op_sel:[0,0,0] op_sel_hi:[1,0,1]
	v_pk_fma_f32 v[198:199], v[96:97], v[30:31], v[198:199] op_sel:[0,0,0] op_sel_hi:[1,0,1]
	v_pk_fma_f32 v[200:201], v[98:99], v[30:31], v[200:201] op_sel:[0,0,0] op_sel_hi:[1,0,1]
	v_pk_fma_f32 v[202:203], v[100:101], v[30:31], v[202:203] op_sel:[0,0,0] op_sel_hi:[1,0,1]
	v_pk_fma_f32 v[204:205], v[102:103], v[30:31], v[204:205] op_sel:[0,0,0] op_sel_hi:[1,0,1]
	v_pk_fma_f32 v[198:199], v[158:159], v[42:43], v[198:199] op_sel:[0,1,0] op_sel_hi:[1,1,1]
	v_pk_fma_f32 v[200:201], v[160:161], v[42:43], v[200:201] op_sel:[0,1,0] op_sel_hi:[1,1,1]
	v_pk_fma_f32 v[202:203], v[162:163], v[42:43], v[202:203] op_sel:[0,1,0] op_sel_hi:[1,1,1]
	v_pk_fma_f32 v[204:205], v[164:165], v[42:43], v[204:205] op_sel:[0,1,0] op_sel_hi:[1,1,1]
	v_pk_fma_f32 v[198:199], v[98:99], v[44:45], v[198:199] op_sel:[0,0,0] op_sel_hi:[1,0,1]
	v_pk_fma_f32 v[200:201], v[100:101], v[44:45], v[200:201] op_sel:[0,0,0] op_sel_hi:[1,0,1]
	v_pk_fma_f32 v[202:203], v[102:103], v[44:45], v[202:203] op_sel:[0,0,0] op_sel_hi:[1,0,1]
	v_pk_fma_f32 v[204:205], v[104:105], v[44:45], v[204:205] op_sel:[0,0,0] op_sel_hi:[1,0,1]
	v_pk_fma_f32 v[198:199], v[160:161], v[44:45], v[198:199] op_sel:[0,1,0] op_sel_hi:[1,1,1]
	v_pk_fma_f32 v[200:201], v[162:163], v[44:45], v[200:201] op_sel:[0,1,0] op_sel_hi:[1,1,1]
	v_pk_fma_f32 v[202:203], v[164:165], v[44:45], v[202:203] op_sel:[0,1,0] op_sel_hi:[1,1,1]
	v_pk_fma_f32 v[204:205], v[166:167], v[44:45], v[204:205] op_sel:[0,1,0] op_sel_hi:[1,1,1]
	v_pk_fma_f32 v[198:199], v[100:101], v[30:31], v[198:199] op_sel:[0,1,0] op_sel_hi:[1,1,1]
	v_pk_fma_f32 v[200:201], v[102:103], v[30:31], v[200:201] op_sel:[0,1,0] op_sel_hi:[1,1,1]
	v_pk_fma_f32 v[202:203], v[104:105], v[30:31], v[202:203] op_sel:[0,1,0] op_sel_hi:[1,1,1]
	v_pk_fma_f32 v[204:205], v[106:107], v[30:31], v[204:205] op_sel:[0,1,0] op_sel_hi:[1,1,1]
	v_pk_fma_f32 v[198:199], v[162:163], v[46:47], v[198:199] op_sel:[0,0,0] op_sel_hi:[1,0,1]
	v_pk_fma_f32 v[200:201], v[164:165], v[46:47], v[200:201] op_sel:[0,0,0] op_sel_hi:[1,0,1]
	v_pk_fma_f32 v[202:203], v[166:167], v[46:47], v[202:203] op_sel:[0,0,0] op_sel_hi:[1,0,1]
	v_pk_fma_f32 v[204:205], v[168:169], v[46:47], v[204:205] op_sel:[0,0,0] op_sel_hi:[1,0,1]
	v_pk_fma_f32 v[198:199], v[102:103], v[46:47], v[198:199] op_sel:[0,1,0] op_sel_hi:[1,1,1]
	v_pk_fma_f32 v[200:201], v[104:105], v[46:47], v[200:201] op_sel:[0,1,0] op_sel_hi:[1,1,1]
	v_pk_fma_f32 v[202:203], v[106:107], v[46:47], v[202:203] op_sel:[0,1,0] op_sel_hi:[1,1,1]
	v_pk_fma_f32 v[204:205], v[108:109], v[46:47], v[204:205] op_sel:[0,1,0] op_sel_hi:[1,1,1]
	v_pk_fma_f32 v[198:199], v[164:165], v[48:49], v[198:199] op_sel:[0,0,0] op_sel_hi:[1,0,1]
	v_pk_fma_f32 v[200:201], v[166:167], v[48:49], v[200:201] op_sel:[0,0,0] op_sel_hi:[1,0,1]
	v_pk_fma_f32 v[202:203], v[168:169], v[48:49], v[202:203] op_sel:[0,0,0] op_sel_hi:[1,0,1]
	v_pk_fma_f32 v[204:205], v[170:171], v[48:49], v[204:205] op_sel:[0,0,0] op_sel_hi:[1,0,1]
	v_pk_fma_f32 v[198:199], v[104:105], v[48:49], v[198:199] op_sel:[0,1,0] op_sel_hi:[1,1,1]
	v_pk_fma_f32 v[200:201], v[106:107], v[48:49], v[200:201] op_sel:[0,1,0] op_sel_hi:[1,1,1]
	v_pk_fma_f32 v[202:203], v[108:109], v[48:49], v[202:203] op_sel:[0,1,0] op_sel_hi:[1,1,1]
	v_pk_fma_f32 v[204:205], v[110:111], v[48:49], v[204:205] op_sel:[0,1,0] op_sel_hi:[1,1,1]
	v_pk_fma_f32 v[198:199], v[166:167], v[50:51], v[198:199] op_sel:[0,1,0] op_sel_hi:[1,1,1]
	v_pk_fma_f32 v[200:201], v[168:169], v[50:51], v[200:201] op_sel:[0,1,0] op_sel_hi:[1,1,1]
	v_pk_fma_f32 v[202:203], v[170:171], v[50:51], v[202:203] op_sel:[0,1,0] op_sel_hi:[1,1,1]
	v_pk_fma_f32 v[204:205], v[172:173], v[50:51], v[204:205] op_sel:[0,1,0] op_sel_hi:[1,1,1]
	v_pk_fma_f32 v[198:199], v[106:107], v[52:53], v[198:199] op_sel:[0,0,0] op_sel_hi:[1,0,1]
	v_pk_fma_f32 v[200:201], v[108:109], v[52:53], v[200:201] op_sel:[0,0,0] op_sel_hi:[1,0,1]
	v_pk_fma_f32 v[202:203], v[110:111], v[52:53], v[202:203] op_sel:[0,0,0] op_sel_hi:[1,0,1]
	v_pk_fma_f32 v[204:205], v[112:113], v[52:53], v[204:205] op_sel:[0,0,0] op_sel_hi:[1,0,1]
	v_pk_fma_f32 v[198:199], v[168:169], v[52:53], v[198:199] op_sel:[0,1,0] op_sel_hi:[1,1,1]
	v_pk_fma_f32 v[200:201], v[170:171], v[52:53], v[200:201] op_sel:[0,1,0] op_sel_hi:[1,1,1]
	v_pk_fma_f32 v[202:203], v[172:173], v[52:53], v[202:203] op_sel:[0,1,0] op_sel_hi:[1,1,1]
	v_pk_fma_f32 v[204:205], v[174:175], v[52:53], v[204:205] op_sel:[0,1,0] op_sel_hi:[1,1,1]
	v_pk_fma_f32 v[198:199], v[108:109], v[50:51], v[198:199] op_sel:[0,0,0] op_sel_hi:[1,0,1]
	v_pk_fma_f32 v[200:201], v[110:111], v[50:51], v[200:201] op_sel:[0,0,0] op_sel_hi:[1,0,1]
; __device__ __forceinline__ void conv_phase(LAS unsigned char* lds, int tile, int tid, const bf16* __restrict__ U, const float* __restrict__ cw, const float* __restrict__ cb, ...
;     ...
;             for (int tk = 0; tk < HT; ++tk) { float a = bias;
; #pragma unroll
;                 for (int j = 0; j < CKW; ++j) a += w[j] * uc[tk + j];
;                 obuf[tk * CH + tid] = a; }
	v_pk_fma_f32 v[202:203], v[112:113], v[50:51], v[202:203] op_sel:[0,0,0] op_sel_hi:[1,0,1]
	v_pk_fma_f32 v[204:205], v[114:115], v[50:51], v[204:205] op_sel:[0,0,0] op_sel_hi:[1,0,1]
	v_pk_fma_f32 v[198:199], v[170:171], v[54:55], v[198:199] op_sel:[0,0,0] op_sel_hi:[1,0,1]
	v_pk_fma_f32 v[200:201], v[172:173], v[54:55], v[200:201] op_sel:[0,0,0] op_sel_hi:[1,0,1]
	v_pk_fma_f32 v[202:203], v[174:175], v[54:55], v[202:203] op_sel:[0,0,0] op_sel_hi:[1,0,1]
	v_pk_fma_f32 v[204:205], v[176:177], v[54:55], v[204:205] op_sel:[0,0,0] op_sel_hi:[1,0,1]
	v_pk_fma_f32 v[198:199], v[110:111], v[54:55], v[198:199] op_sel:[0,1,0] op_sel_hi:[1,1,1]
	v_pk_fma_f32 v[200:201], v[112:113], v[54:55], v[200:201] op_sel:[0,1,0] op_sel_hi:[1,1,1]
	v_pk_fma_f32 v[202:203], v[114:115], v[54:55], v[202:203] op_sel:[0,1,0] op_sel_hi:[1,1,1]
	v_pk_fma_f32 v[204:205], v[116:117], v[54:55], v[204:205] op_sel:[0,1,0] op_sel_hi:[1,1,1]
	ds_write2st64_b32 v64, v198, v199 offset0:64 offset1:72
	ds_write2st64_b32 v64, v200, v201 offset0:80 offset1:88
	ds_write2st64_b32 v64, v202, v203 offset0:96 offset1:104
	ds_write2st64_b32 v64, v204, v205 offset0:112 offset1:120
	v_pk_fma_f32 v[198:199], v[88:89], v[18:19], v[56:57] op_sel:[0,1,0] op_sel_hi:[1,1,0]
	v_pk_fma_f32 v[200:201], v[90:91], v[18:19], v[56:57] op_sel:[0,1,0] op_sel_hi:[1,1,0]
	v_pk_fma_f32 v[202:203], v[92:93], v[18:19], v[56:57] op_sel:[0,1,0] op_sel_hi:[1,1,0]
	v_pk_fma_f32 v[204:205], v[94:95], v[18:19], v[56:57] op_sel:[0,1,0] op_sel_hi:[1,1,0]
	v_pk_fma_f32 v[198:199], v[150:151], v[32:33], v[198:199] op_sel:[0,0,0] op_sel_hi:[1,0,1]
	v_pk_fma_f32 v[200:201], v[152:153], v[32:33], v[200:201] op_sel:[0,0,0] op_sel_hi:[1,0,1]
	v_pk_fma_f32 v[202:203], v[154:155], v[32:33], v[202:203] op_sel:[0,0,0] op_sel_hi:[1,0,1]
	v_pk_fma_f32 v[204:205], v[156:157], v[32:33], v[204:205] op_sel:[0,0,0] op_sel_hi:[1,0,1]
	v_pk_fma_f32 v[198:199], v[90:91], v[26:27], v[198:199] op_sel:[0,0,0] op_sel_hi:[1,0,1]
	v_pk_fma_f32 v[200:201], v[92:93], v[26:27], v[200:201] op_sel:[0,0,0] op_sel_hi:[1,0,1]
	v_pk_fma_f32 v[202:203], v[94:95], v[26:27], v[202:203] op_sel:[0,0,0] op_sel_hi:[1,0,1]
	v_pk_fma_f32 v[204:205], v[96:97], v[26:27], v[204:205] op_sel:[0,0,0] op_sel_hi:[1,0,1]
	v_pk_fma_f32 v[198:199], v[152:153], v[32:33], v[198:199] op_sel:[0,1,0] op_sel_hi:[1,1,1]
	v_pk_fma_f32 v[200:201], v[154:155], v[32:33], v[200:201] op_sel:[0,1,0] op_sel_hi:[1,1,1]
	v_pk_fma_f32 v[202:203], v[156:157], v[32:33], v[202:203] op_sel:[0,1,0] op_sel_hi:[1,1,1]
	v_pk_fma_f32 v[204:205], v[158:159], v[32:33], v[204:205] op_sel:[0,1,0] op_sel_hi:[1,1,1]
	v_pk_fma_f32 v[198:199], v[92:93], v[26:27], v[198:199] op_sel:[0,1,0] op_sel_hi:[1,1,1]
	v_pk_fma_f32 v[200:201], v[94:95], v[26:27], v[200:201] op_sel:[0,1,0] op_sel_hi:[1,1,1]
	v_pk_fma_f32 v[202:203], v[96:97], v[26:27], v[202:203] op_sel:[0,1,0] op_sel_hi:[1,1,1]
	v_pk_fma_f32 v[204:205], v[98:99], v[26:27], v[204:205] op_sel:[0,1,0] op_sel_hi:[1,1,1]
	v_pk_fma_f32 v[198:199], v[154:155], v[34:35], v[198:199] op_sel:[0,0,0] op_sel_hi:[1,0,1]
	v_pk_fma_f32 v[200:201], v[156:157], v[34:35], v[200:201] op_sel:[0,0,0] op_sel_hi:[1,0,1]
	v_pk_fma_f32 v[202:203], v[158:159], v[34:35], v[202:203] op_sel:[0,0,0] op_sel_hi:[1,0,1]
	v_pk_fma_f32 v[204:205], v[160:161], v[34:35], v[204:205] op_sel:[0,0,0] op_sel_hi:[1,0,1]
	v_pk_fma_f32 v[198:199], v[94:95], v[34:35], v[198:199] op_sel:[0,1,0] op_sel_hi:[1,1,1]
	v_pk_fma_f32 v[200:201], v[96:97], v[34:35], v[200:201] op_sel:[0,1,0] op_sel_hi:[1,1,1]
	v_pk_fma_f32 v[202:203], v[98:99], v[34:35], v[202:203] op_sel:[0,1,0] op_sel_hi:[1,1,1]
	v_pk_fma_f32 v[204:205], v[100:101], v[34:35], v[204:205] op_sel:[0,1,0] op_sel_hi:[1,1,1]
	v_pk_fma_f32 v[198:199], v[156:157], v[36:37], v[198:199] op_sel:[0,0,0] op_sel_hi:[1,0,1]
	v_pk_fma_f32 v[200:201], v[158:159], v[36:37], v[200:201] op_sel:[0,0,0] op_sel_hi:[1,0,1]
	v_pk_fma_f32 v[202:203], v[160:161], v[36:37], v[202:203] op_sel:[0,0,0] op_sel_hi:[1,0,1]
	v_pk_fma_f32 v[204:205], v[162:163], v[36:37], v[204:205] op_sel:[0,0,0] op_sel_hi:[1,0,1]
	v_pk_fma_f32 v[198:199], v[96:97], v[28:29], v[198:199] op_sel:[0,0,0] op_sel_hi:[1,0,1]
	v_pk_fma_f32 v[200:201], v[98:99], v[28:29], v[200:201] op_sel:[0,0,0] op_sel_hi:[1,0,1]
	v_pk_fma_f32 v[202:203], v[100:101], v[28:29], v[202:203] op_sel:[0,0,0] op_sel_hi:[1,0,1]
	v_pk_fma_f32 v[204:205], v[102:103], v[28:29], v[204:205] op_sel:[0,0,0] op_sel_hi:[1,0,1]
	v_pk_fma_f32 v[198:199], v[158:159], v[36:37], v[198:199] op_sel:[0,1,0] op_sel_hi:[1,1,1]
	v_pk_fma_f32 v[200:201], v[160:161], v[36:37], v[200:201] op_sel:[0,1,0] op_sel_hi:[1,1,1]
	v_pk_fma_f32 v[202:203], v[162:163], v[36:37], v[202:203] op_sel:[0,1,0] op_sel_hi:[1,1,1]
	v_pk_fma_f32 v[204:205], v[164:165], v[36:37], v[204:205] op_sel:[0,1,0] op_sel_hi:[1,1,1]
	v_pk_fma_f32 v[198:199], v[98:99], v[38:39], v[198:199] op_sel:[0,0,0] op_sel_hi:[1,0,1]
	v_pk_fma_f32 v[200:201], v[100:101], v[38:39], v[200:201] op_sel:[0,0,0] op_sel_hi:[1,0,1]
	v_pk_fma_f32 v[202:203], v[102:103], v[38:39], v[202:203] op_sel:[0,0,0] op_sel_hi:[1,0,1]
	v_pk_fma_f32 v[204:205], v[104:105], v[38:39], v[204:205] op_sel:[0,0,0] op_sel_hi:[1,0,1]
	v_pk_fma_f32 v[198:199], v[160:161], v[38:39], v[198:199] op_sel:[0,1,0] op_sel_hi:[1,1,1]
	v_pk_fma_f32 v[200:201], v[162:163], v[38:39], v[200:201] op_sel:[0,1,0] op_sel_hi:[1,1,1]
	v_pk_fma_f32 v[202:203], v[164:165], v[38:39], v[202:203] op_sel:[0,1,0] op_sel_hi:[1,1,1]
	v_pk_fma_f32 v[204:205], v[166:167], v[38:39], v[204:205] op_sel:[0,1,0] op_sel_hi:[1,1,1]
	v_pk_fma_f32 v[198:199], v[100:101], v[28:29], v[198:199] op_sel:[0,1,0] op_sel_hi:[1,1,1]
; __device__ __forceinline__ void conv_phase(LAS unsigned char* lds, int tile, int tid, const bf16* __restrict__ U, const float* __restrict__ cw, const float* __restrict__ cb, ...
;     ...
;             for (int tk = 0; tk < HT; ++tk) { float a = bias;
; #pragma unroll
;                 for (int j = 0; j < CKW; ++j) a += w[j] * uc[tk + j];
;                 obuf[tk * CH + tid] = a; }
	v_pk_fma_f32 v[200:201], v[102:103], v[28:29], v[200:201] op_sel:[0,1,0] op_sel_hi:[1,1,1]
	v_pk_fma_f32 v[202:203], v[104:105], v[28:29], v[202:203] op_sel:[0,1,0] op_sel_hi:[1,1,1]
	v_pk_fma_f32 v[204:205], v[106:107], v[28:29], v[204:205] op_sel:[0,1,0] op_sel_hi:[1,1,1]
	v_pk_fma_f32 v[198:199], v[162:163], v[40:41], v[198:199] op_sel:[0,0,0] op_sel_hi:[1,0,1]
	v_pk_fma_f32 v[200:201], v[164:165], v[40:41], v[200:201] op_sel:[0,0,0] op_sel_hi:[1,0,1]
	v_pk_fma_f32 v[202:203], v[166:167], v[40:41], v[202:203] op_sel:[0,0,0] op_sel_hi:[1,0,1]
	v_pk_fma_f32 v[204:205], v[168:169], v[40:41], v[204:205] op_sel:[0,0,0] op_sel_hi:[1,0,1]
	v_pk_fma_f32 v[198:199], v[102:103], v[40:41], v[198:199] op_sel:[0,1,0] op_sel_hi:[1,1,1]
	v_pk_fma_f32 v[200:201], v[104:105], v[40:41], v[200:201] op_sel:[0,1,0] op_sel_hi:[1,1,1]
	v_pk_fma_f32 v[202:203], v[106:107], v[40:41], v[202:203] op_sel:[0,1,0] op_sel_hi:[1,1,1]
	v_pk_fma_f32 v[204:205], v[108:109], v[40:41], v[204:205] op_sel:[0,1,0] op_sel_hi:[1,1,1]
	v_pk_fma_f32 v[198:199], v[164:165], v[42:43], v[198:199] op_sel:[0,0,0] op_sel_hi:[1,0,1]
	v_pk_fma_f32 v[200:201], v[166:167], v[42:43], v[200:201] op_sel:[0,0,0] op_sel_hi:[1,0,1]
	v_pk_fma_f32 v[202:203], v[168:169], v[42:43], v[202:203] op_sel:[0,0,0] op_sel_hi:[1,0,1]
	v_pk_fma_f32 v[204:205], v[170:171], v[42:43], v[204:205] op_sel:[0,0,0] op_sel_hi:[1,0,1]
	v_pk_fma_f32 v[198:199], v[104:105], v[30:31], v[198:199] op_sel:[0,0,0] op_sel_hi:[1,0,1]
	v_pk_fma_f32 v[200:201], v[106:107], v[30:31], v[200:201] op_sel:[0,0,0] op_sel_hi:[1,0,1]
	v_pk_fma_f32 v[202:203], v[108:109], v[30:31], v[202:203] op_sel:[0,0,0] op_sel_hi:[1,0,1]
	v_pk_fma_f32 v[204:205], v[110:111], v[30:31], v[204:205] op_sel:[0,0,0] op_sel_hi:[1,0,1]
	v_pk_fma_f32 v[198:199], v[166:167], v[42:43], v[198:199] op_sel:[0,1,0] op_sel_hi:[1,1,1]
	v_pk_fma_f32 v[200:201], v[168:169], v[42:43], v[200:201] op_sel:[0,1,0] op_sel_hi:[1,1,1]
	v_pk_fma_f32 v[202:203], v[170:171], v[42:43], v[202:203] op_sel:[0,1,0] op_sel_hi:[1,1,1]
	v_pk_fma_f32 v[204:205], v[172:173], v[42:43], v[204:205] op_sel:[0,1,0] op_sel_hi:[1,1,1]
	v_pk_fma_f32 v[198:199], v[106:107], v[44:45], v[198:199] op_sel:[0,0,0] op_sel_hi:[1,0,1]
	v_pk_fma_f32 v[200:201], v[108:109], v[44:45], v[200:201] op_sel:[0,0,0] op_sel_hi:[1,0,1]
	v_pk_fma_f32 v[202:203], v[110:111], v[44:45], v[202:203] op_sel:[0,0,0] op_sel_hi:[1,0,1]
	v_pk_fma_f32 v[204:205], v[112:113], v[44:45], v[204:205] op_sel:[0,0,0] op_sel_hi:[1,0,1]
	v_pk_fma_f32 v[198:199], v[168:169], v[44:45], v[198:199] op_sel:[0,1,0] op_sel_hi:[1,1,1]
	v_pk_fma_f32 v[200:201], v[170:171], v[44:45], v[200:201] op_sel:[0,1,0] op_sel_hi:[1,1,1]
	v_pk_fma_f32 v[202:203], v[172:173], v[44:45], v[202:203] op_sel:[0,1,0] op_sel_hi:[1,1,1]
	v_pk_fma_f32 v[204:205], v[174:175], v[44:45], v[204:205] op_sel:[0,1,0] op_sel_hi:[1,1,1]
	v_pk_fma_f32 v[198:199], v[108:109], v[30:31], v[198:199] op_sel:[0,1,0] op_sel_hi:[1,1,1]
	v_pk_fma_f32 v[200:201], v[110:111], v[30:31], v[200:201] op_sel:[0,1,0] op_sel_hi:[1,1,1]
	v_pk_fma_f32 v[202:203], v[112:113], v[30:31], v[202:203] op_sel:[0,1,0] op_sel_hi:[1,1,1]
	v_pk_fma_f32 v[204:205], v[114:115], v[30:31], v[204:205] op_sel:[0,1,0] op_sel_hi:[1,1,1]
	v_pk_fma_f32 v[198:199], v[170:171], v[46:47], v[198:199] op_sel:[0,0,0] op_sel_hi:[1,0,1]
	v_pk_fma_f32 v[200:201], v[172:173], v[46:47], v[200:201] op_sel:[0,0,0] op_sel_hi:[1,0,1]
	v_pk_fma_f32 v[202:203], v[174:175], v[46:47], v[202:203] op_sel:[0,0,0] op_sel_hi:[1,0,1]
	v_pk_fma_f32 v[204:205], v[176:177], v[46:47], v[204:205] op_sel:[0,0,0] op_sel_hi:[1,0,1]
	v_pk_fma_f32 v[198:199], v[110:111], v[46:47], v[198:199] op_sel:[0,1,0] op_sel_hi:[1,1,1]
	v_pk_fma_f32 v[200:201], v[112:113], v[46:47], v[200:201] op_sel:[0,1,0] op_sel_hi:[1,1,1]
	v_pk_fma_f32 v[202:203], v[114:115], v[46:47], v[202:203] op_sel:[0,1,0] op_sel_hi:[1,1,1]
	v_pk_fma_f32 v[204:205], v[116:117], v[46:47], v[204:205] op_sel:[0,1,0] op_sel_hi:[1,1,1]
	v_pk_fma_f32 v[198:199], v[172:173], v[48:49], v[198:199] op_sel:[0,0,0] op_sel_hi:[1,0,1]
	v_pk_fma_f32 v[200:201], v[174:175], v[48:49], v[200:201] op_sel:[0,0,0] op_sel_hi:[1,0,1]
	v_pk_fma_f32 v[202:203], v[176:177], v[48:49], v[202:203] op_sel:[0,0,0] op_sel_hi:[1,0,1]
	v_pk_fma_f32 v[204:205], v[178:179], v[48:49], v[204:205] op_sel:[0,0,0] op_sel_hi:[1,0,1]
	v_pk_fma_f32 v[198:199], v[112:113], v[48:49], v[198:199] op_sel:[0,1,0] op_sel_hi:[1,1,1]
	v_pk_fma_f32 v[200:201], v[114:115], v[48:49], v[200:201] op_sel:[0,1,0] op_sel_hi:[1,1,1]
	v_pk_fma_f32 v[202:203], v[116:117], v[48:49], v[202:203] op_sel:[0,1,0] op_sel_hi:[1,1,1]
	v_pk_fma_f32 v[204:205], v[118:119], v[48:49], v[204:205] op_sel:[0,1,0] op_sel_hi:[1,1,1]
	v_pk_fma_f32 v[198:199], v[174:175], v[50:51], v[198:199] op_sel:[0,1,0] op_sel_hi:[1,1,1]
	v_pk_fma_f32 v[200:201], v[176:177], v[50:51], v[200:201] op_sel:[0,1,0] op_sel_hi:[1,1,1]
	v_pk_fma_f32 v[202:203], v[178:179], v[50:51], v[202:203] op_sel:[0,1,0] op_sel_hi:[1,1,1]
	v_pk_fma_f32 v[204:205], v[180:181], v[50:51], v[204:205] op_sel:[0,1,0] op_sel_hi:[1,1,1]
	v_pk_fma_f32 v[198:199], v[114:115], v[52:53], v[198:199] op_sel:[0,0,0] op_sel_hi:[1,0,1]
	v_pk_fma_f32 v[200:201], v[116:117], v[52:53], v[200:201] op_sel:[0,0,0] op_sel_hi:[1,0,1]
	v_pk_fma_f32 v[202:203], v[118:119], v[52:53], v[202:203] op_sel:[0,0,0] op_sel_hi:[1,0,1]
	v_pk_fma_f32 v[204:205], v[120:121], v[52:53], v[204:205] op_sel:[0,0,0] op_sel_hi:[1,0,1]
	v_pk_fma_f32 v[198:199], v[176:177], v[52:53], v[198:199] op_sel:[0,1,0] op_sel_hi:[1,1,1]
	v_pk_fma_f32 v[200:201], v[178:179], v[52:53], v[200:201] op_sel:[0,1,0] op_sel_hi:[1,1,1]
; __device__ __forceinline__ void conv_phase(LAS unsigned char* lds, int tile, int tid, const bf16* __restrict__ U, const float* __restrict__ cw, const float* __restrict__ cb, ...
;     ...
;             for (int tk = 0; tk < HT; ++tk) { float a = bias;
; #pragma unroll
;                 for (int j = 0; j < CKW; ++j) a += w[j] * uc[tk + j];
;                 obuf[tk * CH + tid] = a; }
	v_pk_fma_f32 v[202:203], v[180:181], v[52:53], v[202:203] op_sel:[0,1,0] op_sel_hi:[1,1,1]
	v_pk_fma_f32 v[204:205], v[182:183], v[52:53], v[204:205] op_sel:[0,1,0] op_sel_hi:[1,1,1]
	v_pk_fma_f32 v[198:199], v[116:117], v[50:51], v[198:199] op_sel:[0,0,0] op_sel_hi:[1,0,1]
	v_pk_fma_f32 v[200:201], v[118:119], v[50:51], v[200:201] op_sel:[0,0,0] op_sel_hi:[1,0,1]
	v_pk_fma_f32 v[202:203], v[120:121], v[50:51], v[202:203] op_sel:[0,0,0] op_sel_hi:[1,0,1]
	v_pk_fma_f32 v[204:205], v[122:123], v[50:51], v[204:205] op_sel:[0,0,0] op_sel_hi:[1,0,1]
	v_pk_fma_f32 v[198:199], v[178:179], v[54:55], v[198:199] op_sel:[0,0,0] op_sel_hi:[1,0,1]
	v_pk_fma_f32 v[200:201], v[180:181], v[54:55], v[200:201] op_sel:[0,0,0] op_sel_hi:[1,0,1]
	v_pk_fma_f32 v[202:203], v[182:183], v[54:55], v[202:203] op_sel:[0,0,0] op_sel_hi:[1,0,1]
	v_pk_fma_f32 v[204:205], v[184:185], v[54:55], v[204:205] op_sel:[0,0,0] op_sel_hi:[1,0,1]
	v_pk_fma_f32 v[198:199], v[118:119], v[54:55], v[198:199] op_sel:[0,1,0] op_sel_hi:[1,1,1]
	v_pk_fma_f32 v[200:201], v[120:121], v[54:55], v[200:201] op_sel:[0,1,0] op_sel_hi:[1,1,1]
	v_pk_fma_f32 v[202:203], v[122:123], v[54:55], v[202:203] op_sel:[0,1,0] op_sel_hi:[1,1,1]
	v_pk_fma_f32 v[204:205], v[124:125], v[54:55], v[204:205] op_sel:[0,1,0] op_sel_hi:[1,1,1]
	ds_write2st64_b32 v64, v198, v199 offset0:128 offset1:136
	ds_write2st64_b32 v64, v200, v201 offset0:144 offset1:152
	ds_write2st64_b32 v64, v202, v203 offset0:160 offset1:168
	ds_write2st64_b32 v64, v204, v205 offset0:176 offset1:184
	v_pk_fma_f32 v[198:199], v[96:97], v[18:19], v[56:57] op_sel:[0,1,0] op_sel_hi:[1,1,0]
	v_pk_fma_f32 v[200:201], v[98:99], v[18:19], v[56:57] op_sel:[0,1,0] op_sel_hi:[1,1,0]
	v_pk_fma_f32 v[202:203], v[100:101], v[18:19], v[56:57] op_sel:[0,1,0] op_sel_hi:[1,1,0]
	v_pk_fma_f32 v[204:205], v[102:103], v[18:19], v[56:57] op_sel:[0,1,0] op_sel_hi:[1,1,0]
	v_pk_fma_f32 v[198:199], v[158:159], v[32:33], v[198:199] op_sel:[0,0,0] op_sel_hi:[1,0,1]
	v_pk_fma_f32 v[200:201], v[160:161], v[32:33], v[200:201] op_sel:[0,0,0] op_sel_hi:[1,0,1]
	v_pk_fma_f32 v[202:203], v[162:163], v[32:33], v[202:203] op_sel:[0,0,0] op_sel_hi:[1,0,1]
	v_pk_fma_f32 v[204:205], v[164:165], v[32:33], v[204:205] op_sel:[0,0,0] op_sel_hi:[1,0,1]
	v_pk_fma_f32 v[198:199], v[98:99], v[26:27], v[198:199] op_sel:[0,0,0] op_sel_hi:[1,0,1]
	v_pk_fma_f32 v[200:201], v[100:101], v[26:27], v[200:201] op_sel:[0,0,0] op_sel_hi:[1,0,1]
	v_pk_fma_f32 v[202:203], v[102:103], v[26:27], v[202:203] op_sel:[0,0,0] op_sel_hi:[1,0,1]
	v_pk_fma_f32 v[204:205], v[104:105], v[26:27], v[204:205] op_sel:[0,0,0] op_sel_hi:[1,0,1]
	v_pk_fma_f32 v[198:199], v[160:161], v[32:33], v[198:199] op_sel:[0,1,0] op_sel_hi:[1,1,1]
	v_pk_fma_f32 v[200:201], v[162:163], v[32:33], v[200:201] op_sel:[0,1,0] op_sel_hi:[1,1,1]
	v_pk_fma_f32 v[202:203], v[164:165], v[32:33], v[202:203] op_sel:[0,1,0] op_sel_hi:[1,1,1]
	v_pk_fma_f32 v[204:205], v[166:167], v[32:33], v[204:205] op_sel:[0,1,0] op_sel_hi:[1,1,1]
	v_pk_fma_f32 v[198:199], v[100:101], v[26:27], v[198:199] op_sel:[0,1,0] op_sel_hi:[1,1,1]
	v_pk_fma_f32 v[200:201], v[102:103], v[26:27], v[200:201] op_sel:[0,1,0] op_sel_hi:[1,1,1]
	v_pk_fma_f32 v[202:203], v[104:105], v[26:27], v[202:203] op_sel:[0,1,0] op_sel_hi:[1,1,1]
	v_pk_fma_f32 v[204:205], v[106:107], v[26:27], v[204:205] op_sel:[0,1,0] op_sel_hi:[1,1,1]
	v_pk_fma_f32 v[198:199], v[162:163], v[34:35], v[198:199] op_sel:[0,0,0] op_sel_hi:[1,0,1]
	v_pk_fma_f32 v[200:201], v[164:165], v[34:35], v[200:201] op_sel:[0,0,0] op_sel_hi:[1,0,1]
	v_pk_fma_f32 v[202:203], v[166:167], v[34:35], v[202:203] op_sel:[0,0,0] op_sel_hi:[1,0,1]
	v_pk_fma_f32 v[204:205], v[168:169], v[34:35], v[204:205] op_sel:[0,0,0] op_sel_hi:[1,0,1]
	v_pk_fma_f32 v[198:199], v[102:103], v[34:35], v[198:199] op_sel:[0,1,0] op_sel_hi:[1,1,1]
	v_pk_fma_f32 v[200:201], v[104:105], v[34:35], v[200:201] op_sel:[0,1,0] op_sel_hi:[1,1,1]
	v_pk_fma_f32 v[202:203], v[106:107], v[34:35], v[202:203] op_sel:[0,1,0] op_sel_hi:[1,1,1]
	v_pk_fma_f32 v[204:205], v[108:109], v[34:35], v[204:205] op_sel:[0,1,0] op_sel_hi:[1,1,1]
	v_pk_fma_f32 v[198:199], v[164:165], v[36:37], v[198:199] op_sel:[0,0,0] op_sel_hi:[1,0,1]
	v_pk_fma_f32 v[200:201], v[166:167], v[36:37], v[200:201] op_sel:[0,0,0] op_sel_hi:[1,0,1]
	v_pk_fma_f32 v[202:203], v[168:169], v[36:37], v[202:203] op_sel:[0,0,0] op_sel_hi:[1,0,1]
	v_pk_fma_f32 v[204:205], v[170:171], v[36:37], v[204:205] op_sel:[0,0,0] op_sel_hi:[1,0,1]
	v_pk_fma_f32 v[198:199], v[104:105], v[28:29], v[198:199] op_sel:[0,0,0] op_sel_hi:[1,0,1]
	v_pk_fma_f32 v[200:201], v[106:107], v[28:29], v[200:201] op_sel:[0,0,0] op_sel_hi:[1,0,1]
	v_pk_fma_f32 v[202:203], v[108:109], v[28:29], v[202:203] op_sel:[0,0,0] op_sel_hi:[1,0,1]
	v_pk_fma_f32 v[204:205], v[110:111], v[28:29], v[204:205] op_sel:[0,0,0] op_sel_hi:[1,0,1]
	v_pk_fma_f32 v[198:199], v[166:167], v[36:37], v[198:199] op_sel:[0,1,0] op_sel_hi:[1,1,1]
	v_pk_fma_f32 v[200:201], v[168:169], v[36:37], v[200:201] op_sel:[0,1,0] op_sel_hi:[1,1,1]
	v_pk_fma_f32 v[202:203], v[170:171], v[36:37], v[202:203] op_sel:[0,1,0] op_sel_hi:[1,1,1]
	v_pk_fma_f32 v[204:205], v[172:173], v[36:37], v[204:205] op_sel:[0,1,0] op_sel_hi:[1,1,1]
	v_pk_fma_f32 v[198:199], v[106:107], v[38:39], v[198:199] op_sel:[0,0,0] op_sel_hi:[1,0,1]
	v_pk_fma_f32 v[200:201], v[108:109], v[38:39], v[200:201] op_sel:[0,0,0] op_sel_hi:[1,0,1]
	v_pk_fma_f32 v[202:203], v[110:111], v[38:39], v[202:203] op_sel:[0,0,0] op_sel_hi:[1,0,1]
	v_pk_fma_f32 v[204:205], v[112:113], v[38:39], v[204:205] op_sel:[0,0,0] op_sel_hi:[1,0,1]
	v_pk_fma_f32 v[198:199], v[168:169], v[38:39], v[198:199] op_sel:[0,1,0] op_sel_hi:[1,1,1]
; __device__ __forceinline__ void conv_phase(LAS unsigned char* lds, int tile, int tid, const bf16* __restrict__ U, const float* __restrict__ cw, const float* __restrict__ cb, ...
;     ...
;             for (int tk = 0; tk < HT; ++tk) { float a = bias;
; #pragma unroll
;                 for (int j = 0; j < CKW; ++j) a += w[j] * uc[tk + j];
;                 obuf[tk * CH + tid] = a; }
	v_pk_fma_f32 v[200:201], v[170:171], v[38:39], v[200:201] op_sel:[0,1,0] op_sel_hi:[1,1,1]
	v_pk_fma_f32 v[202:203], v[172:173], v[38:39], v[202:203] op_sel:[0,1,0] op_sel_hi:[1,1,1]
	v_pk_fma_f32 v[204:205], v[174:175], v[38:39], v[204:205] op_sel:[0,1,0] op_sel_hi:[1,1,1]
	v_pk_fma_f32 v[198:199], v[108:109], v[28:29], v[198:199] op_sel:[0,1,0] op_sel_hi:[1,1,1]
	v_pk_fma_f32 v[200:201], v[110:111], v[28:29], v[200:201] op_sel:[0,1,0] op_sel_hi:[1,1,1]
	v_pk_fma_f32 v[202:203], v[112:113], v[28:29], v[202:203] op_sel:[0,1,0] op_sel_hi:[1,1,1]
	v_pk_fma_f32 v[204:205], v[114:115], v[28:29], v[204:205] op_sel:[0,1,0] op_sel_hi:[1,1,1]
	v_pk_fma_f32 v[198:199], v[170:171], v[40:41], v[198:199] op_sel:[0,0,0] op_sel_hi:[1,0,1]
	v_pk_fma_f32 v[200:201], v[172:173], v[40:41], v[200:201] op_sel:[0,0,0] op_sel_hi:[1,0,1]
	v_pk_fma_f32 v[202:203], v[174:175], v[40:41], v[202:203] op_sel:[0,0,0] op_sel_hi:[1,0,1]
	v_pk_fma_f32 v[204:205], v[176:177], v[40:41], v[204:205] op_sel:[0,0,0] op_sel_hi:[1,0,1]
	v_pk_fma_f32 v[198:199], v[110:111], v[40:41], v[198:199] op_sel:[0,1,0] op_sel_hi:[1,1,1]
	v_pk_fma_f32 v[200:201], v[112:113], v[40:41], v[200:201] op_sel:[0,1,0] op_sel_hi:[1,1,1]
	v_pk_fma_f32 v[202:203], v[114:115], v[40:41], v[202:203] op_sel:[0,1,0] op_sel_hi:[1,1,1]
	v_pk_fma_f32 v[204:205], v[116:117], v[40:41], v[204:205] op_sel:[0,1,0] op_sel_hi:[1,1,1]
	v_pk_fma_f32 v[198:199], v[172:173], v[42:43], v[198:199] op_sel:[0,0,0] op_sel_hi:[1,0,1]
	v_pk_fma_f32 v[200:201], v[174:175], v[42:43], v[200:201] op_sel:[0,0,0] op_sel_hi:[1,0,1]
	v_pk_fma_f32 v[202:203], v[176:177], v[42:43], v[202:203] op_sel:[0,0,0] op_sel_hi:[1,0,1]
	v_pk_fma_f32 v[204:205], v[178:179], v[42:43], v[204:205] op_sel:[0,0,0] op_sel_hi:[1,0,1]
	v_pk_fma_f32 v[198:199], v[112:113], v[30:31], v[198:199] op_sel:[0,0,0] op_sel_hi:[1,0,1]
	v_pk_fma_f32 v[200:201], v[114:115], v[30:31], v[200:201] op_sel:[0,0,0] op_sel_hi:[1,0,1]
	v_pk_fma_f32 v[202:203], v[116:117], v[30:31], v[202:203] op_sel:[0,0,0] op_sel_hi:[1,0,1]
	v_pk_fma_f32 v[204:205], v[118:119], v[30:31], v[204:205] op_sel:[0,0,0] op_sel_hi:[1,0,1]
	v_pk_fma_f32 v[198:199], v[174:175], v[42:43], v[198:199] op_sel:[0,1,0] op_sel_hi:[1,1,1]
	v_pk_fma_f32 v[200:201], v[176:177], v[42:43], v[200:201] op_sel:[0,1,0] op_sel_hi:[1,1,1]
	v_pk_fma_f32 v[202:203], v[178:179], v[42:43], v[202:203] op_sel:[0,1,0] op_sel_hi:[1,1,1]
	v_pk_fma_f32 v[204:205], v[180:181], v[42:43], v[204:205] op_sel:[0,1,0] op_sel_hi:[1,1,1]
	v_pk_fma_f32 v[198:199], v[114:115], v[44:45], v[198:199] op_sel:[0,0,0] op_sel_hi:[1,0,1]
	v_pk_fma_f32 v[200:201], v[116:117], v[44:45], v[200:201] op_sel:[0,0,0] op_sel_hi:[1,0,1]
	v_pk_fma_f32 v[202:203], v[118:119], v[44:45], v[202:203] op_sel:[0,0,0] op_sel_hi:[1,0,1]
	v_pk_fma_f32 v[204:205], v[120:121], v[44:45], v[204:205] op_sel:[0,0,0] op_sel_hi:[1,0,1]
	v_pk_fma_f32 v[198:199], v[176:177], v[44:45], v[198:199] op_sel:[0,1,0] op_sel_hi:[1,1,1]
	v_pk_fma_f32 v[200:201], v[178:179], v[44:45], v[200:201] op_sel:[0,1,0] op_sel_hi:[1,1,1]
	v_pk_fma_f32 v[202:203], v[180:181], v[44:45], v[202:203] op_sel:[0,1,0] op_sel_hi:[1,1,1]
	v_pk_fma_f32 v[204:205], v[182:183], v[44:45], v[204:205] op_sel:[0,1,0] op_sel_hi:[1,1,1]
	v_pk_fma_f32 v[198:199], v[116:117], v[30:31], v[198:199] op_sel:[0,1,0] op_sel_hi:[1,1,1]
	v_pk_fma_f32 v[200:201], v[118:119], v[30:31], v[200:201] op_sel:[0,1,0] op_sel_hi:[1,1,1]
	v_pk_fma_f32 v[202:203], v[120:121], v[30:31], v[202:203] op_sel:[0,1,0] op_sel_hi:[1,1,1]
	v_pk_fma_f32 v[204:205], v[122:123], v[30:31], v[204:205] op_sel:[0,1,0] op_sel_hi:[1,1,1]
	v_pk_fma_f32 v[198:199], v[178:179], v[46:47], v[198:199] op_sel:[0,0,0] op_sel_hi:[1,0,1]
	v_pk_fma_f32 v[200:201], v[180:181], v[46:47], v[200:201] op_sel:[0,0,0] op_sel_hi:[1,0,1]
	v_pk_fma_f32 v[202:203], v[182:183], v[46:47], v[202:203] op_sel:[0,0,0] op_sel_hi:[1,0,1]
; __device__ __forceinline__ void conv_phase(LAS unsigned char* lds, int tile, int tid, const bf16* __restrict__ U, const float* __restrict__ cw, const float* __restrict__ cb, ...
;     ...
;             for (int tk = 0; tk < HT; ++tk) { float a = bias;
; #pragma unroll
;                 for (int j = 0; j < CKW; ++j) a += w[j] * uc[tk + j];
;                 obuf[tk * CH + tid] = a; }
	v_pk_fma_f32 v[204:205], v[184:185], v[46:47], v[204:205] op_sel:[0,0,0] op_sel_hi:[1,0,1]
	v_pk_fma_f32 v[198:199], v[118:119], v[46:47], v[198:199] op_sel:[0,1,0] op_sel_hi:[1,1,1]
	v_pk_fma_f32 v[200:201], v[120:121], v[46:47], v[200:201] op_sel:[0,1,0] op_sel_hi:[1,1,1]
	v_pk_fma_f32 v[202:203], v[122:123], v[46:47], v[202:203] op_sel:[0,1,0] op_sel_hi:[1,1,1]
	v_pk_fma_f32 v[204:205], v[124:125], v[46:47], v[204:205] op_sel:[0,1,0] op_sel_hi:[1,1,1]
	v_pk_fma_f32 v[198:199], v[180:181], v[48:49], v[198:199] op_sel:[0,0,0] op_sel_hi:[1,0,1]
	v_pk_fma_f32 v[200:201], v[182:183], v[48:49], v[200:201] op_sel:[0,0,0] op_sel_hi:[1,0,1]
	v_pk_fma_f32 v[202:203], v[184:185], v[48:49], v[202:203] op_sel:[0,0,0] op_sel_hi:[1,0,1]
	v_pk_fma_f32 v[204:205], v[186:187], v[48:49], v[204:205] op_sel:[0,0,0] op_sel_hi:[1,0,1]
	v_pk_fma_f32 v[198:199], v[120:121], v[48:49], v[198:199] op_sel:[0,1,0] op_sel_hi:[1,1,1]
	v_pk_fma_f32 v[200:201], v[122:123], v[48:49], v[200:201] op_sel:[0,1,0] op_sel_hi:[1,1,1]
	v_pk_fma_f32 v[202:203], v[124:125], v[48:49], v[202:203] op_sel:[0,1,0] op_sel_hi:[1,1,1]
	v_pk_fma_f32 v[204:205], v[126:127], v[48:49], v[204:205] op_sel:[0,1,0] op_sel_hi:[1,1,1]
	v_pk_fma_f32 v[198:199], v[182:183], v[50:51], v[198:199] op_sel:[0,1,0] op_sel_hi:[1,1,1]
	v_pk_fma_f32 v[200:201], v[184:185], v[50:51], v[200:201] op_sel:[0,1,0] op_sel_hi:[1,1,1]
	v_pk_fma_f32 v[202:203], v[186:187], v[50:51], v[202:203] op_sel:[0,1,0] op_sel_hi:[1,1,1]
	v_pk_fma_f32 v[204:205], v[188:189], v[50:51], v[204:205] op_sel:[0,1,0] op_sel_hi:[1,1,1]
	v_pk_fma_f32 v[198:199], v[122:123], v[52:53], v[198:199] op_sel:[0,0,0] op_sel_hi:[1,0,1]
	v_pk_fma_f32 v[200:201], v[124:125], v[52:53], v[200:201] op_sel:[0,0,0] op_sel_hi:[1,0,1]
	v_pk_fma_f32 v[202:203], v[126:127], v[52:53], v[202:203] op_sel:[0,0,0] op_sel_hi:[1,0,1]
	v_pk_fma_f32 v[204:205], v[128:129], v[52:53], v[204:205] op_sel:[0,0,0] op_sel_hi:[1,0,1]
	v_pk_fma_f32 v[198:199], v[184:185], v[52:53], v[198:199] op_sel:[0,1,0] op_sel_hi:[1,1,1]
	v_pk_fma_f32 v[200:201], v[186:187], v[52:53], v[200:201] op_sel:[0,1,0] op_sel_hi:[1,1,1]
	v_pk_fma_f32 v[202:203], v[188:189], v[52:53], v[202:203] op_sel:[0,1,0] op_sel_hi:[1,1,1]
	v_pk_fma_f32 v[204:205], v[190:191], v[52:53], v[204:205] op_sel:[0,1,0] op_sel_hi:[1,1,1]
	v_pk_fma_f32 v[198:199], v[124:125], v[50:51], v[198:199] op_sel:[0,0,0] op_sel_hi:[1,0,1]
	v_pk_fma_f32 v[200:201], v[126:127], v[50:51], v[200:201] op_sel:[0,0,0] op_sel_hi:[1,0,1]
	v_pk_fma_f32 v[202:203], v[128:129], v[50:51], v[202:203] op_sel:[0,0,0] op_sel_hi:[1,0,1]
	v_pk_fma_f32 v[204:205], v[130:131], v[50:51], v[204:205] op_sel:[0,0,0] op_sel_hi:[1,0,1]
	v_pk_fma_f32 v[198:199], v[186:187], v[54:55], v[198:199] op_sel:[0,0,0] op_sel_hi:[1,0,1]
	v_pk_fma_f32 v[200:201], v[188:189], v[54:55], v[200:201] op_sel:[0,0,0] op_sel_hi:[1,0,1]
	v_pk_fma_f32 v[202:203], v[190:191], v[54:55], v[202:203] op_sel:[0,0,0] op_sel_hi:[1,0,1]
	v_pk_fma_f32 v[204:205], v[192:193], v[54:55], v[204:205] op_sel:[0,0,0] op_sel_hi:[1,0,1]
	v_pk_fma_f32 v[198:199], v[126:127], v[54:55], v[198:199] op_sel:[0,1,0] op_sel_hi:[1,1,1]
	v_pk_fma_f32 v[200:201], v[128:129], v[54:55], v[200:201] op_sel:[0,1,0] op_sel_hi:[1,1,1]
	v_pk_fma_f32 v[202:203], v[130:131], v[54:55], v[202:203] op_sel:[0,1,0] op_sel_hi:[1,1,1]
	v_pk_fma_f32 v[204:205], v[132:133], v[54:55], v[204:205] op_sel:[0,1,0] op_sel_hi:[1,1,1]
	ds_write2st64_b32 v64, v198, v199 offset0:192 offset1:200
	ds_write2st64_b32 v64, v200, v201 offset0:208 offset1:216
	ds_write2st64_b32 v64, v202, v203 offset0:224 offset1:232
	ds_write2st64_b32 v64, v204, v205 offset0:240 offset1:248
	v_add_u32_e32 v14, s21, v66
	v_ashrrev_i32_e32 v15, 31, v14
	v_lshlrev_b64 v[14:15], 11, v[14:15]
	s_xor_b64 s[10:11], s[6:7], -1
	v_lshl_add_u64 v[14:15], v[10:11], 0, v[14:15]
	s_mov_b32 s12, 0
	s_waitcnt lgkmcnt(0)
	s_barrier
